# v010 + code placement: every 32-MFMA block of the 8 GEMM K-loops padded onto an 8-byte boundary (19 s_nop 0 in load segments)
# baseline (speedup 1.0000x reference)
; #define PG8_LAS __attribute__((address_space(3)))
; #define PG8_STAGE_A(bufoff, h, ptr, nsel) do { if constexpr (Sched::GATHER) { if (nsel) PG8_STAGE_X(bufoff, ptr, vAn[h], PG8_A_AUX); else PG8_STAGE_X(bufoff, ptr, vAc[h], PG8_A_AUX); } \
;         else PG8_STAGE_X(bufoff, (ptr) + (h) * hstep, voffA, PG8_A_AUX); } while (0)
; #define PG8_STAGE(bufoff, gbase, voff) PG8_STAGE_X(bufoff, gbase, voff, PG8_B_AUX)
; #define PG8_LDA(dst, b, h) do { _Pragma("unroll") for (int m = 0; m < 4; ++m) _Pragma("unroll") for (int k = 0; k < 2; ++k) dst[m][k] = *(const PG8_LAS bf16x8*)(lds + PG8_SA(b, h) + aoff + m * 2048 + k * 1024); } while (0)
; #define PG8_LDB(dst, b, h) do { _Pragma("unroll") for (int n = 0; n < 2; ++n) _Pragma("unroll") for (int k = 0; k < 2; ++k) dst[n][k] = *(const PG8_LAS bf16x8*)(lds + PG8_SB(b, h) + boff + n * 2048 + k * 1024); } while (0)
; #define PG8_WAIT_V(n) asm volatile("s_waitcnt vmcnt(" #n ")" ::: "memory")
; #define PG8_WAIT_L(n) asm volatile("s_waitcnt lgkmcnt(" #n ")" ::: "memory")
; #define PG8_BAR __builtin_amdgcn_s_barrier()
; #define PG8_SCHED __builtin_amdgcn_sched_barrier(0)
; template <class Epi, class Sched, bool ALIGN_EPI = false, bool SP2 = false>
; __device__ __forceinline__ void gemm_phase(PG8_LAS unsigned char* lds, const Gemm g, const Sched& S, const Epi& E) {
;     ...
;             const char* a2 = last ? nA : cA + (size_t)(t + 2) * kstep; const char* b2 = last ? nB : cB + (size_t)(t + 2) * kstep;
;             const char* a3 = a2 + kstep; const char* b3 = b2 + kstep;
;             if (last && has_next) S.a_ready(nxt);
;             if constexpr (Sched::GATHER) { if (last) { const u32x4 pv_ = *(const PG8_LAS u32x4*)(lds + STAGE_BYTES + tid * 16); vAn[0][0] = pv_.x; vAn[0][1] = pv_.y; vAn[1][0] = pv_.z; vAn[1][1] = pv_.w; } }
;             if constexpr (SP2) {
;             PG8_LDB(B0, 0, 0); PG8_LDB(B1, 0, 1); PG8_SCHED; PG8_LDA(At, 0, 0); PG8_STAGE_A(PG8_SA(1, 1), 1, a1, false);
;             PG8_WAIT_V(8); PG8_WAIT_L(0); PG8_BAR; PG8_MMA(0, 0, At, B0); PG8_MMA(0, 1, At, B1); PG8_BAR; PG8_SCHED;
;             PG8_LDA(At, 0, 1); PG8_STAGE(PG8_SB(0, 0), b2, voffB); PG8_STAGE(PG8_SB(0, 1), b2 + hstep, voffB); PG8_STAGE_A(PG8_SA(0, 0), 0, a2, last);
;             PG8_WAIT_V(8); PG8_WAIT_L(0); PG8_BAR; PG8_MMA(1, 0, At, B0); PG8_MMA(1, 1, At, B1); PG8_BAR; PG8_SCHED;
.LBB13_241:
	v_add_u32_e32 v160, s37, v99
	v_add_u32_e32 v173, s39, v99
	ds_read_b128 v[132:135], v160
	ds_read_b128 v[136:139], v160 offset:1024
	ds_read_b128 v[156:159], v160 offset:2048
	ds_read_b128 v[160:163], v160 offset:3072
	ds_read_b128 v[164:167], v173
	ds_read_b128 v[174:177], v173 offset:1024
	ds_read_b128 v[178:181], v173 offset:2048
	ds_read_b128 v[182:185], v173 offset:3072
	s_add_u32 s24, s12, 0xfffc0080
	s_addc_u32 s25, s13, -1
	s_cmp_eq_u32 s38, 12
	s_cselect_b32 s27, s2, s25
	s_cselect_b32 s26, s3, s24
	s_cselect_b32 s25, s9, s19
	s_cselect_b32 s24, s11, s17
	v_lshl_add_u64 v[198:199], s[12:13], 0, v[152:153]
	s_add_i32 m0, s47, 0xc000
	ds_read_b128 v[186:189], v172
	ds_read_b128 v[190:193], v172 offset:1024
	ds_read_b128 v[194:197], v172 offset:2048
	ds_read_b128 v[208:211], v172 offset:3072
	ds_read_b128 v[212:215], v172 offset:4096
	ds_read_b128 v[216:219], v172 offset:5120
	ds_read_b128 v[220:223], v172 offset:6144
	ds_read_b128 v[224:227], v172 offset:7168
	global_load_lds_dwordx4 v[198:199], off
	v_lshl_add_u64 v[198:199], s[12:13], 0, v[154:155]
	s_add_i32 m0, s47, 0xe000
	s_nop 0
	global_load_lds_dwordx4 v[198:199], off
	s_nop 0
	s_waitcnt vmcnt(8)
	s_waitcnt lgkmcnt(0)
	s_barrier
	s_setprio 1
	s_waitcnt lgkmcnt(0)
	v_mfma_f32_16x16x32_bf16 v[128:131], v[132:135], v[186:189], v[128:131]
	v_mfma_f32_16x16x32_bf16 v[124:127], v[156:159], v[186:189], v[124:127]
	v_mfma_f32_16x16x32_bf16 v[112:115], v[132:135], v[194:197], v[112:115]
	v_mfma_f32_16x16x32_bf16 v[108:111], v[156:159], v[194:197], v[108:111]
	v_mfma_f32_16x16x32_bf16 v[94:97], v[132:135], v[212:215], v[94:97]
	v_mfma_f32_16x16x32_bf16 v[90:93], v[156:159], v[212:215], v[90:93]
	v_mfma_f32_16x16x32_bf16 v[78:81], v[132:135], v[220:223], v[78:81]
	v_mfma_f32_16x16x32_bf16 v[74:77], v[156:159], v[220:223], v[74:77]
	v_mfma_f32_16x16x32_bf16 v[128:131], v[136:139], v[190:193], v[128:131]
	v_mfma_f32_16x16x32_bf16 v[124:127], v[160:163], v[190:193], v[124:127]
	v_mfma_f32_16x16x32_bf16 v[112:115], v[136:139], v[208:211], v[112:115]
	v_mfma_f32_16x16x32_bf16 v[108:111], v[160:163], v[208:211], v[108:111]
	v_mfma_f32_16x16x32_bf16 v[94:97], v[136:139], v[216:219], v[94:97]
	v_mfma_f32_16x16x32_bf16 v[90:93], v[160:163], v[216:219], v[90:93]
	v_mfma_f32_16x16x32_bf16 v[78:81], v[136:139], v[224:227], v[78:81]
	v_mfma_f32_16x16x32_bf16 v[74:77], v[160:163], v[224:227], v[74:77]
	s_setprio 0
	s_setprio 1
	v_mfma_f32_16x16x32_bf16 v[120:123], v[164:167], v[186:189], v[120:123]
	v_mfma_f32_16x16x32_bf16 v[116:119], v[178:181], v[186:189], v[116:119]
	v_mfma_f32_16x16x32_bf16 v[104:107], v[164:167], v[194:197], v[104:107]
	v_mfma_f32_16x16x32_bf16 v[100:103], v[178:181], v[194:197], v[100:103]
	v_mfma_f32_16x16x32_bf16 v[86:89], v[164:167], v[212:215], v[86:89]
	v_mfma_f32_16x16x32_bf16 v[82:85], v[178:181], v[212:215], v[82:85]
	v_mfma_f32_16x16x32_bf16 v[70:73], v[164:167], v[220:223], v[70:73]
	v_mfma_f32_16x16x32_bf16 v[66:69], v[178:181], v[220:223], v[66:69]
	v_mfma_f32_16x16x32_bf16 v[120:123], v[174:177], v[190:193], v[120:123]
	v_mfma_f32_16x16x32_bf16 v[116:119], v[182:185], v[190:193], v[116:119]
	v_mfma_f32_16x16x32_bf16 v[104:107], v[174:177], v[208:211], v[104:107]
	v_mfma_f32_16x16x32_bf16 v[100:103], v[182:185], v[208:211], v[100:103]
	v_mfma_f32_16x16x32_bf16 v[86:89], v[174:177], v[216:219], v[86:89]
	v_mfma_f32_16x16x32_bf16 v[82:85], v[182:185], v[216:219], v[82:85]
	v_mfma_f32_16x16x32_bf16 v[70:73], v[174:177], v[224:227], v[70:73]
	v_mfma_f32_16x16x32_bf16 v[66:69], v[182:185], v[224:227], v[66:69]
	s_setprio 0
	s_barrier
	s_add_i32 s48, s37, s40
	v_lshl_add_u64 v[198:199], s[24:25], 0, v[142:143]
	s_mov_b32 m0, s48
	ds_read_b128 v[186:189], v172 offset:16384
	ds_read_b128 v[190:193], v172 offset:17408
	ds_read_b128 v[194:197], v172 offset:18432
	ds_read_b128 v[208:211], v172 offset:19456
	ds_read_b128 v[212:215], v172 offset:20480
	ds_read_b128 v[216:219], v172 offset:21504
	ds_read_b128 v[220:223], v172 offset:22528
	ds_read_b128 v[224:227], v172 offset:23552
	global_load_lds_dwordx4 v[198:199], off
	s_add_i32 m0, s48, 0x2000
	s_add_u32 s48, s24, 0x40000
	v_lshl_add_u64 v[228:229], s[24:25], 0, v[146:147]
	s_addc_u32 s49, s25, 0
	s_add_i32 s52, s39, s40
	global_load_lds_dwordx4 v[228:229], off
	v_lshl_add_u64 v[230:231], s[48:49], 0, v[142:143]
	s_mov_b32 m0, s52
	v_lshl_add_u64 v[232:233], s[26:27], 0, v[144:145]
	global_load_lds_dwordx4 v[230:231], off
	v_lshl_add_u64 v[230:231], s[48:49], 0, v[146:147]
	s_add_i32 m0, s52, 0x2000
	s_nop 0
	global_load_lds_dwordx4 v[230:231], off
	v_lshl_add_u64 v[230:231], s[26:27], 0, v[140:141]
	s_mov_b32 m0, s47
	s_nop 0
	global_load_lds_dwordx4 v[230:231], off
	s_add_i32 m0, s47, 0x2000
	s_nop 0
	global_load_lds_dwordx4 v[232:233], off
	s_waitcnt vmcnt(8)
	s_waitcnt lgkmcnt(0)
	s_barrier
; #define PG8_STAGE_A(bufoff, h, ptr, nsel) do { if constexpr (Sched::GATHER) { if (nsel) PG8_STAGE_X(bufoff, ptr, vAn[h], PG8_A_AUX); else PG8_STAGE_X(bufoff, ptr, vAc[h], PG8_A_AUX); } \
;         else PG8_STAGE_X(bufoff, (ptr) + (h) * hstep, voffA, PG8_A_AUX); } while (0)
; #define PG8_STAGE(bufoff, gbase, voff) PG8_STAGE_X(bufoff, gbase, voff, PG8_B_AUX)
; #define PG8_LDA(dst, b, h) do { _Pragma("unroll") for (int m = 0; m < 4; ++m) _Pragma("unroll") for (int k = 0; k < 2; ++k) dst[m][k] = *(const PG8_LAS bf16x8*)(lds + PG8_SA(b, h) + aoff + m * 2048 + k * 1024); } while (0)
; #define PG8_LDB(dst, b, h) do { _Pragma("unroll") for (int n = 0; n < 2; ++n) _Pragma("unroll") for (int k = 0; k < 2; ++k) dst[n][k] = *(const PG8_LAS bf16x8*)(lds + PG8_SB(b, h) + boff + n * 2048 + k * 1024); } while (0)
; #define PG8_MMA(ai, bj, At, Bt) do { __builtin_amdgcn_s_setprio(1); _Pragma("unroll") for (int m = 0; m < 4; ++m) _Pragma("unroll") for (int n = 0; n < 2; ++n) _Pragma("unroll") for (int k = 0; k < 2; ++k) \
;         acc[ai][bj][m][n] = __builtin_amdgcn_mfma_f32_16x16x32_bf16(Bt[n][k], At[m][k], acc[ai][bj][m][n], 0, 0, 0); __builtin_amdgcn_s_setprio(0); } while (0)
; #define PG8_WAIT_V(n) asm volatile("s_waitcnt vmcnt(" #n ")" ::: "memory")
; #define PG8_WAIT_L(n) asm volatile("s_waitcnt lgkmcnt(" #n ")" ::: "memory")
; #define PG8_BAR __builtin_amdgcn_s_barrier()
; #define PG8_SCHED __builtin_amdgcn_sched_barrier(0)
; template <class Epi, class Sched, bool ALIGN_EPI = false, bool SP2 = false>
; __device__ __forceinline__ void gemm_phase(PG8_LAS unsigned char* lds, const Gemm g, const Sched& S, const Epi& E) {
;     ...
;             PG8_WAIT_V(8); PG8_WAIT_L(0); PG8_BAR; PG8_MMA(1, 0, At, B0); PG8_MMA(1, 1, At, B1); PG8_BAR; PG8_SCHED;
;             PG8_LDB(B0, 1, 0); PG8_LDB(B1, 1, 1); PG8_SCHED; PG8_LDA(At, 1, 0); PG8_STAGE_A(PG8_SA(0, 1), 1, a2, last);
;             PG8_WAIT_V(8); PG8_WAIT_L(0); PG8_BAR; PG8_MMA(0, 0, At, B0); PG8_MMA(0, 1, At, B1); PG8_BAR; PG8_SCHED;
;             PG8_LDA(At, 1, 1); PG8_STAGE(PG8_SB(1, 0), b3, voffB); PG8_STAGE(PG8_SB(1, 1), b3 + hstep, voffB); PG8_STAGE_A(PG8_SA(1, 0), 0, a3, last);
	s_setprio 1
	s_waitcnt lgkmcnt(0)
	v_mfma_f32_16x16x32_bf16 v[62:65], v[132:135], v[186:189], v[62:65]
	v_mfma_f32_16x16x32_bf16 v[58:61], v[156:159], v[186:189], v[58:61]
	v_mfma_f32_16x16x32_bf16 v[46:49], v[132:135], v[194:197], v[46:49]
	v_mfma_f32_16x16x32_bf16 v[42:45], v[156:159], v[194:197], v[42:45]
	v_mfma_f32_16x16x32_bf16 v[30:33], v[132:135], v[212:215], v[30:33]
	v_mfma_f32_16x16x32_bf16 v[26:29], v[156:159], v[212:215], v[26:29]
	v_mfma_f32_16x16x32_bf16 v[14:17], v[132:135], v[220:223], v[14:17]
	v_mfma_f32_16x16x32_bf16 v[10:13], v[156:159], v[220:223], v[10:13]
	v_mfma_f32_16x16x32_bf16 v[62:65], v[136:139], v[190:193], v[62:65]
	v_mfma_f32_16x16x32_bf16 v[58:61], v[160:163], v[190:193], v[58:61]
	v_mfma_f32_16x16x32_bf16 v[46:49], v[136:139], v[208:211], v[46:49]
	v_mfma_f32_16x16x32_bf16 v[42:45], v[160:163], v[208:211], v[42:45]
	v_mfma_f32_16x16x32_bf16 v[30:33], v[136:139], v[216:219], v[30:33]
	v_mfma_f32_16x16x32_bf16 v[26:29], v[160:163], v[216:219], v[26:29]
	v_mfma_f32_16x16x32_bf16 v[14:17], v[136:139], v[224:227], v[14:17]
	v_mfma_f32_16x16x32_bf16 v[10:13], v[160:163], v[224:227], v[10:13]
	s_setprio 0
	s_setprio 1
	v_mfma_f32_16x16x32_bf16 v[54:57], v[164:167], v[186:189], v[54:57]
	v_mfma_f32_16x16x32_bf16 v[50:53], v[178:181], v[186:189], v[50:53]
	v_mfma_f32_16x16x32_bf16 v[38:41], v[164:167], v[194:197], v[38:41]
	v_mfma_f32_16x16x32_bf16 v[34:37], v[178:181], v[194:197], v[34:37]
	v_mfma_f32_16x16x32_bf16 v[22:25], v[164:167], v[212:215], v[22:25]
	v_mfma_f32_16x16x32_bf16 v[18:21], v[178:181], v[212:215], v[18:21]
	v_mfma_f32_16x16x32_bf16 v[6:9], v[164:167], v[220:223], v[6:9]
	v_mfma_f32_16x16x32_bf16 v[2:5], v[178:181], v[220:223], v[2:5]
	v_mfma_f32_16x16x32_bf16 v[54:57], v[174:177], v[190:193], v[54:57]
	v_mfma_f32_16x16x32_bf16 v[50:53], v[182:185], v[190:193], v[50:53]
	v_mfma_f32_16x16x32_bf16 v[38:41], v[174:177], v[208:211], v[38:41]
	v_mfma_f32_16x16x32_bf16 v[34:37], v[182:185], v[208:211], v[34:37]
	v_mfma_f32_16x16x32_bf16 v[22:25], v[174:177], v[216:219], v[22:25]
	v_mfma_f32_16x16x32_bf16 v[18:21], v[182:185], v[216:219], v[18:21]
	v_mfma_f32_16x16x32_bf16 v[6:9], v[174:177], v[224:227], v[6:9]
	v_mfma_f32_16x16x32_bf16 v[2:5], v[182:185], v[224:227], v[2:5]
	s_setprio 0
	s_barrier
	v_add_u32_e32 v160, s41, v99
	v_add_u32_e32 v173, s42, v99
	ds_read_b128 v[132:135], v160
	ds_read_b128 v[136:139], v160 offset:1024
	ds_read_b128 v[156:159], v160 offset:2048
	ds_read_b128 v[160:163], v160 offset:3072
	ds_read_b128 v[164:167], v173
	ds_read_b128 v[174:177], v173 offset:1024
	ds_read_b128 v[178:181], v173 offset:2048
	ds_read_b128 v[182:185], v173 offset:3072
	s_add_u32 s26, s26, 0x40000
	s_addc_u32 s27, s27, 0
	v_lshl_add_u64 v[242:243], s[26:27], 0, v[140:141]
	s_add_i32 m0, s47, 0x4000
	ds_read_b128 v[186:189], v172 offset:32768
	ds_read_b128 v[190:193], v172 offset:33792
	ds_read_b128 v[194:197], v172 offset:34816
	ds_read_b128 v[208:211], v172 offset:35840
	ds_read_b128 v[212:215], v172 offset:36864
	ds_read_b128 v[216:219], v172 offset:37888
	ds_read_b128 v[220:223], v172 offset:38912
	ds_read_b128 v[224:227], v172 offset:39936
	global_load_lds_dwordx4 v[242:243], off
	v_lshl_add_u64 v[242:243], s[26:27], 0, v[144:145]
	s_add_i32 m0, s47, 0x6000
	s_nop 0
	global_load_lds_dwordx4 v[242:243], off
	s_nop 0
	s_waitcnt vmcnt(8)
	s_waitcnt lgkmcnt(0)
	s_barrier
	s_setprio 1
	s_waitcnt lgkmcnt(0)
	v_mfma_f32_16x16x32_bf16 v[128:131], v[132:135], v[186:189], v[128:131]
	v_mfma_f32_16x16x32_bf16 v[124:127], v[156:159], v[186:189], v[124:127]
	v_mfma_f32_16x16x32_bf16 v[112:115], v[132:135], v[194:197], v[112:115]
	v_mfma_f32_16x16x32_bf16 v[108:111], v[156:159], v[194:197], v[108:111]
	v_mfma_f32_16x16x32_bf16 v[94:97], v[132:135], v[212:215], v[94:97]
	v_mfma_f32_16x16x32_bf16 v[90:93], v[156:159], v[212:215], v[90:93]
	v_mfma_f32_16x16x32_bf16 v[78:81], v[132:135], v[220:223], v[78:81]
	v_mfma_f32_16x16x32_bf16 v[74:77], v[156:159], v[220:223], v[74:77]
	v_mfma_f32_16x16x32_bf16 v[128:131], v[136:139], v[190:193], v[128:131]
	v_mfma_f32_16x16x32_bf16 v[124:127], v[160:163], v[190:193], v[124:127]
	v_mfma_f32_16x16x32_bf16 v[112:115], v[136:139], v[208:211], v[112:115]
	v_mfma_f32_16x16x32_bf16 v[108:111], v[160:163], v[208:211], v[108:111]
	v_mfma_f32_16x16x32_bf16 v[94:97], v[136:139], v[216:219], v[94:97]
	v_mfma_f32_16x16x32_bf16 v[90:93], v[160:163], v[216:219], v[90:93]
	v_mfma_f32_16x16x32_bf16 v[78:81], v[136:139], v[224:227], v[78:81]
	v_mfma_f32_16x16x32_bf16 v[74:77], v[160:163], v[224:227], v[74:77]
	s_setprio 0
	s_setprio 1
	v_mfma_f32_16x16x32_bf16 v[120:123], v[164:167], v[186:189], v[120:123]
	v_mfma_f32_16x16x32_bf16 v[116:119], v[178:181], v[186:189], v[116:119]
	v_mfma_f32_16x16x32_bf16 v[104:107], v[164:167], v[194:197], v[104:107]
	v_mfma_f32_16x16x32_bf16 v[100:103], v[178:181], v[194:197], v[100:103]
	v_mfma_f32_16x16x32_bf16 v[86:89], v[164:167], v[212:215], v[86:89]
	v_mfma_f32_16x16x32_bf16 v[82:85], v[178:181], v[212:215], v[82:85]
	v_mfma_f32_16x16x32_bf16 v[70:73], v[164:167], v[220:223], v[70:73]
	v_mfma_f32_16x16x32_bf16 v[66:69], v[178:181], v[220:223], v[66:69]
	v_mfma_f32_16x16x32_bf16 v[120:123], v[174:177], v[190:193], v[120:123]
	v_mfma_f32_16x16x32_bf16 v[116:119], v[182:185], v[190:193], v[116:119]
	v_mfma_f32_16x16x32_bf16 v[104:107], v[174:177], v[208:211], v[104:107]
	v_mfma_f32_16x16x32_bf16 v[100:103], v[182:185], v[208:211], v[100:103]
	v_mfma_f32_16x16x32_bf16 v[86:89], v[174:177], v[216:219], v[86:89]
	v_mfma_f32_16x16x32_bf16 v[82:85], v[182:185], v[216:219], v[82:85]
	v_mfma_f32_16x16x32_bf16 v[70:73], v[174:177], v[224:227], v[70:73]
	v_mfma_f32_16x16x32_bf16 v[66:69], v[182:185], v[224:227], v[66:69]
	s_setprio 0
	s_barrier
; #define PG8_STAGE_A(bufoff, h, ptr, nsel) do { if constexpr (Sched::GATHER) { if (nsel) PG8_STAGE_X(bufoff, ptr, vAn[h], PG8_A_AUX); else PG8_STAGE_X(bufoff, ptr, vAc[h], PG8_A_AUX); } \
;         else PG8_STAGE_X(bufoff, (ptr) + (h) * hstep, voffA, PG8_A_AUX); } while (0)
; #define PG8_STAGE(bufoff, gbase, voff) PG8_STAGE_X(bufoff, gbase, voff, PG8_B_AUX)
; #define PG8_LDA(dst, b, h) do { _Pragma("unroll") for (int m = 0; m < 4; ++m) _Pragma("unroll") for (int k = 0; k < 2; ++k) dst[m][k] = *(const PG8_LAS bf16x8*)(lds + PG8_SA(b, h) + aoff + m * 2048 + k * 1024); } while (0)
; #define PG8_MMA(ai, bj, At, Bt) do { __builtin_amdgcn_s_setprio(1); _Pragma("unroll") for (int m = 0; m < 4; ++m) _Pragma("unroll") for (int n = 0; n < 2; ++n) _Pragma("unroll") for (int k = 0; k < 2; ++k) \
;         acc[ai][bj][m][n] = __builtin_amdgcn_mfma_f32_16x16x32_bf16(Bt[n][k], At[m][k], acc[ai][bj][m][n], 0, 0, 0); __builtin_amdgcn_s_setprio(0); } while (0)
; #define PG8_WAIT_V(n) asm volatile("s_waitcnt vmcnt(" #n ")" ::: "memory")
; #define PG8_WAIT_L(n) asm volatile("s_waitcnt lgkmcnt(" #n ")" ::: "memory")
; #define PG8_BAR __builtin_amdgcn_s_barrier()
; #define PG8_SCHED __builtin_amdgcn_sched_barrier(0)
; template <class Epi, class Sched, bool ALIGN_EPI = false, bool SP2 = false>
; __device__ __forceinline__ void gemm_phase(PG8_LAS unsigned char* lds, const Gemm g, const Sched& S, const Epi& E) {
;     ...
;             PG8_LDA(At, 1, 1); PG8_STAGE(PG8_SB(1, 0), b3, voffB); PG8_STAGE(PG8_SB(1, 1), b3 + hstep, voffB); PG8_STAGE_A(PG8_SA(1, 0), 0, a3, last);
;             PG8_WAIT_V(8); PG8_WAIT_L(0); PG8_BAR; PG8_MMA(1, 0, At, B0); PG8_MMA(1, 1, At, B1); PG8_BAR; PG8_SCHED;
;     ...
;         }
;         if constexpr (ALIGN_EPI) { if (wr == 0) PG8_BAR; }
	s_mov_b32 m0, s45
	v_lshl_add_u64 v[198:199], v[198:199], 0, s[54:55]
	s_add_u32 s24, s24, 0x40080
	ds_read_b128 v[186:189], v172 offset:49152
	ds_read_b128 v[190:193], v172 offset:50176
	ds_read_b128 v[194:197], v172 offset:51200
	ds_read_b128 v[208:211], v172 offset:52224
	ds_read_b128 v[212:215], v172 offset:53248
	ds_read_b128 v[216:219], v172 offset:54272
	ds_read_b128 v[220:223], v172 offset:55296
	ds_read_b128 v[224:227], v172 offset:56320
	global_load_lds_dwordx4 v[198:199], off
	v_lshl_add_u64 v[198:199], v[228:229], 0, s[54:55]
	s_mov_b32 m0, s46
	s_addc_u32 s25, s25, 0
	global_load_lds_dwordx4 v[198:199], off
	v_lshl_add_u64 v[198:199], s[24:25], 0, v[142:143]
	s_mov_b32 m0, s56
	s_nop 0
	global_load_lds_dwordx4 v[198:199], off
	v_lshl_add_u64 v[198:199], s[24:25], 0, v[146:147]
	s_mov_b32 m0, s57
	s_nop 0
	global_load_lds_dwordx4 v[198:199], off
	v_lshl_add_u64 v[198:199], v[230:231], 0, s[54:55]
	s_mov_b32 m0, s50
	s_nop 0
	global_load_lds_dwordx4 v[198:199], off
	v_lshl_add_u64 v[198:199], v[232:233], 0, s[54:55]
	s_mov_b32 m0, s51
	s_nop 0
	global_load_lds_dwordx4 v[198:199], off
	s_waitcnt vmcnt(8)
	s_waitcnt lgkmcnt(0)
	s_barrier
	s_setprio 1
	s_waitcnt lgkmcnt(0)
	v_mfma_f32_16x16x32_bf16 v[62:65], v[132:135], v[186:189], v[62:65]
	v_mfma_f32_16x16x32_bf16 v[58:61], v[156:159], v[186:189], v[58:61]
	v_mfma_f32_16x16x32_bf16 v[46:49], v[132:135], v[194:197], v[46:49]
	v_mfma_f32_16x16x32_bf16 v[42:45], v[156:159], v[194:197], v[42:45]
	v_mfma_f32_16x16x32_bf16 v[30:33], v[132:135], v[212:215], v[30:33]
	v_mfma_f32_16x16x32_bf16 v[26:29], v[156:159], v[212:215], v[26:29]
	v_mfma_f32_16x16x32_bf16 v[14:17], v[132:135], v[220:223], v[14:17]
	v_mfma_f32_16x16x32_bf16 v[10:13], v[156:159], v[220:223], v[10:13]
	v_mfma_f32_16x16x32_bf16 v[62:65], v[136:139], v[190:193], v[62:65]
	v_mfma_f32_16x16x32_bf16 v[58:61], v[160:163], v[190:193], v[58:61]
	v_mfma_f32_16x16x32_bf16 v[46:49], v[136:139], v[208:211], v[46:49]
	v_mfma_f32_16x16x32_bf16 v[42:45], v[160:163], v[208:211], v[42:45]
	v_mfma_f32_16x16x32_bf16 v[30:33], v[136:139], v[216:219], v[30:33]
	v_mfma_f32_16x16x32_bf16 v[26:29], v[160:163], v[216:219], v[26:29]
	v_mfma_f32_16x16x32_bf16 v[14:17], v[136:139], v[224:227], v[14:17]
	v_mfma_f32_16x16x32_bf16 v[10:13], v[160:163], v[224:227], v[10:13]
	s_setprio 0
	s_setprio 1
	v_mfma_f32_16x16x32_bf16 v[54:57], v[164:167], v[186:189], v[54:57]
	v_mfma_f32_16x16x32_bf16 v[50:53], v[178:181], v[186:189], v[50:53]
	v_mfma_f32_16x16x32_bf16 v[38:41], v[164:167], v[194:197], v[38:41]
	v_mfma_f32_16x16x32_bf16 v[34:37], v[178:181], v[194:197], v[34:37]
	v_mfma_f32_16x16x32_bf16 v[22:25], v[164:167], v[212:215], v[22:25]
	v_mfma_f32_16x16x32_bf16 v[18:21], v[178:181], v[212:215], v[18:21]
	v_mfma_f32_16x16x32_bf16 v[6:9], v[164:167], v[220:223], v[6:9]
	v_mfma_f32_16x16x32_bf16 v[2:5], v[178:181], v[220:223], v[2:5]
	v_mfma_f32_16x16x32_bf16 v[54:57], v[174:177], v[190:193], v[54:57]
	v_mfma_f32_16x16x32_bf16 v[50:53], v[182:185], v[190:193], v[50:53]
	v_mfma_f32_16x16x32_bf16 v[38:41], v[174:177], v[208:211], v[38:41]
	v_mfma_f32_16x16x32_bf16 v[34:37], v[182:185], v[208:211], v[34:37]
	v_mfma_f32_16x16x32_bf16 v[22:25], v[174:177], v[216:219], v[22:25]
	v_mfma_f32_16x16x32_bf16 v[18:21], v[182:185], v[216:219], v[18:21]
	v_mfma_f32_16x16x32_bf16 v[6:9], v[174:177], v[224:227], v[6:9]
	v_mfma_f32_16x16x32_bf16 v[2:5], v[182:185], v[224:227], v[2:5]
	s_setprio 0
	s_barrier
	s_add_i32 s38, s38, 2
	s_add_u32 s12, s12, 0x100
	s_addc_u32 s13, s13, 0
	s_add_u32 s17, s17, 0x100
	s_addc_u32 s19, s19, 0
	s_cmp_gt_u32 s38, 13
	s_cbranch_scc0 .LBB13_241
	s_and_b64 vcc, exec, s[14:15]
	s_cbranch_vccz .LBB13_244
	s_barrier

; #define PG8_LAS __attribute__((address_space(3)))
; #define PG8_STAGE_A(bufoff, h, ptr, nsel) do { if constexpr (Sched::GATHER) { if (nsel) PG8_STAGE_X(bufoff, ptr, vAn[h], PG8_A_AUX); else PG8_STAGE_X(bufoff, ptr, vAc[h], PG8_A_AUX); } \
;         else PG8_STAGE_X(bufoff, (ptr) + (h) * hstep, voffA, PG8_A_AUX); } while (0)
; #define PG8_STAGE(bufoff, gbase, voff) PG8_STAGE_X(bufoff, gbase, voff, PG8_B_AUX)
; #define PG8_LDA(dst, b, h) do { _Pragma("unroll") for (int m = 0; m < 4; ++m) _Pragma("unroll") for (int k = 0; k < 2; ++k) dst[m][k] = *(const PG8_LAS bf16x8*)(lds + PG8_SA(b, h) + aoff + m * 2048 + k * 1024); } while (0)
; #define PG8_LDB(dst, b, h) do { _Pragma("unroll") for (int n = 0; n < 2; ++n) _Pragma("unroll") for (int k = 0; k < 2; ++k) dst[n][k] = *(const PG8_LAS bf16x8*)(lds + PG8_SB(b, h) + boff + n * 2048 + k * 1024); } while (0)
; #define PG8_WAIT_V(n) asm volatile("s_waitcnt vmcnt(" #n ")" ::: "memory")
; #define PG8_WAIT_L(n) asm volatile("s_waitcnt lgkmcnt(" #n ")" ::: "memory")
; #define PG8_BAR __builtin_amdgcn_s_barrier()
; #define PG8_SCHED __builtin_amdgcn_sched_barrier(0)
; template <class Epi, class Sched, bool ALIGN_EPI = false, bool SP2 = false>
; __device__ __forceinline__ void gemm_phase(PG8_LAS unsigned char* lds, const Gemm g, const Sched& S, const Epi& E) {
;     ...
;             const char* a2 = last ? nA : cA + (size_t)(t + 2) * kstep; const char* b2 = last ? nB : cB + (size_t)(t + 2) * kstep;
;             const char* a3 = a2 + kstep; const char* b3 = b2 + kstep;
;             if (last && has_next) S.a_ready(nxt);
;             if constexpr (Sched::GATHER) { if (last) { const u32x4 pv_ = *(const PG8_LAS u32x4*)(lds + STAGE_BYTES + tid * 16); vAn[0][0] = pv_.x; vAn[0][1] = pv_.y; vAn[1][0] = pv_.z; vAn[1][1] = pv_.w; } }
;             if constexpr (SP2) {
;             PG8_LDB(B0, 0, 0); PG8_LDB(B1, 0, 1); PG8_SCHED; PG8_LDA(At, 0, 0); PG8_STAGE_A(PG8_SA(1, 1), 1, a1, false);
;             PG8_WAIT_V(8); PG8_WAIT_L(0); PG8_BAR; PG8_MMA(0, 0, At, B0); PG8_MMA(0, 1, At, B1); PG8_BAR; PG8_SCHED;
;             PG8_LDA(At, 0, 1); PG8_STAGE(PG8_SB(0, 0), b2, voffB); PG8_STAGE(PG8_SB(0, 1), b2 + hstep, voffB); PG8_STAGE_A(PG8_SA(0, 0), 0, a2, last);
;             PG8_WAIT_V(8); PG8_WAIT_L(0); PG8_BAR; PG8_MMA(1, 0, At, B0); PG8_MMA(1, 1, At, B1); PG8_BAR; PG8_SCHED;
.LBB13_822:
	v_add_u32_e32 v155, s46, v152
	ds_read_b128 v[148:151], v155
	ds_read_b128 v[156:159], v155 offset:1024
	ds_read_b128 v[160:163], v155 offset:2048
	ds_read_b128 v[164:167], v155 offset:3072
	v_add_u32_e32 v155, s47, v152
	ds_read_b128 v[168:171], v155
	ds_read_b128 v[172:175], v155 offset:1024
	ds_read_b128 v[176:179], v155 offset:2048
	ds_read_b128 v[180:183], v155 offset:3072
	s_add_u32 s26, s24, 0xfffc0080
	s_addc_u32 s27, s25, -1
	s_cmp_eq_u32 s73, 12
	s_cselect_b32 s29, s17, s27
	s_cselect_b32 s28, s52, s26
	s_cselect_b32 s27, s13, s72
	s_cselect_b32 s26, s60, s64
	v_lshl_add_u64 v[224:225], s[24:25], 0, v[144:145]
	s_add_i32 m0, s58, 0xc000
	ds_read_b128 v[184:187], v154
	ds_read_b128 v[188:191], v154 offset:1024
	ds_read_b128 v[192:195], v154 offset:2048
	ds_read_b128 v[196:199], v154 offset:3072
	ds_read_b128 v[208:211], v154 offset:4096
	ds_read_b128 v[212:215], v154 offset:5120
	ds_read_b128 v[216:219], v154 offset:6144
	ds_read_b128 v[220:223], v154 offset:7168
	global_load_lds_dwordx4 v[224:225], off
	v_lshl_add_u64 v[224:225], s[24:25], 0, v[146:147]
	s_add_i32 m0, s58, 0xe000
	s_nop 0
	global_load_lds_dwordx4 v[224:225], off
	s_nop 0
	s_waitcnt vmcnt(8)
	s_waitcnt lgkmcnt(0)
	s_barrier
	s_setprio 1
	s_waitcnt lgkmcnt(0)
	v_mfma_f32_16x16x32_bf16 v[128:131], v[148:151], v[184:187], v[128:131]
	v_mfma_f32_16x16x32_bf16 v[124:127], v[160:163], v[184:187], v[124:127]
	v_mfma_f32_16x16x32_bf16 v[112:115], v[148:151], v[192:195], v[112:115]
	v_mfma_f32_16x16x32_bf16 v[108:111], v[160:163], v[192:195], v[108:111]
	v_mfma_f32_16x16x32_bf16 v[94:97], v[148:151], v[208:211], v[94:97]
	v_mfma_f32_16x16x32_bf16 v[90:93], v[160:163], v[208:211], v[90:93]
	v_mfma_f32_16x16x32_bf16 v[78:81], v[148:151], v[216:219], v[78:81]
	v_mfma_f32_16x16x32_bf16 v[74:77], v[160:163], v[216:219], v[74:77]
	v_mfma_f32_16x16x32_bf16 v[128:131], v[156:159], v[188:191], v[128:131]
	v_mfma_f32_16x16x32_bf16 v[124:127], v[164:167], v[188:191], v[124:127]
	v_mfma_f32_16x16x32_bf16 v[112:115], v[156:159], v[196:199], v[112:115]
	v_mfma_f32_16x16x32_bf16 v[108:111], v[164:167], v[196:199], v[108:111]
	v_mfma_f32_16x16x32_bf16 v[94:97], v[156:159], v[212:215], v[94:97]
	v_mfma_f32_16x16x32_bf16 v[90:93], v[164:167], v[212:215], v[90:93]
	v_mfma_f32_16x16x32_bf16 v[78:81], v[156:159], v[220:223], v[78:81]
	v_mfma_f32_16x16x32_bf16 v[74:77], v[164:167], v[220:223], v[74:77]
	s_setprio 0
	s_setprio 1
	v_mfma_f32_16x16x32_bf16 v[120:123], v[168:171], v[184:187], v[120:123]
	v_mfma_f32_16x16x32_bf16 v[116:119], v[176:179], v[184:187], v[116:119]
	v_mfma_f32_16x16x32_bf16 v[104:107], v[168:171], v[192:195], v[104:107]
	v_mfma_f32_16x16x32_bf16 v[100:103], v[176:179], v[192:195], v[100:103]
	v_mfma_f32_16x16x32_bf16 v[86:89], v[168:171], v[208:211], v[86:89]
	v_mfma_f32_16x16x32_bf16 v[82:85], v[176:179], v[208:211], v[82:85]
	v_mfma_f32_16x16x32_bf16 v[70:73], v[168:171], v[216:219], v[70:73]
	v_mfma_f32_16x16x32_bf16 v[66:69], v[176:179], v[216:219], v[66:69]
	v_mfma_f32_16x16x32_bf16 v[120:123], v[172:175], v[188:191], v[120:123]
	v_mfma_f32_16x16x32_bf16 v[116:119], v[180:183], v[188:191], v[116:119]
	v_mfma_f32_16x16x32_bf16 v[104:107], v[172:175], v[196:199], v[104:107]
	v_mfma_f32_16x16x32_bf16 v[100:103], v[180:183], v[196:199], v[100:103]
	v_mfma_f32_16x16x32_bf16 v[86:89], v[172:175], v[212:215], v[86:89]
	v_mfma_f32_16x16x32_bf16 v[82:85], v[180:183], v[212:215], v[82:85]
	v_mfma_f32_16x16x32_bf16 v[70:73], v[172:175], v[220:223], v[70:73]
	v_mfma_f32_16x16x32_bf16 v[66:69], v[180:183], v[220:223], v[66:69]
	s_setprio 0
	s_barrier
	s_mov_b32 m0, s49
	v_lshl_add_u64 v[224:225], s[26:27], 0, v[140:141]
	s_add_u32 s86, s26, 0x40000
	ds_read_b128 v[184:187], v154 offset:16384
	ds_read_b128 v[188:191], v154 offset:17408
	ds_read_b128 v[192:195], v154 offset:18432
	ds_read_b128 v[196:199], v154 offset:19456
	ds_read_b128 v[208:211], v154 offset:20480
	ds_read_b128 v[212:215], v154 offset:21504
	ds_read_b128 v[216:219], v154 offset:22528
	ds_read_b128 v[220:223], v154 offset:23552
	global_load_lds_dwordx4 v[224:225], off
	v_lshl_add_u64 v[226:227], s[26:27], 0, v[136:137]
	s_mov_b32 m0, s53
	s_addc_u32 s87, s27, 0
	global_load_lds_dwordx4 v[226:227], off
	v_lshl_add_u64 v[228:229], s[86:87], 0, v[140:141]
	s_mov_b32 m0, s56
	v_lshl_add_u64 v[230:231], s[28:29], 0, v[138:139]
	global_load_lds_dwordx4 v[228:229], off
	v_lshl_add_u64 v[228:229], s[86:87], 0, v[136:137]
	s_mov_b32 m0, s57
	s_nop 0
	global_load_lds_dwordx4 v[228:229], off
	v_lshl_add_u64 v[228:229], s[28:29], 0, v[142:143]
	s_mov_b32 m0, s58
	s_nop 0
	global_load_lds_dwordx4 v[228:229], off
	s_mov_b32 m0, s59
	s_nop 0
	global_load_lds_dwordx4 v[230:231], off
	s_nop 0
	s_waitcnt vmcnt(8)
	s_waitcnt lgkmcnt(0)
	s_barrier
; #define PG8_STAGE_A(bufoff, h, ptr, nsel) do { if constexpr (Sched::GATHER) { if (nsel) PG8_STAGE_X(bufoff, ptr, vAn[h], PG8_A_AUX); else PG8_STAGE_X(bufoff, ptr, vAc[h], PG8_A_AUX); } \
;         else PG8_STAGE_X(bufoff, (ptr) + (h) * hstep, voffA, PG8_A_AUX); } while (0)
; #define PG8_STAGE(bufoff, gbase, voff) PG8_STAGE_X(bufoff, gbase, voff, PG8_B_AUX)
; #define PG8_LDA(dst, b, h) do { _Pragma("unroll") for (int m = 0; m < 4; ++m) _Pragma("unroll") for (int k = 0; k < 2; ++k) dst[m][k] = *(const PG8_LAS bf16x8*)(lds + PG8_SA(b, h) + aoff + m * 2048 + k * 1024); } while (0)
; #define PG8_LDB(dst, b, h) do { _Pragma("unroll") for (int n = 0; n < 2; ++n) _Pragma("unroll") for (int k = 0; k < 2; ++k) dst[n][k] = *(const PG8_LAS bf16x8*)(lds + PG8_SB(b, h) + boff + n * 2048 + k * 1024); } while (0)
; #define PG8_MMA(ai, bj, At, Bt) do { __builtin_amdgcn_s_setprio(1); _Pragma("unroll") for (int m = 0; m < 4; ++m) _Pragma("unroll") for (int n = 0; n < 2; ++n) _Pragma("unroll") for (int k = 0; k < 2; ++k) \
;         acc[ai][bj][m][n] = __builtin_amdgcn_mfma_f32_16x16x32_bf16(Bt[n][k], At[m][k], acc[ai][bj][m][n], 0, 0, 0); __builtin_amdgcn_s_setprio(0); } while (0)
; #define PG8_WAIT_V(n) asm volatile("s_waitcnt vmcnt(" #n ")" ::: "memory")
; #define PG8_WAIT_L(n) asm volatile("s_waitcnt lgkmcnt(" #n ")" ::: "memory")
; #define PG8_BAR __builtin_amdgcn_s_barrier()
; #define PG8_SCHED __builtin_amdgcn_sched_barrier(0)
; template <class Epi, class Sched, bool ALIGN_EPI = false, bool SP2 = false>
; __device__ __forceinline__ void gemm_phase(PG8_LAS unsigned char* lds, const Gemm g, const Sched& S, const Epi& E) {
;     ...
;             PG8_WAIT_V(8); PG8_WAIT_L(0); PG8_BAR; PG8_MMA(1, 0, At, B0); PG8_MMA(1, 1, At, B1); PG8_BAR; PG8_SCHED;
;             PG8_LDB(B0, 1, 0); PG8_LDB(B1, 1, 1); PG8_SCHED; PG8_LDA(At, 1, 0); PG8_STAGE_A(PG8_SA(0, 1), 1, a2, last);
;             PG8_WAIT_V(8); PG8_WAIT_L(0); PG8_BAR; PG8_MMA(0, 0, At, B0); PG8_MMA(0, 1, At, B1); PG8_BAR; PG8_SCHED;
;             PG8_LDA(At, 1, 1); PG8_STAGE(PG8_SB(1, 0), b3, voffB); PG8_STAGE(PG8_SB(1, 1), b3 + hstep, voffB); PG8_STAGE_A(PG8_SA(1, 0), 0, a3, last);
	s_setprio 1
	s_waitcnt lgkmcnt(0)
	v_mfma_f32_16x16x32_bf16 v[62:65], v[148:151], v[184:187], v[62:65]
	v_mfma_f32_16x16x32_bf16 v[58:61], v[160:163], v[184:187], v[58:61]
	v_mfma_f32_16x16x32_bf16 v[46:49], v[148:151], v[192:195], v[46:49]
	v_mfma_f32_16x16x32_bf16 v[42:45], v[160:163], v[192:195], v[42:45]
	v_mfma_f32_16x16x32_bf16 v[30:33], v[148:151], v[208:211], v[30:33]
	v_mfma_f32_16x16x32_bf16 v[26:29], v[160:163], v[208:211], v[26:29]
	v_mfma_f32_16x16x32_bf16 v[14:17], v[148:151], v[216:219], v[14:17]
	v_mfma_f32_16x16x32_bf16 v[10:13], v[160:163], v[216:219], v[10:13]
	v_mfma_f32_16x16x32_bf16 v[62:65], v[156:159], v[188:191], v[62:65]
	v_mfma_f32_16x16x32_bf16 v[58:61], v[164:167], v[188:191], v[58:61]
	v_mfma_f32_16x16x32_bf16 v[46:49], v[156:159], v[196:199], v[46:49]
	v_mfma_f32_16x16x32_bf16 v[42:45], v[164:167], v[196:199], v[42:45]
	v_mfma_f32_16x16x32_bf16 v[30:33], v[156:159], v[212:215], v[30:33]
	v_mfma_f32_16x16x32_bf16 v[26:29], v[164:167], v[212:215], v[26:29]
	v_mfma_f32_16x16x32_bf16 v[14:17], v[156:159], v[220:223], v[14:17]
	v_mfma_f32_16x16x32_bf16 v[10:13], v[164:167], v[220:223], v[10:13]
	s_setprio 0
	s_setprio 1
	v_mfma_f32_16x16x32_bf16 v[54:57], v[168:171], v[184:187], v[54:57]
	v_mfma_f32_16x16x32_bf16 v[50:53], v[176:179], v[184:187], v[50:53]
	v_mfma_f32_16x16x32_bf16 v[38:41], v[168:171], v[192:195], v[38:41]
	v_mfma_f32_16x16x32_bf16 v[34:37], v[176:179], v[192:195], v[34:37]
	v_mfma_f32_16x16x32_bf16 v[22:25], v[168:171], v[208:211], v[22:25]
	v_mfma_f32_16x16x32_bf16 v[18:21], v[176:179], v[208:211], v[18:21]
	v_mfma_f32_16x16x32_bf16 v[6:9], v[168:171], v[216:219], v[6:9]
	v_mfma_f32_16x16x32_bf16 v[2:5], v[176:179], v[216:219], v[2:5]
	v_mfma_f32_16x16x32_bf16 v[54:57], v[172:175], v[188:191], v[54:57]
	v_mfma_f32_16x16x32_bf16 v[50:53], v[180:183], v[188:191], v[50:53]
	v_mfma_f32_16x16x32_bf16 v[38:41], v[172:175], v[196:199], v[38:41]
	v_mfma_f32_16x16x32_bf16 v[34:37], v[180:183], v[196:199], v[34:37]
	v_mfma_f32_16x16x32_bf16 v[22:25], v[172:175], v[212:215], v[22:25]
	v_mfma_f32_16x16x32_bf16 v[18:21], v[180:183], v[212:215], v[18:21]
	v_mfma_f32_16x16x32_bf16 v[6:9], v[172:175], v[220:223], v[6:9]
	v_mfma_f32_16x16x32_bf16 v[2:5], v[180:183], v[220:223], v[2:5]
	s_setprio 0
	s_barrier
	v_add_u32_e32 v155, s50, v152
	ds_read_b128 v[148:151], v155
	ds_read_b128 v[156:159], v155 offset:1024
	ds_read_b128 v[160:163], v155 offset:2048
	ds_read_b128 v[164:167], v155 offset:3072
	v_add_u32_e32 v155, s51, v152
	ds_read_b128 v[168:171], v155
	ds_read_b128 v[172:175], v155 offset:1024
	ds_read_b128 v[176:179], v155 offset:2048
	ds_read_b128 v[180:183], v155 offset:3072
	s_add_u32 s28, s28, 0x40000
	s_addc_u32 s29, s29, 0
	s_mov_b32 m0, s61
	v_lshl_add_u64 v[232:233], s[28:29], 0, v[142:143]
	ds_read_b128 v[184:187], v154 offset:32768
	ds_read_b128 v[188:191], v154 offset:33792
	ds_read_b128 v[192:195], v154 offset:34816
	ds_read_b128 v[196:199], v154 offset:35840
	ds_read_b128 v[208:211], v154 offset:36864
	ds_read_b128 v[212:215], v154 offset:37888
	ds_read_b128 v[216:219], v154 offset:38912
	ds_read_b128 v[220:223], v154 offset:39936
	global_load_lds_dwordx4 v[232:233], off
	v_lshl_add_u64 v[232:233], s[28:29], 0, v[138:139]
	s_mov_b32 m0, s68
	s_nop 0
	global_load_lds_dwordx4 v[232:233], off
	s_nop 0
	s_waitcnt vmcnt(8)
	s_waitcnt lgkmcnt(0)
	s_barrier
	s_setprio 1
	s_waitcnt lgkmcnt(0)
	v_mfma_f32_16x16x32_bf16 v[128:131], v[148:151], v[184:187], v[128:131]
	v_mfma_f32_16x16x32_bf16 v[124:127], v[160:163], v[184:187], v[124:127]
	v_mfma_f32_16x16x32_bf16 v[112:115], v[148:151], v[192:195], v[112:115]
	v_mfma_f32_16x16x32_bf16 v[108:111], v[160:163], v[192:195], v[108:111]
	v_mfma_f32_16x16x32_bf16 v[94:97], v[148:151], v[208:211], v[94:97]
	v_mfma_f32_16x16x32_bf16 v[90:93], v[160:163], v[208:211], v[90:93]
	v_mfma_f32_16x16x32_bf16 v[78:81], v[148:151], v[216:219], v[78:81]
	v_mfma_f32_16x16x32_bf16 v[74:77], v[160:163], v[216:219], v[74:77]
	v_mfma_f32_16x16x32_bf16 v[128:131], v[156:159], v[188:191], v[128:131]
	v_mfma_f32_16x16x32_bf16 v[124:127], v[164:167], v[188:191], v[124:127]
	v_mfma_f32_16x16x32_bf16 v[112:115], v[156:159], v[196:199], v[112:115]
	v_mfma_f32_16x16x32_bf16 v[108:111], v[164:167], v[196:199], v[108:111]
	v_mfma_f32_16x16x32_bf16 v[94:97], v[156:159], v[212:215], v[94:97]
	v_mfma_f32_16x16x32_bf16 v[90:93], v[164:167], v[212:215], v[90:93]
	v_mfma_f32_16x16x32_bf16 v[78:81], v[156:159], v[220:223], v[78:81]
	v_mfma_f32_16x16x32_bf16 v[74:77], v[164:167], v[220:223], v[74:77]
	s_setprio 0
	s_setprio 1
	v_mfma_f32_16x16x32_bf16 v[120:123], v[168:171], v[184:187], v[120:123]
	v_mfma_f32_16x16x32_bf16 v[116:119], v[176:179], v[184:187], v[116:119]
	v_mfma_f32_16x16x32_bf16 v[104:107], v[168:171], v[192:195], v[104:107]
	v_mfma_f32_16x16x32_bf16 v[100:103], v[176:179], v[192:195], v[100:103]
	v_mfma_f32_16x16x32_bf16 v[86:89], v[168:171], v[208:211], v[86:89]
	v_mfma_f32_16x16x32_bf16 v[82:85], v[176:179], v[208:211], v[82:85]
	v_mfma_f32_16x16x32_bf16 v[70:73], v[168:171], v[216:219], v[70:73]
	v_mfma_f32_16x16x32_bf16 v[66:69], v[176:179], v[216:219], v[66:69]
	v_mfma_f32_16x16x32_bf16 v[120:123], v[172:175], v[188:191], v[120:123]
	v_mfma_f32_16x16x32_bf16 v[116:119], v[180:183], v[188:191], v[116:119]
	v_mfma_f32_16x16x32_bf16 v[104:107], v[172:175], v[196:199], v[104:107]
	v_mfma_f32_16x16x32_bf16 v[100:103], v[180:183], v[196:199], v[100:103]
	v_mfma_f32_16x16x32_bf16 v[86:89], v[172:175], v[212:215], v[86:89]
	v_mfma_f32_16x16x32_bf16 v[82:85], v[180:183], v[212:215], v[82:85]
	v_mfma_f32_16x16x32_bf16 v[70:73], v[172:175], v[220:223], v[70:73]
	v_mfma_f32_16x16x32_bf16 v[66:69], v[180:183], v[220:223], v[66:69]
	s_setprio 0
	s_barrier
; #define PG8_STAGE_A(bufoff, h, ptr, nsel) do { if constexpr (Sched::GATHER) { if (nsel) PG8_STAGE_X(bufoff, ptr, vAn[h], PG8_A_AUX); else PG8_STAGE_X(bufoff, ptr, vAc[h], PG8_A_AUX); } \
;         else PG8_STAGE_X(bufoff, (ptr) + (h) * hstep, voffA, PG8_A_AUX); } while (0)
; #define PG8_STAGE(bufoff, gbase, voff) PG8_STAGE_X(bufoff, gbase, voff, PG8_B_AUX)
; #define PG8_LDA(dst, b, h) do { _Pragma("unroll") for (int m = 0; m < 4; ++m) _Pragma("unroll") for (int k = 0; k < 2; ++k) dst[m][k] = *(const PG8_LAS bf16x8*)(lds + PG8_SA(b, h) + aoff + m * 2048 + k * 1024); } while (0)
; #define PG8_MMA(ai, bj, At, Bt) do { __builtin_amdgcn_s_setprio(1); _Pragma("unroll") for (int m = 0; m < 4; ++m) _Pragma("unroll") for (int n = 0; n < 2; ++n) _Pragma("unroll") for (int k = 0; k < 2; ++k) \
;         acc[ai][bj][m][n] = __builtin_amdgcn_mfma_f32_16x16x32_bf16(Bt[n][k], At[m][k], acc[ai][bj][m][n], 0, 0, 0); __builtin_amdgcn_s_setprio(0); } while (0)
; #define PG8_WAIT_V(n) asm volatile("s_waitcnt vmcnt(" #n ")" ::: "memory")
; #define PG8_WAIT_L(n) asm volatile("s_waitcnt lgkmcnt(" #n ")" ::: "memory")
; #define PG8_BAR __builtin_amdgcn_s_barrier()
; #define PG8_SCHED __builtin_amdgcn_sched_barrier(0)
; template <class Epi, class Sched, bool ALIGN_EPI = false, bool SP2 = false>
; __device__ __forceinline__ void gemm_phase(PG8_LAS unsigned char* lds, const Gemm g, const Sched& S, const Epi& E) {
;     ...
;             PG8_LDA(At, 1, 1); PG8_STAGE(PG8_SB(1, 0), b3, voffB); PG8_STAGE(PG8_SB(1, 1), b3 + hstep, voffB); PG8_STAGE_A(PG8_SA(1, 0), 0, a3, last);
;             PG8_WAIT_V(8); PG8_WAIT_L(0); PG8_BAR; PG8_MMA(1, 0, At, B0); PG8_MMA(1, 1, At, B1); PG8_BAR; PG8_SCHED;
;     ...
;         }
;         if constexpr (ALIGN_EPI) { if (wr == 0) PG8_BAR; }
	s_mov_b32 m0, s69
	v_lshl_add_u64 v[224:225], v[224:225], 0, s[54:55]
	s_add_u32 s26, s26, 0x40080
	ds_read_b128 v[184:187], v154 offset:49152
	ds_read_b128 v[188:191], v154 offset:50176
	ds_read_b128 v[192:195], v154 offset:51200
	ds_read_b128 v[196:199], v154 offset:52224
	ds_read_b128 v[208:211], v154 offset:53248
	ds_read_b128 v[212:215], v154 offset:54272
	ds_read_b128 v[216:219], v154 offset:55296
	ds_read_b128 v[220:223], v154 offset:56320
	global_load_lds_dwordx4 v[224:225], off
	v_lshl_add_u64 v[224:225], v[226:227], 0, s[54:55]
	s_mov_b32 m0, s88
	s_addc_u32 s27, s27, 0
	global_load_lds_dwordx4 v[224:225], off
	v_lshl_add_u64 v[224:225], s[26:27], 0, v[140:141]
	s_mov_b32 m0, s38
	s_nop 0
	global_load_lds_dwordx4 v[224:225], off
	v_lshl_add_u64 v[224:225], s[26:27], 0, v[136:137]
	s_mov_b32 m0, s95
	s_nop 0
	global_load_lds_dwordx4 v[224:225], off
	v_lshl_add_u64 v[224:225], v[228:229], 0, s[54:55]
	s_mov_b32 m0, s89
	s_nop 0
	global_load_lds_dwordx4 v[224:225], off
	v_lshl_add_u64 v[224:225], v[230:231], 0, s[54:55]
	s_mov_b32 m0, s94
	s_nop 0
	global_load_lds_dwordx4 v[224:225], off
	s_waitcnt vmcnt(8)
	s_waitcnt lgkmcnt(0)
	s_barrier
	s_setprio 1
	s_waitcnt lgkmcnt(0)
	v_mfma_f32_16x16x32_bf16 v[62:65], v[148:151], v[184:187], v[62:65]
	v_mfma_f32_16x16x32_bf16 v[58:61], v[160:163], v[184:187], v[58:61]
	v_mfma_f32_16x16x32_bf16 v[46:49], v[148:151], v[192:195], v[46:49]
	v_mfma_f32_16x16x32_bf16 v[42:45], v[160:163], v[192:195], v[42:45]
	v_mfma_f32_16x16x32_bf16 v[30:33], v[148:151], v[208:211], v[30:33]
	v_mfma_f32_16x16x32_bf16 v[26:29], v[160:163], v[208:211], v[26:29]
	v_mfma_f32_16x16x32_bf16 v[14:17], v[148:151], v[216:219], v[14:17]
	v_mfma_f32_16x16x32_bf16 v[10:13], v[160:163], v[216:219], v[10:13]
	v_mfma_f32_16x16x32_bf16 v[62:65], v[156:159], v[188:191], v[62:65]
	v_mfma_f32_16x16x32_bf16 v[58:61], v[164:167], v[188:191], v[58:61]
	v_mfma_f32_16x16x32_bf16 v[46:49], v[156:159], v[196:199], v[46:49]
	v_mfma_f32_16x16x32_bf16 v[42:45], v[164:167], v[196:199], v[42:45]
	v_mfma_f32_16x16x32_bf16 v[30:33], v[156:159], v[212:215], v[30:33]
	v_mfma_f32_16x16x32_bf16 v[26:29], v[164:167], v[212:215], v[26:29]
	v_mfma_f32_16x16x32_bf16 v[14:17], v[156:159], v[220:223], v[14:17]
	v_mfma_f32_16x16x32_bf16 v[10:13], v[164:167], v[220:223], v[10:13]
	s_setprio 0
	s_setprio 1
	v_mfma_f32_16x16x32_bf16 v[54:57], v[168:171], v[184:187], v[54:57]
	v_mfma_f32_16x16x32_bf16 v[50:53], v[176:179], v[184:187], v[50:53]
	v_mfma_f32_16x16x32_bf16 v[38:41], v[168:171], v[192:195], v[38:41]
	v_mfma_f32_16x16x32_bf16 v[34:37], v[176:179], v[192:195], v[34:37]
	v_mfma_f32_16x16x32_bf16 v[22:25], v[168:171], v[208:211], v[22:25]
	v_mfma_f32_16x16x32_bf16 v[18:21], v[176:179], v[208:211], v[18:21]
	v_mfma_f32_16x16x32_bf16 v[6:9], v[168:171], v[216:219], v[6:9]
	v_mfma_f32_16x16x32_bf16 v[2:5], v[176:179], v[216:219], v[2:5]
	v_mfma_f32_16x16x32_bf16 v[54:57], v[172:175], v[188:191], v[54:57]
	v_mfma_f32_16x16x32_bf16 v[50:53], v[180:183], v[188:191], v[50:53]
	v_mfma_f32_16x16x32_bf16 v[38:41], v[172:175], v[196:199], v[38:41]
	v_mfma_f32_16x16x32_bf16 v[34:37], v[180:183], v[196:199], v[34:37]
	v_mfma_f32_16x16x32_bf16 v[22:25], v[172:175], v[212:215], v[22:25]
	v_mfma_f32_16x16x32_bf16 v[18:21], v[180:183], v[212:215], v[18:21]
	v_mfma_f32_16x16x32_bf16 v[6:9], v[172:175], v[220:223], v[6:9]
	v_mfma_f32_16x16x32_bf16 v[2:5], v[180:183], v[220:223], v[2:5]
	s_setprio 0
	s_barrier
	s_add_i32 s73, s73, 2
	s_add_u32 s24, s24, 0x100
	s_addc_u32 s25, s25, 0
	s_add_u32 s64, s64, 0x100
	s_addc_u32 s72, s72, 0
	s_cmp_gt_u32 s73, 13
	s_cbranch_scc0 .LBB13_822
	s_and_b64 vcc, exec, s[14:15]
	s_mov_b32 s64, 0x18000
	s_cbranch_vccz .LBB13_825
	s_barrier

; #define PG8_LAS __attribute__((address_space(3)))
; #define PG8_STAGE_A(bufoff, h, ptr, nsel) do { if constexpr (Sched::GATHER) { if (nsel) PG8_STAGE_X(bufoff, ptr, vAn[h], PG8_A_AUX); else PG8_STAGE_X(bufoff, ptr, vAc[h], PG8_A_AUX); } \
;         else PG8_STAGE_X(bufoff, (ptr) + (h) * hstep, voffA, PG8_A_AUX); } while (0)
; #define PG8_STAGE(bufoff, gbase, voff) PG8_STAGE_X(bufoff, gbase, voff, PG8_B_AUX)
; #define PG8_LDA(dst, b, h) do { _Pragma("unroll") for (int m = 0; m < 4; ++m) _Pragma("unroll") for (int k = 0; k < 2; ++k) dst[m][k] = *(const PG8_LAS bf16x8*)(lds + PG8_SA(b, h) + aoff + m * 2048 + k * 1024); } while (0)
; #define PG8_LDB(dst, b, h) do { _Pragma("unroll") for (int n = 0; n < 2; ++n) _Pragma("unroll") for (int k = 0; k < 2; ++k) dst[n][k] = *(const PG8_LAS bf16x8*)(lds + PG8_SB(b, h) + boff + n * 2048 + k * 1024); } while (0)
; #define PG8_WAIT_V(n) asm volatile("s_waitcnt vmcnt(" #n ")" ::: "memory")
; #define PG8_WAIT_L(n) asm volatile("s_waitcnt lgkmcnt(" #n ")" ::: "memory")
; #define PG8_BAR __builtin_amdgcn_s_barrier()
; #define PG8_SCHED __builtin_amdgcn_sched_barrier(0)
; template <class Epi, class Sched, bool ALIGN_EPI = false, bool SP2 = false>
; __device__ __forceinline__ void gemm_phase(PG8_LAS unsigned char* lds, const Gemm g, const Sched& S, const Epi& E) {
;     ...
;             const char* a2 = last ? nA : cA + (size_t)(t + 2) * kstep; const char* b2 = last ? nB : cB + (size_t)(t + 2) * kstep;
;             const char* a3 = a2 + kstep; const char* b3 = b2 + kstep;
;             if (last && has_next) S.a_ready(nxt);
;             if constexpr (Sched::GATHER) { if (last) { const u32x4 pv_ = *(const PG8_LAS u32x4*)(lds + STAGE_BYTES + tid * 16); vAn[0][0] = pv_.x; vAn[0][1] = pv_.y; vAn[1][0] = pv_.z; vAn[1][1] = pv_.w; } }
;             if constexpr (SP2) {
;             PG8_LDB(B0, 0, 0); PG8_LDB(B1, 0, 1); PG8_SCHED; PG8_LDA(At, 0, 0); PG8_STAGE_A(PG8_SA(1, 1), 1, a1, false);
;             PG8_WAIT_V(8); PG8_WAIT_L(0); PG8_BAR; PG8_MMA(0, 0, At, B0); PG8_MMA(0, 1, At, B1); PG8_BAR; PG8_SCHED;
;             PG8_LDA(At, 0, 1); PG8_STAGE(PG8_SB(0, 0), b2, voffB); PG8_STAGE(PG8_SB(0, 1), b2 + hstep, voffB); PG8_STAGE_A(PG8_SA(0, 0), 0, a2, last);
;             PG8_WAIT_V(8); PG8_WAIT_L(0); PG8_BAR; PG8_MMA(1, 0, At, B0); PG8_MMA(1, 1, At, B1); PG8_BAR; PG8_SCHED;
.LBB13_844:
	v_add_u32_e32 v155, s46, v152
	ds_read_b128 v[148:151], v155
	ds_read_b128 v[156:159], v155 offset:1024
	ds_read_b128 v[160:163], v155 offset:2048
	ds_read_b128 v[164:167], v155 offset:3072
	v_add_u32_e32 v155, s47, v152
	ds_read_b128 v[168:171], v155
	ds_read_b128 v[172:175], v155 offset:1024
	ds_read_b128 v[176:179], v155 offset:2048
	ds_read_b128 v[180:183], v155 offset:3072
	s_add_u32 s24, s22, 0xfffc0080
	s_addc_u32 s25, s23, -1
	s_cmp_eq_u32 s64, 12
	s_cselect_b32 s27, s17, s25
	s_cselect_b32 s26, s34, s24
	s_cselect_b32 s25, s15, s60
	s_cselect_b32 s24, s38, s52
	v_lshl_add_u64 v[224:225], s[22:23], 0, v[144:145]
	s_add_i32 m0, s48, 0xc000
	ds_read_b128 v[184:187], v154
	ds_read_b128 v[188:191], v154 offset:1024
	ds_read_b128 v[192:195], v154 offset:2048
	ds_read_b128 v[196:199], v154 offset:3072
	ds_read_b128 v[208:211], v154 offset:4096
	ds_read_b128 v[212:215], v154 offset:5120
	ds_read_b128 v[216:219], v154 offset:6144
	ds_read_b128 v[220:223], v154 offset:7168
	global_load_lds_dwordx4 v[224:225], off
	v_lshl_add_u64 v[224:225], s[22:23], 0, v[146:147]
	s_add_i32 m0, s48, 0xe000
	s_nop 0
	global_load_lds_dwordx4 v[224:225], off
	s_nop 0
	s_waitcnt vmcnt(8)
	s_waitcnt lgkmcnt(0)
	s_barrier
	s_setprio 1
	s_waitcnt lgkmcnt(0)
	v_mfma_f32_16x16x32_bf16 v[128:131], v[148:151], v[184:187], v[128:131]
	v_mfma_f32_16x16x32_bf16 v[124:127], v[160:163], v[184:187], v[124:127]
	v_mfma_f32_16x16x32_bf16 v[112:115], v[148:151], v[192:195], v[112:115]
	v_mfma_f32_16x16x32_bf16 v[108:111], v[160:163], v[192:195], v[108:111]
	v_mfma_f32_16x16x32_bf16 v[94:97], v[148:151], v[208:211], v[94:97]
	v_mfma_f32_16x16x32_bf16 v[90:93], v[160:163], v[208:211], v[90:93]
	v_mfma_f32_16x16x32_bf16 v[78:81], v[148:151], v[216:219], v[78:81]
	v_mfma_f32_16x16x32_bf16 v[74:77], v[160:163], v[216:219], v[74:77]
	v_mfma_f32_16x16x32_bf16 v[128:131], v[156:159], v[188:191], v[128:131]
	v_mfma_f32_16x16x32_bf16 v[124:127], v[164:167], v[188:191], v[124:127]
	v_mfma_f32_16x16x32_bf16 v[112:115], v[156:159], v[196:199], v[112:115]
	v_mfma_f32_16x16x32_bf16 v[108:111], v[164:167], v[196:199], v[108:111]
	v_mfma_f32_16x16x32_bf16 v[94:97], v[156:159], v[212:215], v[94:97]
	v_mfma_f32_16x16x32_bf16 v[90:93], v[164:167], v[212:215], v[90:93]
	v_mfma_f32_16x16x32_bf16 v[78:81], v[156:159], v[220:223], v[78:81]
	v_mfma_f32_16x16x32_bf16 v[74:77], v[164:167], v[220:223], v[74:77]
	s_setprio 0
	s_setprio 1
	v_mfma_f32_16x16x32_bf16 v[120:123], v[168:171], v[184:187], v[120:123]
	v_mfma_f32_16x16x32_bf16 v[116:119], v[176:179], v[184:187], v[116:119]
	v_mfma_f32_16x16x32_bf16 v[104:107], v[168:171], v[192:195], v[104:107]
	v_mfma_f32_16x16x32_bf16 v[100:103], v[176:179], v[192:195], v[100:103]
	v_mfma_f32_16x16x32_bf16 v[86:89], v[168:171], v[208:211], v[86:89]
	v_mfma_f32_16x16x32_bf16 v[82:85], v[176:179], v[208:211], v[82:85]
	v_mfma_f32_16x16x32_bf16 v[70:73], v[168:171], v[216:219], v[70:73]
	v_mfma_f32_16x16x32_bf16 v[66:69], v[176:179], v[216:219], v[66:69]
	v_mfma_f32_16x16x32_bf16 v[120:123], v[172:175], v[188:191], v[120:123]
	v_mfma_f32_16x16x32_bf16 v[116:119], v[180:183], v[188:191], v[116:119]
	v_mfma_f32_16x16x32_bf16 v[104:107], v[172:175], v[196:199], v[104:107]
	v_mfma_f32_16x16x32_bf16 v[100:103], v[180:183], v[196:199], v[100:103]
	v_mfma_f32_16x16x32_bf16 v[86:89], v[172:175], v[212:215], v[86:89]
	v_mfma_f32_16x16x32_bf16 v[82:85], v[180:183], v[212:215], v[82:85]
	v_mfma_f32_16x16x32_bf16 v[70:73], v[172:175], v[220:223], v[70:73]
	v_mfma_f32_16x16x32_bf16 v[66:69], v[180:183], v[220:223], v[66:69]
	s_setprio 0
	s_barrier
	s_mov_b32 m0, s0
	v_lshl_add_u64 v[224:225], s[24:25], 0, v[140:141]
	s_add_u32 s72, s24, 0x40000
	ds_read_b128 v[184:187], v154 offset:16384
	ds_read_b128 v[188:191], v154 offset:17408
	ds_read_b128 v[192:195], v154 offset:18432
	ds_read_b128 v[196:199], v154 offset:19456
	ds_read_b128 v[208:211], v154 offset:20480
	ds_read_b128 v[212:215], v154 offset:21504
	ds_read_b128 v[216:219], v154 offset:22528
	ds_read_b128 v[220:223], v154 offset:23552
	global_load_lds_dwordx4 v[224:225], off
	v_lshl_add_u64 v[226:227], s[24:25], 0, v[136:137]
	s_mov_b32 m0, s1
	s_addc_u32 s73, s25, 0
	global_load_lds_dwordx4 v[226:227], off
	v_lshl_add_u64 v[228:229], s[72:73], 0, v[140:141]
	s_mov_b32 m0, s2
	v_lshl_add_u64 v[230:231], s[26:27], 0, v[138:139]
	global_load_lds_dwordx4 v[228:229], off
	v_lshl_add_u64 v[228:229], s[72:73], 0, v[136:137]
	s_mov_b32 m0, s3
	s_nop 0
	global_load_lds_dwordx4 v[228:229], off
	v_lshl_add_u64 v[228:229], s[26:27], 0, v[142:143]
	s_mov_b32 m0, s48
	s_nop 0
	global_load_lds_dwordx4 v[228:229], off
	s_mov_b32 m0, s49
	s_nop 0
	global_load_lds_dwordx4 v[230:231], off
	s_nop 0
	s_waitcnt vmcnt(8)
	s_waitcnt lgkmcnt(0)
	s_barrier
; #define PG8_STAGE_A(bufoff, h, ptr, nsel) do { if constexpr (Sched::GATHER) { if (nsel) PG8_STAGE_X(bufoff, ptr, vAn[h], PG8_A_AUX); else PG8_STAGE_X(bufoff, ptr, vAc[h], PG8_A_AUX); } \
;         else PG8_STAGE_X(bufoff, (ptr) + (h) * hstep, voffA, PG8_A_AUX); } while (0)
; #define PG8_STAGE(bufoff, gbase, voff) PG8_STAGE_X(bufoff, gbase, voff, PG8_B_AUX)
; #define PG8_LDA(dst, b, h) do { _Pragma("unroll") for (int m = 0; m < 4; ++m) _Pragma("unroll") for (int k = 0; k < 2; ++k) dst[m][k] = *(const PG8_LAS bf16x8*)(lds + PG8_SA(b, h) + aoff + m * 2048 + k * 1024); } while (0)
; #define PG8_LDB(dst, b, h) do { _Pragma("unroll") for (int n = 0; n < 2; ++n) _Pragma("unroll") for (int k = 0; k < 2; ++k) dst[n][k] = *(const PG8_LAS bf16x8*)(lds + PG8_SB(b, h) + boff + n * 2048 + k * 1024); } while (0)
; #define PG8_MMA(ai, bj, At, Bt) do { __builtin_amdgcn_s_setprio(1); _Pragma("unroll") for (int m = 0; m < 4; ++m) _Pragma("unroll") for (int n = 0; n < 2; ++n) _Pragma("unroll") for (int k = 0; k < 2; ++k) \
;         acc[ai][bj][m][n] = __builtin_amdgcn_mfma_f32_16x16x32_bf16(Bt[n][k], At[m][k], acc[ai][bj][m][n], 0, 0, 0); __builtin_amdgcn_s_setprio(0); } while (0)
; #define PG8_WAIT_V(n) asm volatile("s_waitcnt vmcnt(" #n ")" ::: "memory")
; #define PG8_WAIT_L(n) asm volatile("s_waitcnt lgkmcnt(" #n ")" ::: "memory")
; #define PG8_BAR __builtin_amdgcn_s_barrier()
; #define PG8_SCHED __builtin_amdgcn_sched_barrier(0)
; template <class Epi, class Sched, bool ALIGN_EPI = false, bool SP2 = false>
; __device__ __forceinline__ void gemm_phase(PG8_LAS unsigned char* lds, const Gemm g, const Sched& S, const Epi& E) {
;     ...
;             PG8_WAIT_V(8); PG8_WAIT_L(0); PG8_BAR; PG8_MMA(1, 0, At, B0); PG8_MMA(1, 1, At, B1); PG8_BAR; PG8_SCHED;
;             PG8_LDB(B0, 1, 0); PG8_LDB(B1, 1, 1); PG8_SCHED; PG8_LDA(At, 1, 0); PG8_STAGE_A(PG8_SA(0, 1), 1, a2, last);
;             PG8_WAIT_V(8); PG8_WAIT_L(0); PG8_BAR; PG8_MMA(0, 0, At, B0); PG8_MMA(0, 1, At, B1); PG8_BAR; PG8_SCHED;
;             PG8_LDA(At, 1, 1); PG8_STAGE(PG8_SB(1, 0), b3, voffB); PG8_STAGE(PG8_SB(1, 1), b3 + hstep, voffB); PG8_STAGE_A(PG8_SA(1, 0), 0, a3, last);
	s_setprio 1
	s_waitcnt lgkmcnt(0)
	v_mfma_f32_16x16x32_bf16 v[62:65], v[148:151], v[184:187], v[62:65]
	v_mfma_f32_16x16x32_bf16 v[58:61], v[160:163], v[184:187], v[58:61]
	v_mfma_f32_16x16x32_bf16 v[46:49], v[148:151], v[192:195], v[46:49]
	v_mfma_f32_16x16x32_bf16 v[42:45], v[160:163], v[192:195], v[42:45]
	v_mfma_f32_16x16x32_bf16 v[30:33], v[148:151], v[208:211], v[30:33]
	v_mfma_f32_16x16x32_bf16 v[26:29], v[160:163], v[208:211], v[26:29]
	v_mfma_f32_16x16x32_bf16 v[14:17], v[148:151], v[216:219], v[14:17]
	v_mfma_f32_16x16x32_bf16 v[10:13], v[160:163], v[216:219], v[10:13]
	v_mfma_f32_16x16x32_bf16 v[62:65], v[156:159], v[188:191], v[62:65]
	v_mfma_f32_16x16x32_bf16 v[58:61], v[164:167], v[188:191], v[58:61]
	v_mfma_f32_16x16x32_bf16 v[46:49], v[156:159], v[196:199], v[46:49]
	v_mfma_f32_16x16x32_bf16 v[42:45], v[164:167], v[196:199], v[42:45]
	v_mfma_f32_16x16x32_bf16 v[30:33], v[156:159], v[212:215], v[30:33]
	v_mfma_f32_16x16x32_bf16 v[26:29], v[164:167], v[212:215], v[26:29]
	v_mfma_f32_16x16x32_bf16 v[14:17], v[156:159], v[220:223], v[14:17]
	v_mfma_f32_16x16x32_bf16 v[10:13], v[164:167], v[220:223], v[10:13]
	s_setprio 0
	s_setprio 1
	v_mfma_f32_16x16x32_bf16 v[54:57], v[168:171], v[184:187], v[54:57]
	v_mfma_f32_16x16x32_bf16 v[50:53], v[176:179], v[184:187], v[50:53]
	v_mfma_f32_16x16x32_bf16 v[38:41], v[168:171], v[192:195], v[38:41]
	v_mfma_f32_16x16x32_bf16 v[34:37], v[176:179], v[192:195], v[34:37]
	v_mfma_f32_16x16x32_bf16 v[22:25], v[168:171], v[208:211], v[22:25]
	v_mfma_f32_16x16x32_bf16 v[18:21], v[176:179], v[208:211], v[18:21]
	v_mfma_f32_16x16x32_bf16 v[6:9], v[168:171], v[216:219], v[6:9]
	v_mfma_f32_16x16x32_bf16 v[2:5], v[176:179], v[216:219], v[2:5]
	v_mfma_f32_16x16x32_bf16 v[54:57], v[172:175], v[188:191], v[54:57]
	v_mfma_f32_16x16x32_bf16 v[50:53], v[180:183], v[188:191], v[50:53]
	v_mfma_f32_16x16x32_bf16 v[38:41], v[172:175], v[196:199], v[38:41]
	v_mfma_f32_16x16x32_bf16 v[34:37], v[180:183], v[196:199], v[34:37]
	v_mfma_f32_16x16x32_bf16 v[22:25], v[172:175], v[212:215], v[22:25]
	v_mfma_f32_16x16x32_bf16 v[18:21], v[180:183], v[212:215], v[18:21]
	v_mfma_f32_16x16x32_bf16 v[6:9], v[172:175], v[220:223], v[6:9]
	v_mfma_f32_16x16x32_bf16 v[2:5], v[180:183], v[220:223], v[2:5]
	s_setprio 0
	s_barrier
	v_add_u32_e32 v155, s50, v152
	ds_read_b128 v[148:151], v155
	ds_read_b128 v[156:159], v155 offset:1024
	ds_read_b128 v[160:163], v155 offset:2048
	ds_read_b128 v[164:167], v155 offset:3072
	v_add_u32_e32 v155, s51, v152
	ds_read_b128 v[168:171], v155
	ds_read_b128 v[172:175], v155 offset:1024
	ds_read_b128 v[176:179], v155 offset:2048
	ds_read_b128 v[180:183], v155 offset:3072
	s_add_u32 s26, s26, 0x40000
	s_addc_u32 s27, s27, 0
	s_mov_b32 m0, s53
	v_lshl_add_u64 v[232:233], s[26:27], 0, v[142:143]
	ds_read_b128 v[184:187], v154 offset:32768
	ds_read_b128 v[188:191], v154 offset:33792
	ds_read_b128 v[192:195], v154 offset:34816
	ds_read_b128 v[196:199], v154 offset:35840
	ds_read_b128 v[208:211], v154 offset:36864
	ds_read_b128 v[212:215], v154 offset:37888
	ds_read_b128 v[216:219], v154 offset:38912
	ds_read_b128 v[220:223], v154 offset:39936
	global_load_lds_dwordx4 v[232:233], off
	v_lshl_add_u64 v[232:233], s[26:27], 0, v[138:139]
	s_mov_b32 m0, s56
	s_nop 0
	global_load_lds_dwordx4 v[232:233], off
	s_nop 0
	s_waitcnt vmcnt(8)
	s_waitcnt lgkmcnt(0)
	s_barrier
	s_setprio 1
	s_waitcnt lgkmcnt(0)
	v_mfma_f32_16x16x32_bf16 v[128:131], v[148:151], v[184:187], v[128:131]
	v_mfma_f32_16x16x32_bf16 v[124:127], v[160:163], v[184:187], v[124:127]
	v_mfma_f32_16x16x32_bf16 v[112:115], v[148:151], v[192:195], v[112:115]
	v_mfma_f32_16x16x32_bf16 v[108:111], v[160:163], v[192:195], v[108:111]
	v_mfma_f32_16x16x32_bf16 v[94:97], v[148:151], v[208:211], v[94:97]
	v_mfma_f32_16x16x32_bf16 v[90:93], v[160:163], v[208:211], v[90:93]
	v_mfma_f32_16x16x32_bf16 v[78:81], v[148:151], v[216:219], v[78:81]
	v_mfma_f32_16x16x32_bf16 v[74:77], v[160:163], v[216:219], v[74:77]
	v_mfma_f32_16x16x32_bf16 v[128:131], v[156:159], v[188:191], v[128:131]
	v_mfma_f32_16x16x32_bf16 v[124:127], v[164:167], v[188:191], v[124:127]
	v_mfma_f32_16x16x32_bf16 v[112:115], v[156:159], v[196:199], v[112:115]
	v_mfma_f32_16x16x32_bf16 v[108:111], v[164:167], v[196:199], v[108:111]
	v_mfma_f32_16x16x32_bf16 v[94:97], v[156:159], v[212:215], v[94:97]
	v_mfma_f32_16x16x32_bf16 v[90:93], v[164:167], v[212:215], v[90:93]
	v_mfma_f32_16x16x32_bf16 v[78:81], v[156:159], v[220:223], v[78:81]
	v_mfma_f32_16x16x32_bf16 v[74:77], v[164:167], v[220:223], v[74:77]
	s_setprio 0
	s_setprio 1
	v_mfma_f32_16x16x32_bf16 v[120:123], v[168:171], v[184:187], v[120:123]
	v_mfma_f32_16x16x32_bf16 v[116:119], v[176:179], v[184:187], v[116:119]
	v_mfma_f32_16x16x32_bf16 v[104:107], v[168:171], v[192:195], v[104:107]
	v_mfma_f32_16x16x32_bf16 v[100:103], v[176:179], v[192:195], v[100:103]
	v_mfma_f32_16x16x32_bf16 v[86:89], v[168:171], v[208:211], v[86:89]
	v_mfma_f32_16x16x32_bf16 v[82:85], v[176:179], v[208:211], v[82:85]
	v_mfma_f32_16x16x32_bf16 v[70:73], v[168:171], v[216:219], v[70:73]
	v_mfma_f32_16x16x32_bf16 v[66:69], v[176:179], v[216:219], v[66:69]
	v_mfma_f32_16x16x32_bf16 v[120:123], v[172:175], v[188:191], v[120:123]
	v_mfma_f32_16x16x32_bf16 v[116:119], v[180:183], v[188:191], v[116:119]
	v_mfma_f32_16x16x32_bf16 v[104:107], v[172:175], v[196:199], v[104:107]
	v_mfma_f32_16x16x32_bf16 v[100:103], v[180:183], v[196:199], v[100:103]
	v_mfma_f32_16x16x32_bf16 v[86:89], v[172:175], v[212:215], v[86:89]
	v_mfma_f32_16x16x32_bf16 v[82:85], v[180:183], v[212:215], v[82:85]
	v_mfma_f32_16x16x32_bf16 v[70:73], v[172:175], v[220:223], v[70:73]
	v_mfma_f32_16x16x32_bf16 v[66:69], v[180:183], v[220:223], v[66:69]
	s_setprio 0
	s_barrier
; #define PG8_STAGE_A(bufoff, h, ptr, nsel) do { if constexpr (Sched::GATHER) { if (nsel) PG8_STAGE_X(bufoff, ptr, vAn[h], PG8_A_AUX); else PG8_STAGE_X(bufoff, ptr, vAc[h], PG8_A_AUX); } \
;         else PG8_STAGE_X(bufoff, (ptr) + (h) * hstep, voffA, PG8_A_AUX); } while (0)
; #define PG8_STAGE(bufoff, gbase, voff) PG8_STAGE_X(bufoff, gbase, voff, PG8_B_AUX)
; #define PG8_LDA(dst, b, h) do { _Pragma("unroll") for (int m = 0; m < 4; ++m) _Pragma("unroll") for (int k = 0; k < 2; ++k) dst[m][k] = *(const PG8_LAS bf16x8*)(lds + PG8_SA(b, h) + aoff + m * 2048 + k * 1024); } while (0)
; #define PG8_MMA(ai, bj, At, Bt) do { __builtin_amdgcn_s_setprio(1); _Pragma("unroll") for (int m = 0; m < 4; ++m) _Pragma("unroll") for (int n = 0; n < 2; ++n) _Pragma("unroll") for (int k = 0; k < 2; ++k) \
;         acc[ai][bj][m][n] = __builtin_amdgcn_mfma_f32_16x16x32_bf16(Bt[n][k], At[m][k], acc[ai][bj][m][n], 0, 0, 0); __builtin_amdgcn_s_setprio(0); } while (0)
; #define PG8_WAIT_V(n) asm volatile("s_waitcnt vmcnt(" #n ")" ::: "memory")
; #define PG8_WAIT_L(n) asm volatile("s_waitcnt lgkmcnt(" #n ")" ::: "memory")
; #define PG8_BAR __builtin_amdgcn_s_barrier()
; #define PG8_SCHED __builtin_amdgcn_sched_barrier(0)
; template <class Epi, class Sched, bool ALIGN_EPI = false, bool SP2 = false>
; __device__ __forceinline__ void gemm_phase(PG8_LAS unsigned char* lds, const Gemm g, const Sched& S, const Epi& E) {
;     ...
;             PG8_LDA(At, 1, 1); PG8_STAGE(PG8_SB(1, 0), b3, voffB); PG8_STAGE(PG8_SB(1, 1), b3 + hstep, voffB); PG8_STAGE_A(PG8_SA(1, 0), 0, a3, last);
;             PG8_WAIT_V(8); PG8_WAIT_L(0); PG8_BAR; PG8_MMA(1, 0, At, B0); PG8_MMA(1, 1, At, B1); PG8_BAR; PG8_SCHED;
;     ...
;         }
;         if constexpr (ALIGN_EPI) { if (wr == 0) PG8_BAR; }
	s_mov_b32 m0, s57
	v_lshl_add_u64 v[224:225], v[224:225], 0, s[54:55]
	s_add_u32 s24, s24, 0x40080
	ds_read_b128 v[184:187], v154 offset:49152
	ds_read_b128 v[188:191], v154 offset:50176
	ds_read_b128 v[192:195], v154 offset:51200
	ds_read_b128 v[196:199], v154 offset:52224
	ds_read_b128 v[208:211], v154 offset:53248
	ds_read_b128 v[212:215], v154 offset:54272
	ds_read_b128 v[216:219], v154 offset:55296
	ds_read_b128 v[220:223], v154 offset:56320
	global_load_lds_dwordx4 v[224:225], off
	v_lshl_add_u64 v[224:225], v[226:227], 0, s[54:55]
	s_mov_b32 m0, s58
	s_addc_u32 s25, s25, 0
	global_load_lds_dwordx4 v[224:225], off
	v_lshl_add_u64 v[224:225], s[24:25], 0, v[140:141]
	s_mov_b32 m0, s68
	s_nop 0
	global_load_lds_dwordx4 v[224:225], off
	v_lshl_add_u64 v[224:225], s[24:25], 0, v[136:137]
	s_mov_b32 m0, s69
	s_nop 0
	global_load_lds_dwordx4 v[224:225], off
	v_lshl_add_u64 v[224:225], v[228:229], 0, s[54:55]
	s_mov_b32 m0, s59
	s_nop 0
	global_load_lds_dwordx4 v[224:225], off
	v_lshl_add_u64 v[224:225], v[230:231], 0, s[54:55]
	s_mov_b32 m0, s61
	s_nop 0
	global_load_lds_dwordx4 v[224:225], off
	s_waitcnt vmcnt(8)
	s_waitcnt lgkmcnt(0)
	s_barrier
	s_setprio 1
	s_waitcnt lgkmcnt(0)
	v_mfma_f32_16x16x32_bf16 v[62:65], v[148:151], v[184:187], v[62:65]
	v_mfma_f32_16x16x32_bf16 v[58:61], v[160:163], v[184:187], v[58:61]
	v_mfma_f32_16x16x32_bf16 v[46:49], v[148:151], v[192:195], v[46:49]
	v_mfma_f32_16x16x32_bf16 v[42:45], v[160:163], v[192:195], v[42:45]
	v_mfma_f32_16x16x32_bf16 v[30:33], v[148:151], v[208:211], v[30:33]
	v_mfma_f32_16x16x32_bf16 v[26:29], v[160:163], v[208:211], v[26:29]
	v_mfma_f32_16x16x32_bf16 v[14:17], v[148:151], v[216:219], v[14:17]
	v_mfma_f32_16x16x32_bf16 v[10:13], v[160:163], v[216:219], v[10:13]
	v_mfma_f32_16x16x32_bf16 v[62:65], v[156:159], v[188:191], v[62:65]
	v_mfma_f32_16x16x32_bf16 v[58:61], v[164:167], v[188:191], v[58:61]
	v_mfma_f32_16x16x32_bf16 v[46:49], v[156:159], v[196:199], v[46:49]
	v_mfma_f32_16x16x32_bf16 v[42:45], v[164:167], v[196:199], v[42:45]
	v_mfma_f32_16x16x32_bf16 v[30:33], v[156:159], v[212:215], v[30:33]
	v_mfma_f32_16x16x32_bf16 v[26:29], v[164:167], v[212:215], v[26:29]
	v_mfma_f32_16x16x32_bf16 v[14:17], v[156:159], v[220:223], v[14:17]
	v_mfma_f32_16x16x32_bf16 v[10:13], v[164:167], v[220:223], v[10:13]
	s_setprio 0
	s_setprio 1
	v_mfma_f32_16x16x32_bf16 v[54:57], v[168:171], v[184:187], v[54:57]
	v_mfma_f32_16x16x32_bf16 v[50:53], v[176:179], v[184:187], v[50:53]
	v_mfma_f32_16x16x32_bf16 v[38:41], v[168:171], v[192:195], v[38:41]
	v_mfma_f32_16x16x32_bf16 v[34:37], v[176:179], v[192:195], v[34:37]
	v_mfma_f32_16x16x32_bf16 v[22:25], v[168:171], v[208:211], v[22:25]
	v_mfma_f32_16x16x32_bf16 v[18:21], v[176:179], v[208:211], v[18:21]
	v_mfma_f32_16x16x32_bf16 v[6:9], v[168:171], v[216:219], v[6:9]
	v_mfma_f32_16x16x32_bf16 v[2:5], v[176:179], v[216:219], v[2:5]
	v_mfma_f32_16x16x32_bf16 v[54:57], v[172:175], v[188:191], v[54:57]
	v_mfma_f32_16x16x32_bf16 v[50:53], v[180:183], v[188:191], v[50:53]
	v_mfma_f32_16x16x32_bf16 v[38:41], v[172:175], v[196:199], v[38:41]
	v_mfma_f32_16x16x32_bf16 v[34:37], v[180:183], v[196:199], v[34:37]
	v_mfma_f32_16x16x32_bf16 v[22:25], v[172:175], v[212:215], v[22:25]
	v_mfma_f32_16x16x32_bf16 v[18:21], v[180:183], v[212:215], v[18:21]
	v_mfma_f32_16x16x32_bf16 v[6:9], v[172:175], v[220:223], v[6:9]
	v_mfma_f32_16x16x32_bf16 v[2:5], v[180:183], v[220:223], v[2:5]
	s_setprio 0
	s_barrier
	s_add_i32 s64, s64, 2
	s_add_u32 s22, s22, 0x100
	s_addc_u32 s23, s23, 0
	s_add_u32 s52, s52, 0x100
	s_addc_u32 s60, s60, 0
	s_cmp_gt_u32 s64, 13
	s_cbranch_scc0 .LBB13_844
	s_and_b64 vcc, exec, s[10:11]
	s_mov_b32 s64, 0x18000
	s_cbranch_vccz .LBB13_847
	s_barrier

; #define PG8_LAS __attribute__((address_space(3)))
; #define PG8_STAGE_A(bufoff, h, ptr, nsel) do { if constexpr (Sched::GATHER) { if (nsel) PG8_STAGE_X(bufoff, ptr, vAn[h], PG8_A_AUX); else PG8_STAGE_X(bufoff, ptr, vAc[h], PG8_A_AUX); } \
;         else PG8_STAGE_X(bufoff, (ptr) + (h) * hstep, voffA, PG8_A_AUX); } while (0)
; #define PG8_STAGE(bufoff, gbase, voff) PG8_STAGE_X(bufoff, gbase, voff, PG8_B_AUX)
; #define PG8_LDA(dst, b, h) do { _Pragma("unroll") for (int m = 0; m < 4; ++m) _Pragma("unroll") for (int k = 0; k < 2; ++k) dst[m][k] = *(const PG8_LAS bf16x8*)(lds + PG8_SA(b, h) + aoff + m * 2048 + k * 1024); } while (0)
; #define PG8_LDB(dst, b, h) do { _Pragma("unroll") for (int n = 0; n < 2; ++n) _Pragma("unroll") for (int k = 0; k < 2; ++k) dst[n][k] = *(const PG8_LAS bf16x8*)(lds + PG8_SB(b, h) + boff + n * 2048 + k * 1024); } while (0)
; #define PG8_WAIT_V(n) asm volatile("s_waitcnt vmcnt(" #n ")" ::: "memory")
; #define PG8_WAIT_L(n) asm volatile("s_waitcnt lgkmcnt(" #n ")" ::: "memory")
; template <class Epi, class Sched, bool ALIGN_EPI = false, bool SP2 = false>
; __device__ __forceinline__ void gemm_phase(PG8_LAS unsigned char* lds, const Gemm g, const Sched& S, const Epi& E) {
;     ...
;         for (int t = 0; t < nt; t += 2) {
;             const bool last = (t == nt - 2);
;             const char* a1 = cA + (size_t)(t + 1) * kstep;
;             const char* a2 = last ? nA : cA + (size_t)(t + 2) * kstep; const char* b2 = last ? nB : cB + (size_t)(t + 2) * kstep;
;             const char* a3 = a2 + kstep; const char* b3 = b2 + kstep;
;             if (last && has_next) S.a_ready(nxt);
;             if constexpr (Sched::GATHER) { if (last) { const u32x4 pv_ = *(const PG8_LAS u32x4*)(lds + STAGE_BYTES + tid * 16); vAn[0][0] = pv_.x; vAn[0][1] = pv_.y; vAn[1][0] = pv_.z; vAn[1][1] = pv_.w; } }
;             if constexpr (SP2) {
;             PG8_LDB(B0, 0, 0); PG8_LDB(B1, 0, 1); PG8_SCHED; PG8_LDA(At, 0, 0); PG8_STAGE_A(PG8_SA(1, 1), 1, a1, false);
;             PG8_WAIT_V(8); PG8_WAIT_L(0); PG8_BAR; PG8_MMA(0, 0, At, B0); PG8_MMA(0, 1, At, B1); PG8_BAR; PG8_SCHED;
;             PG8_LDA(At, 0, 1); PG8_STAGE(PG8_SB(0, 0), b2, voffB); PG8_STAGE(PG8_SB(0, 1), b2 + hstep, voffB); PG8_STAGE_A(PG8_SA(0, 0), 0, a2, last);
;             PG8_WAIT_V(8); PG8_WAIT_L(0); PG8_BAR; PG8_MMA(1, 0, At, B0); PG8_MMA(1, 1, At, B1); PG8_BAR; PG8_SCHED;
.LBB13_926:
	v_add_u32_e32 v90, s43, v184
	v_add_u32_e32 v178, s46, v184
	ds_read_b128 v[74:77], v90
	ds_read_b128 v[78:81], v90 offset:1024
	ds_read_b128 v[82:85], v90 offset:2048
	ds_read_b128 v[90:93], v90 offset:3072
	ds_read_b128 v[148:151], v178
	ds_read_b128 v[152:155], v178 offset:1024
	ds_read_b128 v[174:177], v178 offset:2048
	ds_read_b128 v[178:181], v178 offset:3072
	s_add_u32 s34, s30, 0xfffc0080
	s_addc_u32 s35, s31, -1
	s_cmp_eq_u32 s86, 12
	s_cselect_b32 s37, s7, s35
	s_cselect_b32 s36, s23, s34
	s_cselect_b32 s35, s21, s76
	s_cselect_b32 s34, s29, s73
	v_lshl_add_u64 v[182:183], s[30:31], 0, v[170:171]
	s_add_i32 m0, s49, 0xc000
	ds_read_b128 v[188:191], v186
	ds_read_b128 v[192:195], v186 offset:1024
	ds_read_b128 v[196:199], v186 offset:2048
	ds_read_b128 v[208:211], v186 offset:3072
	ds_read_b128 v[212:215], v186 offset:4096
	ds_read_b128 v[216:219], v186 offset:5120
	ds_read_b128 v[220:223], v186 offset:6144
	ds_read_b128 v[224:227], v186 offset:7168
	global_load_lds_dwordx4 v[182:183], off
	v_lshl_add_u64 v[182:183], s[30:31], 0, v[172:173]
	s_add_i32 m0, s49, 0xe000
	s_nop 0
	global_load_lds_dwordx4 v[182:183], off
	s_nop 0
	s_waitcnt vmcnt(8)
	s_waitcnt lgkmcnt(0)
	s_barrier
	s_setprio 1
	s_waitcnt lgkmcnt(0)
	v_mfma_f32_16x16x32_bf16 v[144:147], v[74:77], v[188:191], v[144:147]
	v_mfma_f32_16x16x32_bf16 v[140:143], v[82:85], v[188:191], v[140:143]
	v_mfma_f32_16x16x32_bf16 v[128:131], v[74:77], v[196:199], v[128:131]
	v_mfma_f32_16x16x32_bf16 v[124:127], v[82:85], v[196:199], v[124:127]
	v_mfma_f32_16x16x32_bf16 v[112:115], v[74:77], v[212:215], v[112:115]
	v_mfma_f32_16x16x32_bf16 v[108:111], v[82:85], v[212:215], v[108:111]
	v_mfma_f32_16x16x32_bf16 v[94:97], v[74:77], v[220:223], v[94:97]
	v_mfma_f32_16x16x32_bf16 v[86:89], v[82:85], v[220:223], v[86:89]
	v_mfma_f32_16x16x32_bf16 v[144:147], v[78:81], v[192:195], v[144:147]
	v_mfma_f32_16x16x32_bf16 v[140:143], v[90:93], v[192:195], v[140:143]
	v_mfma_f32_16x16x32_bf16 v[128:131], v[78:81], v[208:211], v[128:131]
	v_mfma_f32_16x16x32_bf16 v[124:127], v[90:93], v[208:211], v[124:127]
	v_mfma_f32_16x16x32_bf16 v[112:115], v[78:81], v[216:219], v[112:115]
	v_mfma_f32_16x16x32_bf16 v[108:111], v[90:93], v[216:219], v[108:111]
	v_mfma_f32_16x16x32_bf16 v[94:97], v[78:81], v[224:227], v[94:97]
	v_mfma_f32_16x16x32_bf16 v[86:89], v[90:93], v[224:227], v[86:89]
	s_setprio 0
	s_setprio 1
	v_mfma_f32_16x16x32_bf16 v[136:139], v[148:151], v[188:191], v[136:139]
	v_mfma_f32_16x16x32_bf16 v[132:135], v[174:177], v[188:191], v[132:135]
	v_mfma_f32_16x16x32_bf16 v[120:123], v[148:151], v[196:199], v[120:123]
	v_mfma_f32_16x16x32_bf16 v[116:119], v[174:177], v[196:199], v[116:119]
	v_mfma_f32_16x16x32_bf16 v[104:107], v[148:151], v[212:215], v[104:107]
	v_mfma_f32_16x16x32_bf16 v[100:103], v[174:177], v[212:215], v[100:103]
	v_mfma_f32_16x16x32_bf16 v[70:73], v[148:151], v[220:223], v[70:73]
	v_mfma_f32_16x16x32_bf16 v[66:69], v[174:177], v[220:223], v[66:69]
	v_mfma_f32_16x16x32_bf16 v[136:139], v[152:155], v[192:195], v[136:139]
	v_mfma_f32_16x16x32_bf16 v[132:135], v[178:181], v[192:195], v[132:135]
	v_mfma_f32_16x16x32_bf16 v[120:123], v[152:155], v[208:211], v[120:123]
	v_mfma_f32_16x16x32_bf16 v[116:119], v[178:181], v[208:211], v[116:119]
	v_mfma_f32_16x16x32_bf16 v[104:107], v[152:155], v[216:219], v[104:107]
	v_mfma_f32_16x16x32_bf16 v[100:103], v[178:181], v[216:219], v[100:103]
	v_mfma_f32_16x16x32_bf16 v[70:73], v[152:155], v[224:227], v[70:73]
	v_mfma_f32_16x16x32_bf16 v[66:69], v[178:181], v[224:227], v[66:69]
	s_setprio 0
	s_barrier
	s_mov_b32 m0, s44
	v_lshl_add_u64 v[182:183], s[34:35], 0, v[162:163]
	s_add_u32 s88, s34, 0x40000
	ds_read_b128 v[188:191], v186 offset:16384
	ds_read_b128 v[192:195], v186 offset:17408
	ds_read_b128 v[196:199], v186 offset:18432
	ds_read_b128 v[208:211], v186 offset:19456
	ds_read_b128 v[212:215], v186 offset:20480
	ds_read_b128 v[216:219], v186 offset:21504
	ds_read_b128 v[220:223], v186 offset:22528
	ds_read_b128 v[224:227], v186 offset:23552
	global_load_lds_dwordx4 v[182:183], off
	v_lshl_add_u64 v[228:229], s[34:35], 0, v[166:167]
	s_mov_b32 m0, s45
	s_addc_u32 s89, s35, 0
	global_load_lds_dwordx4 v[228:229], off
	v_lshl_add_u64 v[230:231], s[88:89], 0, v[162:163]
	s_mov_b32 m0, s47
	v_lshl_add_u64 v[232:233], s[36:37], 0, v[164:165]
	global_load_lds_dwordx4 v[230:231], off
	v_lshl_add_u64 v[230:231], s[88:89], 0, v[166:167]
	s_mov_b32 m0, s48
	s_nop 0
	global_load_lds_dwordx4 v[230:231], off
	v_lshl_add_u64 v[230:231], s[36:37], 0, v[160:161]
	s_mov_b32 m0, s49
	s_nop 0
	global_load_lds_dwordx4 v[230:231], off
	s_mov_b32 m0, s50
	s_nop 0
	global_load_lds_dwordx4 v[232:233], off
	s_nop 0
	s_waitcnt vmcnt(8)
	s_waitcnt lgkmcnt(0)
	s_barrier
; #define PG8_STAGE_A(bufoff, h, ptr, nsel) do { if constexpr (Sched::GATHER) { if (nsel) PG8_STAGE_X(bufoff, ptr, vAn[h], PG8_A_AUX); else PG8_STAGE_X(bufoff, ptr, vAc[h], PG8_A_AUX); } \
;         else PG8_STAGE_X(bufoff, (ptr) + (h) * hstep, voffA, PG8_A_AUX); } while (0)
; #define PG8_STAGE(bufoff, gbase, voff) PG8_STAGE_X(bufoff, gbase, voff, PG8_B_AUX)
; #define PG8_LDA(dst, b, h) do { _Pragma("unroll") for (int m = 0; m < 4; ++m) _Pragma("unroll") for (int k = 0; k < 2; ++k) dst[m][k] = *(const PG8_LAS bf16x8*)(lds + PG8_SA(b, h) + aoff + m * 2048 + k * 1024); } while (0)
; #define PG8_LDB(dst, b, h) do { _Pragma("unroll") for (int n = 0; n < 2; ++n) _Pragma("unroll") for (int k = 0; k < 2; ++k) dst[n][k] = *(const PG8_LAS bf16x8*)(lds + PG8_SB(b, h) + boff + n * 2048 + k * 1024); } while (0)
; #define PG8_MMA(ai, bj, At, Bt) do { __builtin_amdgcn_s_setprio(1); _Pragma("unroll") for (int m = 0; m < 4; ++m) _Pragma("unroll") for (int n = 0; n < 2; ++n) _Pragma("unroll") for (int k = 0; k < 2; ++k) \
;         acc[ai][bj][m][n] = __builtin_amdgcn_mfma_f32_16x16x32_bf16(Bt[n][k], At[m][k], acc[ai][bj][m][n], 0, 0, 0); __builtin_amdgcn_s_setprio(0); } while (0)
; #define PG8_WAIT_V(n) asm volatile("s_waitcnt vmcnt(" #n ")" ::: "memory")
; #define PG8_WAIT_L(n) asm volatile("s_waitcnt lgkmcnt(" #n ")" ::: "memory")
; #define PG8_BAR __builtin_amdgcn_s_barrier()
; #define PG8_SCHED __builtin_amdgcn_sched_barrier(0)
; template <class Epi, class Sched, bool ALIGN_EPI = false, bool SP2 = false>
; __device__ __forceinline__ void gemm_phase(PG8_LAS unsigned char* lds, const Gemm g, const Sched& S, const Epi& E) {
;     ...
;             PG8_WAIT_V(8); PG8_WAIT_L(0); PG8_BAR; PG8_MMA(1, 0, At, B0); PG8_MMA(1, 1, At, B1); PG8_BAR; PG8_SCHED;
;             PG8_LDB(B0, 1, 0); PG8_LDB(B1, 1, 1); PG8_SCHED; PG8_LDA(At, 1, 0); PG8_STAGE_A(PG8_SA(0, 1), 1, a2, last);
;             PG8_WAIT_V(8); PG8_WAIT_L(0); PG8_BAR; PG8_MMA(0, 0, At, B0); PG8_MMA(0, 1, At, B1); PG8_BAR; PG8_SCHED;
;             PG8_LDA(At, 1, 1); PG8_STAGE(PG8_SB(1, 0), b3, voffB); PG8_STAGE(PG8_SB(1, 1), b3 + hstep, voffB); PG8_STAGE_A(PG8_SA(1, 0), 0, a3, last);
	s_setprio 1
	s_waitcnt lgkmcnt(0)
	v_mfma_f32_16x16x32_bf16 v[62:65], v[74:77], v[188:191], v[62:65]
	v_mfma_f32_16x16x32_bf16 v[58:61], v[82:85], v[188:191], v[58:61]
	v_mfma_f32_16x16x32_bf16 v[46:49], v[74:77], v[196:199], v[46:49]
	v_mfma_f32_16x16x32_bf16 v[42:45], v[82:85], v[196:199], v[42:45]
	v_mfma_f32_16x16x32_bf16 v[30:33], v[74:77], v[212:215], v[30:33]
	v_mfma_f32_16x16x32_bf16 v[26:29], v[82:85], v[212:215], v[26:29]
	v_mfma_f32_16x16x32_bf16 v[14:17], v[74:77], v[220:223], v[14:17]
	v_mfma_f32_16x16x32_bf16 v[10:13], v[82:85], v[220:223], v[10:13]
	v_mfma_f32_16x16x32_bf16 v[62:65], v[78:81], v[192:195], v[62:65]
	v_mfma_f32_16x16x32_bf16 v[58:61], v[90:93], v[192:195], v[58:61]
	v_mfma_f32_16x16x32_bf16 v[46:49], v[78:81], v[208:211], v[46:49]
	v_mfma_f32_16x16x32_bf16 v[42:45], v[90:93], v[208:211], v[42:45]
	v_mfma_f32_16x16x32_bf16 v[30:33], v[78:81], v[216:219], v[30:33]
	v_mfma_f32_16x16x32_bf16 v[26:29], v[90:93], v[216:219], v[26:29]
	v_mfma_f32_16x16x32_bf16 v[14:17], v[78:81], v[224:227], v[14:17]
	v_mfma_f32_16x16x32_bf16 v[10:13], v[90:93], v[224:227], v[10:13]
	s_setprio 0
	s_setprio 1
	v_mfma_f32_16x16x32_bf16 v[54:57], v[148:151], v[188:191], v[54:57]
	v_mfma_f32_16x16x32_bf16 v[50:53], v[174:177], v[188:191], v[50:53]
	v_mfma_f32_16x16x32_bf16 v[38:41], v[148:151], v[196:199], v[38:41]
	v_mfma_f32_16x16x32_bf16 v[34:37], v[174:177], v[196:199], v[34:37]
	v_mfma_f32_16x16x32_bf16 v[22:25], v[148:151], v[212:215], v[22:25]
	v_mfma_f32_16x16x32_bf16 v[18:21], v[174:177], v[212:215], v[18:21]
	v_mfma_f32_16x16x32_bf16 v[6:9], v[148:151], v[220:223], v[6:9]
	v_mfma_f32_16x16x32_bf16 v[2:5], v[174:177], v[220:223], v[2:5]
	v_mfma_f32_16x16x32_bf16 v[54:57], v[152:155], v[192:195], v[54:57]
	v_mfma_f32_16x16x32_bf16 v[50:53], v[178:181], v[192:195], v[50:53]
	v_mfma_f32_16x16x32_bf16 v[38:41], v[152:155], v[208:211], v[38:41]
	v_mfma_f32_16x16x32_bf16 v[34:37], v[178:181], v[208:211], v[34:37]
	v_mfma_f32_16x16x32_bf16 v[22:25], v[152:155], v[216:219], v[22:25]
	v_mfma_f32_16x16x32_bf16 v[18:21], v[178:181], v[216:219], v[18:21]
	v_mfma_f32_16x16x32_bf16 v[6:9], v[152:155], v[224:227], v[6:9]
	v_mfma_f32_16x16x32_bf16 v[2:5], v[178:181], v[224:227], v[2:5]
	s_setprio 0
	s_barrier
	v_add_u32_e32 v90, s53, v184
	v_add_u32_e32 v178, s60, v184
	ds_read_b128 v[74:77], v90
	ds_read_b128 v[78:81], v90 offset:1024
	ds_read_b128 v[82:85], v90 offset:2048
	ds_read_b128 v[90:93], v90 offset:3072
	ds_read_b128 v[148:151], v178
	ds_read_b128 v[152:155], v178 offset:1024
	ds_read_b128 v[174:177], v178 offset:2048
	ds_read_b128 v[178:181], v178 offset:3072
	s_add_u32 s36, s36, 0x40000
	s_addc_u32 s37, s37, 0
	s_mov_b32 m0, s51
	v_lshl_add_u64 v[242:243], s[36:37], 0, v[160:161]
	ds_read_b128 v[188:191], v186 offset:32768
	ds_read_b128 v[192:195], v186 offset:33792
	ds_read_b128 v[196:199], v186 offset:34816
	ds_read_b128 v[208:211], v186 offset:35840
	ds_read_b128 v[212:215], v186 offset:36864
	ds_read_b128 v[216:219], v186 offset:37888
	ds_read_b128 v[220:223], v186 offset:38912
	ds_read_b128 v[224:227], v186 offset:39936
	global_load_lds_dwordx4 v[242:243], off
	v_lshl_add_u64 v[242:243], s[36:37], 0, v[164:165]
	s_mov_b32 m0, s52
	s_nop 0
	global_load_lds_dwordx4 v[242:243], off
	s_nop 0
	s_waitcnt vmcnt(8)
	s_waitcnt lgkmcnt(0)
	s_barrier
	s_setprio 1
	s_waitcnt lgkmcnt(0)
	v_mfma_f32_16x16x32_bf16 v[144:147], v[74:77], v[188:191], v[144:147]
	v_mfma_f32_16x16x32_bf16 v[140:143], v[82:85], v[188:191], v[140:143]
	v_mfma_f32_16x16x32_bf16 v[128:131], v[74:77], v[196:199], v[128:131]
	v_mfma_f32_16x16x32_bf16 v[124:127], v[82:85], v[196:199], v[124:127]
	v_mfma_f32_16x16x32_bf16 v[112:115], v[74:77], v[212:215], v[112:115]
	v_mfma_f32_16x16x32_bf16 v[108:111], v[82:85], v[212:215], v[108:111]
	v_mfma_f32_16x16x32_bf16 v[94:97], v[74:77], v[220:223], v[94:97]
	v_mfma_f32_16x16x32_bf16 v[86:89], v[82:85], v[220:223], v[86:89]
	v_mfma_f32_16x16x32_bf16 v[144:147], v[78:81], v[192:195], v[144:147]
	v_mfma_f32_16x16x32_bf16 v[140:143], v[90:93], v[192:195], v[140:143]
	v_mfma_f32_16x16x32_bf16 v[128:131], v[78:81], v[208:211], v[128:131]
	v_mfma_f32_16x16x32_bf16 v[124:127], v[90:93], v[208:211], v[124:127]
	v_mfma_f32_16x16x32_bf16 v[112:115], v[78:81], v[216:219], v[112:115]
	v_mfma_f32_16x16x32_bf16 v[108:111], v[90:93], v[216:219], v[108:111]
	v_mfma_f32_16x16x32_bf16 v[94:97], v[78:81], v[224:227], v[94:97]
	v_mfma_f32_16x16x32_bf16 v[86:89], v[90:93], v[224:227], v[86:89]
	s_setprio 0
	s_setprio 1
	v_mfma_f32_16x16x32_bf16 v[136:139], v[148:151], v[188:191], v[136:139]
	v_mfma_f32_16x16x32_bf16 v[132:135], v[174:177], v[188:191], v[132:135]
	v_mfma_f32_16x16x32_bf16 v[120:123], v[148:151], v[196:199], v[120:123]
	v_mfma_f32_16x16x32_bf16 v[116:119], v[174:177], v[196:199], v[116:119]
	v_mfma_f32_16x16x32_bf16 v[104:107], v[148:151], v[212:215], v[104:107]
	v_mfma_f32_16x16x32_bf16 v[100:103], v[174:177], v[212:215], v[100:103]
	v_mfma_f32_16x16x32_bf16 v[70:73], v[148:151], v[220:223], v[70:73]
	v_mfma_f32_16x16x32_bf16 v[66:69], v[174:177], v[220:223], v[66:69]
	v_mfma_f32_16x16x32_bf16 v[136:139], v[152:155], v[192:195], v[136:139]
	v_mfma_f32_16x16x32_bf16 v[132:135], v[178:181], v[192:195], v[132:135]
	v_mfma_f32_16x16x32_bf16 v[120:123], v[152:155], v[208:211], v[120:123]
	v_mfma_f32_16x16x32_bf16 v[116:119], v[178:181], v[208:211], v[116:119]
	v_mfma_f32_16x16x32_bf16 v[104:107], v[152:155], v[216:219], v[104:107]
	v_mfma_f32_16x16x32_bf16 v[100:103], v[178:181], v[216:219], v[100:103]
	v_mfma_f32_16x16x32_bf16 v[70:73], v[152:155], v[224:227], v[70:73]
	v_mfma_f32_16x16x32_bf16 v[66:69], v[178:181], v[224:227], v[66:69]
	s_setprio 0
	s_barrier
; #define PG8_STAGE_A(bufoff, h, ptr, nsel) do { if constexpr (Sched::GATHER) { if (nsel) PG8_STAGE_X(bufoff, ptr, vAn[h], PG8_A_AUX); else PG8_STAGE_X(bufoff, ptr, vAc[h], PG8_A_AUX); } \
;         else PG8_STAGE_X(bufoff, (ptr) + (h) * hstep, voffA, PG8_A_AUX); } while (0)
; #define PG8_STAGE(bufoff, gbase, voff) PG8_STAGE_X(bufoff, gbase, voff, PG8_B_AUX)
; #define PG8_LDA(dst, b, h) do { _Pragma("unroll") for (int m = 0; m < 4; ++m) _Pragma("unroll") for (int k = 0; k < 2; ++k) dst[m][k] = *(const PG8_LAS bf16x8*)(lds + PG8_SA(b, h) + aoff + m * 2048 + k * 1024); } while (0)
; #define PG8_MMA(ai, bj, At, Bt) do { __builtin_amdgcn_s_setprio(1); _Pragma("unroll") for (int m = 0; m < 4; ++m) _Pragma("unroll") for (int n = 0; n < 2; ++n) _Pragma("unroll") for (int k = 0; k < 2; ++k) \
;         acc[ai][bj][m][n] = __builtin_amdgcn_mfma_f32_16x16x32_bf16(Bt[n][k], At[m][k], acc[ai][bj][m][n], 0, 0, 0); __builtin_amdgcn_s_setprio(0); } while (0)
; #define PG8_WAIT_V(n) asm volatile("s_waitcnt vmcnt(" #n ")" ::: "memory")
; #define PG8_WAIT_L(n) asm volatile("s_waitcnt lgkmcnt(" #n ")" ::: "memory")
; #define PG8_BAR __builtin_amdgcn_s_barrier()
; #define PG8_SCHED __builtin_amdgcn_sched_barrier(0)
; template <class Epi, class Sched, bool ALIGN_EPI = false, bool SP2 = false>
; __device__ __forceinline__ void gemm_phase(PG8_LAS unsigned char* lds, const Gemm g, const Sched& S, const Epi& E) {
;     ...
;             PG8_LDA(At, 1, 1); PG8_STAGE(PG8_SB(1, 0), b3, voffB); PG8_STAGE(PG8_SB(1, 1), b3 + hstep, voffB); PG8_STAGE_A(PG8_SA(1, 0), 0, a3, last);
;             PG8_WAIT_V(8); PG8_WAIT_L(0); PG8_BAR; PG8_MMA(1, 0, At, B0); PG8_MMA(1, 1, At, B1); PG8_BAR; PG8_SCHED;
	s_mov_b32 m0, s56
	v_lshl_add_u64 v[182:183], v[182:183], 0, s[54:55]
	s_add_u32 s34, s34, 0x40080
	ds_read_b128 v[188:191], v186 offset:49152
	ds_read_b128 v[192:195], v186 offset:50176
	ds_read_b128 v[196:199], v186 offset:51200
	ds_read_b128 v[208:211], v186 offset:52224
	ds_read_b128 v[212:215], v186 offset:53248
	ds_read_b128 v[216:219], v186 offset:54272
	ds_read_b128 v[220:223], v186 offset:55296
	ds_read_b128 v[224:227], v186 offset:56320
	global_load_lds_dwordx4 v[182:183], off
	v_lshl_add_u64 v[182:183], v[228:229], 0, s[54:55]
	s_mov_b32 m0, s57
	s_addc_u32 s35, s35, 0
	global_load_lds_dwordx4 v[182:183], off
	v_lshl_add_u64 v[182:183], s[34:35], 0, v[162:163]
	s_mov_b32 m0, s61
	s_nop 0
	global_load_lds_dwordx4 v[182:183], off
	v_lshl_add_u64 v[182:183], s[34:35], 0, v[166:167]
	s_mov_b32 m0, s64
	s_nop 0
	global_load_lds_dwordx4 v[182:183], off
	v_lshl_add_u64 v[182:183], v[230:231], 0, s[54:55]
	s_mov_b32 m0, s58
	s_nop 0
	global_load_lds_dwordx4 v[182:183], off
	v_lshl_add_u64 v[182:183], v[232:233], 0, s[54:55]
	s_mov_b32 m0, s59
	s_nop 0
	global_load_lds_dwordx4 v[182:183], off
	s_waitcnt vmcnt(8)
	s_waitcnt lgkmcnt(0)
	s_barrier
	s_setprio 1
	s_waitcnt lgkmcnt(0)
	v_mfma_f32_16x16x32_bf16 v[62:65], v[74:77], v[188:191], v[62:65]
	v_mfma_f32_16x16x32_bf16 v[58:61], v[82:85], v[188:191], v[58:61]
	v_mfma_f32_16x16x32_bf16 v[46:49], v[74:77], v[196:199], v[46:49]
	v_mfma_f32_16x16x32_bf16 v[42:45], v[82:85], v[196:199], v[42:45]
	v_mfma_f32_16x16x32_bf16 v[30:33], v[74:77], v[212:215], v[30:33]
	v_mfma_f32_16x16x32_bf16 v[26:29], v[82:85], v[212:215], v[26:29]
	v_mfma_f32_16x16x32_bf16 v[14:17], v[74:77], v[220:223], v[14:17]
	v_mfma_f32_16x16x32_bf16 v[10:13], v[82:85], v[220:223], v[10:13]
	v_mfma_f32_16x16x32_bf16 v[62:65], v[78:81], v[192:195], v[62:65]
	v_mfma_f32_16x16x32_bf16 v[58:61], v[90:93], v[192:195], v[58:61]
	v_mfma_f32_16x16x32_bf16 v[46:49], v[78:81], v[208:211], v[46:49]
	v_mfma_f32_16x16x32_bf16 v[42:45], v[90:93], v[208:211], v[42:45]
	v_mfma_f32_16x16x32_bf16 v[30:33], v[78:81], v[216:219], v[30:33]
	v_mfma_f32_16x16x32_bf16 v[26:29], v[90:93], v[216:219], v[26:29]
	v_mfma_f32_16x16x32_bf16 v[14:17], v[78:81], v[224:227], v[14:17]
	v_mfma_f32_16x16x32_bf16 v[10:13], v[90:93], v[224:227], v[10:13]
	s_setprio 0
	s_setprio 1
	v_mfma_f32_16x16x32_bf16 v[54:57], v[148:151], v[188:191], v[54:57]
	v_mfma_f32_16x16x32_bf16 v[50:53], v[174:177], v[188:191], v[50:53]
	v_mfma_f32_16x16x32_bf16 v[38:41], v[148:151], v[196:199], v[38:41]
	v_mfma_f32_16x16x32_bf16 v[34:37], v[174:177], v[196:199], v[34:37]
	v_mfma_f32_16x16x32_bf16 v[22:25], v[148:151], v[212:215], v[22:25]
	v_mfma_f32_16x16x32_bf16 v[18:21], v[174:177], v[212:215], v[18:21]
	v_mfma_f32_16x16x32_bf16 v[6:9], v[148:151], v[220:223], v[6:9]
	v_mfma_f32_16x16x32_bf16 v[2:5], v[174:177], v[220:223], v[2:5]
	v_mfma_f32_16x16x32_bf16 v[54:57], v[152:155], v[192:195], v[54:57]
	v_mfma_f32_16x16x32_bf16 v[50:53], v[178:181], v[192:195], v[50:53]
	v_mfma_f32_16x16x32_bf16 v[38:41], v[152:155], v[208:211], v[38:41]
	v_mfma_f32_16x16x32_bf16 v[34:37], v[178:181], v[208:211], v[34:37]
	v_mfma_f32_16x16x32_bf16 v[22:25], v[152:155], v[216:219], v[22:25]
	v_mfma_f32_16x16x32_bf16 v[18:21], v[178:181], v[216:219], v[18:21]
	v_mfma_f32_16x16x32_bf16 v[6:9], v[152:155], v[224:227], v[6:9]
	v_mfma_f32_16x16x32_bf16 v[2:5], v[178:181], v[224:227], v[2:5]
	s_setprio 0
	s_barrier
	s_add_i32 s86, s86, 2
	s_add_u32 s30, s30, 0x100
	s_addc_u32 s31, s31, 0
	s_add_u32 s73, s73, 0x100
	s_addc_u32 s76, s76, 0
	s_cmp_gt_u32 s86, 13
	s_cbranch_scc0 .LBB13_926
	s_and_b64 vcc, exec, s[16:17]
	s_cbranch_vccz .LBB13_929
	s_barrier

; #define PG8_LAS __attribute__((address_space(3)))
; #define PG8_STAGE_A(bufoff, h, ptr, nsel) do { if constexpr (Sched::GATHER) { if (nsel) PG8_STAGE_X(bufoff, ptr, vAn[h], PG8_A_AUX); else PG8_STAGE_X(bufoff, ptr, vAc[h], PG8_A_AUX); } \
;         else PG8_STAGE_X(bufoff, (ptr) + (h) * hstep, voffA, PG8_A_AUX); } while (0)
; #define PG8_STAGE(bufoff, gbase, voff) PG8_STAGE_X(bufoff, gbase, voff, PG8_B_AUX)
; #define PG8_LDA(dst, b, h) do { _Pragma("unroll") for (int m = 0; m < 4; ++m) _Pragma("unroll") for (int k = 0; k < 2; ++k) dst[m][k] = *(const PG8_LAS bf16x8*)(lds + PG8_SA(b, h) + aoff + m * 2048 + k * 1024); } while (0)
; #define PG8_LDB(dst, b, h) do { _Pragma("unroll") for (int n = 0; n < 2; ++n) _Pragma("unroll") for (int k = 0; k < 2; ++k) dst[n][k] = *(const PG8_LAS bf16x8*)(lds + PG8_SB(b, h) + boff + n * 2048 + k * 1024); } while (0)
; #define PG8_WAIT_V(n) asm volatile("s_waitcnt vmcnt(" #n ")" ::: "memory")
; #define PG8_WAIT_L(n) asm volatile("s_waitcnt lgkmcnt(" #n ")" ::: "memory")
; template <class Epi, class Sched, bool ALIGN_EPI = false, bool SP2 = false>
; __device__ __forceinline__ void gemm_phase(PG8_LAS unsigned char* lds, const Gemm g, const Sched& S, const Epi& E) {
;     ...
;         for (int t = 0; t < nt; t += 2) {
;             const bool last = (t == nt - 2);
;             const char* a1 = cA + (size_t)(t + 1) * kstep;
;             const char* a2 = last ? nA : cA + (size_t)(t + 2) * kstep; const char* b2 = last ? nB : cB + (size_t)(t + 2) * kstep;
;             const char* a3 = a2 + kstep; const char* b3 = b2 + kstep;
;             if (last && has_next) S.a_ready(nxt);
;             if constexpr (Sched::GATHER) { if (last) { const u32x4 pv_ = *(const PG8_LAS u32x4*)(lds + STAGE_BYTES + tid * 16); vAn[0][0] = pv_.x; vAn[0][1] = pv_.y; vAn[1][0] = pv_.z; vAn[1][1] = pv_.w; } }
;             if constexpr (SP2) {
;             PG8_LDB(B0, 0, 0); PG8_LDB(B1, 0, 1); PG8_SCHED; PG8_LDA(At, 0, 0); PG8_STAGE_A(PG8_SA(1, 1), 1, a1, false);
;             PG8_WAIT_V(8); PG8_WAIT_L(0); PG8_BAR; PG8_MMA(0, 0, At, B0); PG8_MMA(0, 1, At, B1); PG8_BAR; PG8_SCHED;
;             PG8_LDA(At, 0, 1); PG8_STAGE(PG8_SB(0, 0), b2, voffB); PG8_STAGE(PG8_SB(0, 1), b2 + hstep, voffB); PG8_STAGE_A(PG8_SA(0, 0), 0, a2, last);
;             PG8_WAIT_V(8); PG8_WAIT_L(0); PG8_BAR; PG8_MMA(1, 0, At, B0); PG8_MMA(1, 1, At, B1); PG8_BAR; PG8_SCHED;
.LBB13_1412:
	v_add_u32_e32 v158, s47, v99
	v_add_u32_e32 v174, s50, v99
	ds_read_b128 v[146:149], v158
	ds_read_b128 v[150:153], v158 offset:1024
	ds_read_b128 v[154:157], v158 offset:2048
	ds_read_b128 v[158:161], v158 offset:3072
	ds_read_b128 v[162:165], v174
	ds_read_b128 v[166:169], v174 offset:1024
	ds_read_b128 v[170:173], v174 offset:2048
	ds_read_b128 v[174:177], v174 offset:3072
	s_add_u32 s34, s30, 0xfffc0080
	s_addc_u32 s35, s31, -1
	s_cmp_eq_u32 s94, 12
	s_cselect_b32 s37, s21, s35
	s_cselect_b32 s36, s27, s34
	s_cselect_b32 s35, s19, s90
	s_cselect_b32 s34, s88, s89
	v_lshl_add_u64 v[198:199], s[30:31], 0, v[140:141]
	s_add_i32 m0, s58, 0xc000
	ds_read_b128 v[178:181], v145
	ds_read_b128 v[182:185], v145 offset:1024
	ds_read_b128 v[186:189], v145 offset:2048
	ds_read_b128 v[190:193], v145 offset:3072
	ds_read_b128 v[194:197], v145 offset:4096
	ds_read_b128 v[208:211], v145 offset:5120
	ds_read_b128 v[212:215], v145 offset:6144
	ds_read_b128 v[216:219], v145 offset:7168
	global_load_lds_dwordx4 v[198:199], off
	v_lshl_add_u64 v[198:199], s[30:31], 0, v[142:143]
	s_add_i32 m0, s58, 0xe000
	s_nop 0
	global_load_lds_dwordx4 v[198:199], off
	s_nop 0
	s_waitcnt vmcnt(8)
	s_waitcnt lgkmcnt(0)
	s_barrier
	s_setprio 1
	s_waitcnt lgkmcnt(0)
	v_mfma_f32_16x16x32_bf16 v[128:131], v[146:149], v[178:181], v[128:131]
	v_mfma_f32_16x16x32_bf16 v[120:123], v[154:157], v[178:181], v[120:123]
	v_mfma_f32_16x16x32_bf16 v[112:115], v[146:149], v[186:189], v[112:115]
	v_mfma_f32_16x16x32_bf16 v[104:107], v[154:157], v[186:189], v[104:107]
	v_mfma_f32_16x16x32_bf16 v[94:97], v[146:149], v[194:197], v[94:97]
	v_mfma_f32_16x16x32_bf16 v[86:89], v[154:157], v[194:197], v[86:89]
	v_mfma_f32_16x16x32_bf16 v[78:81], v[146:149], v[212:215], v[78:81]
	v_mfma_f32_16x16x32_bf16 v[70:73], v[154:157], v[212:215], v[70:73]
	v_mfma_f32_16x16x32_bf16 v[128:131], v[150:153], v[182:185], v[128:131]
	v_mfma_f32_16x16x32_bf16 v[120:123], v[158:161], v[182:185], v[120:123]
	v_mfma_f32_16x16x32_bf16 v[112:115], v[150:153], v[190:193], v[112:115]
	v_mfma_f32_16x16x32_bf16 v[104:107], v[158:161], v[190:193], v[104:107]
	v_mfma_f32_16x16x32_bf16 v[94:97], v[150:153], v[208:211], v[94:97]
	v_mfma_f32_16x16x32_bf16 v[86:89], v[158:161], v[208:211], v[86:89]
	v_mfma_f32_16x16x32_bf16 v[78:81], v[150:153], v[216:219], v[78:81]
	v_mfma_f32_16x16x32_bf16 v[70:73], v[158:161], v[216:219], v[70:73]
	s_setprio 0
	s_setprio 1
	v_mfma_f32_16x16x32_bf16 v[124:127], v[162:165], v[178:181], v[124:127]
	v_mfma_f32_16x16x32_bf16 v[116:119], v[170:173], v[178:181], v[116:119]
	v_mfma_f32_16x16x32_bf16 v[108:111], v[162:165], v[186:189], v[108:111]
	v_mfma_f32_16x16x32_bf16 v[100:103], v[170:173], v[186:189], v[100:103]
	v_mfma_f32_16x16x32_bf16 v[90:93], v[162:165], v[194:197], v[90:93]
	v_mfma_f32_16x16x32_bf16 v[82:85], v[170:173], v[194:197], v[82:85]
	v_mfma_f32_16x16x32_bf16 v[74:77], v[162:165], v[212:215], v[74:77]
	v_mfma_f32_16x16x32_bf16 v[66:69], v[170:173], v[212:215], v[66:69]
	v_mfma_f32_16x16x32_bf16 v[124:127], v[166:169], v[182:185], v[124:127]
	v_mfma_f32_16x16x32_bf16 v[116:119], v[174:177], v[182:185], v[116:119]
	v_mfma_f32_16x16x32_bf16 v[108:111], v[166:169], v[190:193], v[108:111]
	v_mfma_f32_16x16x32_bf16 v[100:103], v[174:177], v[190:193], v[100:103]
	v_mfma_f32_16x16x32_bf16 v[90:93], v[166:169], v[208:211], v[90:93]
	v_mfma_f32_16x16x32_bf16 v[82:85], v[174:177], v[208:211], v[82:85]
	v_mfma_f32_16x16x32_bf16 v[74:77], v[166:169], v[216:219], v[74:77]
	v_mfma_f32_16x16x32_bf16 v[66:69], v[174:177], v[216:219], v[66:69]
	s_setprio 0
	s_barrier
	s_mov_b32 m0, s4
	v_lshl_add_u64 v[198:199], s[34:35], 0, v[136:137]
	s_add_u32 vcc_lo, s34, 0x40000
	ds_read_b128 v[178:181], v145 offset:16384
	ds_read_b128 v[182:185], v145 offset:17408
	ds_read_b128 v[186:189], v145 offset:18432
	ds_read_b128 v[190:193], v145 offset:19456
	ds_read_b128 v[194:197], v145 offset:20480
	ds_read_b128 v[208:211], v145 offset:21504
	ds_read_b128 v[212:215], v145 offset:22528
	ds_read_b128 v[216:219], v145 offset:23552
	global_load_lds_dwordx4 v[198:199], off
	v_lshl_add_u64 v[220:221], s[34:35], 0, v[132:133]
	s_mov_b32 m0, s5
	s_addc_u32 vcc_hi, s35, 0
	global_load_lds_dwordx4 v[220:221], off
	v_lshl_add_u64 v[222:223], vcc, 0, v[136:137]
	s_mov_b32 m0, s29
	v_lshl_add_u64 v[224:225], s[36:37], 0, v[134:135]
	global_load_lds_dwordx4 v[222:223], off
	v_lshl_add_u64 v[222:223], vcc, 0, v[132:133]
	s_mov_b32 m0, s52
	s_nop 0
	global_load_lds_dwordx4 v[222:223], off
	v_lshl_add_u64 v[222:223], s[36:37], 0, v[138:139]
	s_mov_b32 m0, s58
	s_nop 0
	global_load_lds_dwordx4 v[222:223], off
	s_mov_b32 m0, s59
	s_nop 0
	global_load_lds_dwordx4 v[224:225], off
	s_nop 0
	s_waitcnt vmcnt(8)
	s_waitcnt lgkmcnt(0)
	s_barrier
; #define PG8_STAGE_A(bufoff, h, ptr, nsel) do { if constexpr (Sched::GATHER) { if (nsel) PG8_STAGE_X(bufoff, ptr, vAn[h], PG8_A_AUX); else PG8_STAGE_X(bufoff, ptr, vAc[h], PG8_A_AUX); } \
;         else PG8_STAGE_X(bufoff, (ptr) + (h) * hstep, voffA, PG8_A_AUX); } while (0)
; #define PG8_STAGE(bufoff, gbase, voff) PG8_STAGE_X(bufoff, gbase, voff, PG8_B_AUX)
; #define PG8_LDA(dst, b, h) do { _Pragma("unroll") for (int m = 0; m < 4; ++m) _Pragma("unroll") for (int k = 0; k < 2; ++k) dst[m][k] = *(const PG8_LAS bf16x8*)(lds + PG8_SA(b, h) + aoff + m * 2048 + k * 1024); } while (0)
; #define PG8_LDB(dst, b, h) do { _Pragma("unroll") for (int n = 0; n < 2; ++n) _Pragma("unroll") for (int k = 0; k < 2; ++k) dst[n][k] = *(const PG8_LAS bf16x8*)(lds + PG8_SB(b, h) + boff + n * 2048 + k * 1024); } while (0)
; #define PG8_MMA(ai, bj, At, Bt) do { __builtin_amdgcn_s_setprio(1); _Pragma("unroll") for (int m = 0; m < 4; ++m) _Pragma("unroll") for (int n = 0; n < 2; ++n) _Pragma("unroll") for (int k = 0; k < 2; ++k) \
;         acc[ai][bj][m][n] = __builtin_amdgcn_mfma_f32_16x16x32_bf16(Bt[n][k], At[m][k], acc[ai][bj][m][n], 0, 0, 0); __builtin_amdgcn_s_setprio(0); } while (0)
; #define PG8_WAIT_V(n) asm volatile("s_waitcnt vmcnt(" #n ")" ::: "memory")
; #define PG8_WAIT_L(n) asm volatile("s_waitcnt lgkmcnt(" #n ")" ::: "memory")
; #define PG8_BAR __builtin_amdgcn_s_barrier()
; #define PG8_SCHED __builtin_amdgcn_sched_barrier(0)
; template <class Epi, class Sched, bool ALIGN_EPI = false, bool SP2 = false>
; __device__ __forceinline__ void gemm_phase(PG8_LAS unsigned char* lds, const Gemm g, const Sched& S, const Epi& E) {
;     ...
;             PG8_WAIT_V(8); PG8_WAIT_L(0); PG8_BAR; PG8_MMA(1, 0, At, B0); PG8_MMA(1, 1, At, B1); PG8_BAR; PG8_SCHED;
;             PG8_LDB(B0, 1, 0); PG8_LDB(B1, 1, 1); PG8_SCHED; PG8_LDA(At, 1, 0); PG8_STAGE_A(PG8_SA(0, 1), 1, a2, last);
;             PG8_WAIT_V(8); PG8_WAIT_L(0); PG8_BAR; PG8_MMA(0, 0, At, B0); PG8_MMA(0, 1, At, B1); PG8_BAR; PG8_SCHED;
;             PG8_LDA(At, 1, 1); PG8_STAGE(PG8_SB(1, 0), b3, voffB); PG8_STAGE(PG8_SB(1, 1), b3 + hstep, voffB); PG8_STAGE_A(PG8_SA(1, 0), 0, a3, last);
	s_setprio 1
	s_waitcnt lgkmcnt(0)
	v_mfma_f32_16x16x32_bf16 v[62:65], v[146:149], v[178:181], v[62:65]
	v_mfma_f32_16x16x32_bf16 v[54:57], v[154:157], v[178:181], v[54:57]
	v_mfma_f32_16x16x32_bf16 v[46:49], v[146:149], v[186:189], v[46:49]
	v_mfma_f32_16x16x32_bf16 v[38:41], v[154:157], v[186:189], v[38:41]
	v_mfma_f32_16x16x32_bf16 v[30:33], v[146:149], v[194:197], v[30:33]
	v_mfma_f32_16x16x32_bf16 v[22:25], v[154:157], v[194:197], v[22:25]
	v_mfma_f32_16x16x32_bf16 v[14:17], v[146:149], v[212:215], v[14:17]
	v_mfma_f32_16x16x32_bf16 v[6:9], v[154:157], v[212:215], v[6:9]
	v_mfma_f32_16x16x32_bf16 v[62:65], v[150:153], v[182:185], v[62:65]
	v_mfma_f32_16x16x32_bf16 v[54:57], v[158:161], v[182:185], v[54:57]
	v_mfma_f32_16x16x32_bf16 v[46:49], v[150:153], v[190:193], v[46:49]
	v_mfma_f32_16x16x32_bf16 v[38:41], v[158:161], v[190:193], v[38:41]
	v_mfma_f32_16x16x32_bf16 v[30:33], v[150:153], v[208:211], v[30:33]
	v_mfma_f32_16x16x32_bf16 v[22:25], v[158:161], v[208:211], v[22:25]
	v_mfma_f32_16x16x32_bf16 v[14:17], v[150:153], v[216:219], v[14:17]
	v_mfma_f32_16x16x32_bf16 v[6:9], v[158:161], v[216:219], v[6:9]
	s_setprio 0
	s_setprio 1
	v_mfma_f32_16x16x32_bf16 v[58:61], v[162:165], v[178:181], v[58:61]
	v_mfma_f32_16x16x32_bf16 v[50:53], v[170:173], v[178:181], v[50:53]
	v_mfma_f32_16x16x32_bf16 v[42:45], v[162:165], v[186:189], v[42:45]
	v_mfma_f32_16x16x32_bf16 v[34:37], v[170:173], v[186:189], v[34:37]
	v_mfma_f32_16x16x32_bf16 v[26:29], v[162:165], v[194:197], v[26:29]
	v_mfma_f32_16x16x32_bf16 v[18:21], v[170:173], v[194:197], v[18:21]
	v_mfma_f32_16x16x32_bf16 v[10:13], v[162:165], v[212:215], v[10:13]
	v_mfma_f32_16x16x32_bf16 v[2:5], v[170:173], v[212:215], v[2:5]
	v_mfma_f32_16x16x32_bf16 v[58:61], v[166:169], v[182:185], v[58:61]
	v_mfma_f32_16x16x32_bf16 v[50:53], v[174:177], v[182:185], v[50:53]
	v_mfma_f32_16x16x32_bf16 v[42:45], v[166:169], v[190:193], v[42:45]
	v_mfma_f32_16x16x32_bf16 v[34:37], v[174:177], v[190:193], v[34:37]
	v_mfma_f32_16x16x32_bf16 v[26:29], v[166:169], v[208:211], v[26:29]
	v_mfma_f32_16x16x32_bf16 v[18:21], v[174:177], v[208:211], v[18:21]
	v_mfma_f32_16x16x32_bf16 v[10:13], v[166:169], v[216:219], v[10:13]
	v_mfma_f32_16x16x32_bf16 v[2:5], v[174:177], v[216:219], v[2:5]
	s_setprio 0
	s_barrier
	v_add_u32_e32 v158, s51, v99
	v_add_u32_e32 v174, s56, v99
	ds_read_b128 v[146:149], v158
	ds_read_b128 v[150:153], v158 offset:1024
	ds_read_b128 v[154:157], v158 offset:2048
	ds_read_b128 v[158:161], v158 offset:3072
	ds_read_b128 v[162:165], v174
	ds_read_b128 v[166:169], v174 offset:1024
	ds_read_b128 v[170:173], v174 offset:2048
	ds_read_b128 v[174:177], v174 offset:3072
	s_add_u32 s36, s36, 0x40000
	s_addc_u32 s37, s37, 0
	s_mov_b32 m0, s60
	v_lshl_add_u64 v[226:227], s[36:37], 0, v[138:139]
	ds_read_b128 v[178:181], v145 offset:32768
	ds_read_b128 v[182:185], v145 offset:33792
	ds_read_b128 v[186:189], v145 offset:34816
	ds_read_b128 v[190:193], v145 offset:35840
	ds_read_b128 v[194:197], v145 offset:36864
	ds_read_b128 v[208:211], v145 offset:37888
	ds_read_b128 v[212:215], v145 offset:38912
	ds_read_b128 v[216:219], v145 offset:39936
	global_load_lds_dwordx4 v[226:227], off
	v_lshl_add_u64 v[226:227], s[36:37], 0, v[134:135]
	s_mov_b32 m0, s61
	s_nop 0
	global_load_lds_dwordx4 v[226:227], off
	s_nop 0
	s_waitcnt vmcnt(8)
	s_waitcnt lgkmcnt(0)
	s_barrier
	s_setprio 1
	s_waitcnt lgkmcnt(0)
	v_mfma_f32_16x16x32_bf16 v[128:131], v[146:149], v[178:181], v[128:131]
	v_mfma_f32_16x16x32_bf16 v[120:123], v[154:157], v[178:181], v[120:123]
	v_mfma_f32_16x16x32_bf16 v[112:115], v[146:149], v[186:189], v[112:115]
	v_mfma_f32_16x16x32_bf16 v[104:107], v[154:157], v[186:189], v[104:107]
	v_mfma_f32_16x16x32_bf16 v[94:97], v[146:149], v[194:197], v[94:97]
	v_mfma_f32_16x16x32_bf16 v[86:89], v[154:157], v[194:197], v[86:89]
	v_mfma_f32_16x16x32_bf16 v[78:81], v[146:149], v[212:215], v[78:81]
	v_mfma_f32_16x16x32_bf16 v[70:73], v[154:157], v[212:215], v[70:73]
	v_mfma_f32_16x16x32_bf16 v[128:131], v[150:153], v[182:185], v[128:131]
	v_mfma_f32_16x16x32_bf16 v[120:123], v[158:161], v[182:185], v[120:123]
	v_mfma_f32_16x16x32_bf16 v[112:115], v[150:153], v[190:193], v[112:115]
	v_mfma_f32_16x16x32_bf16 v[104:107], v[158:161], v[190:193], v[104:107]
	v_mfma_f32_16x16x32_bf16 v[94:97], v[150:153], v[208:211], v[94:97]
	v_mfma_f32_16x16x32_bf16 v[86:89], v[158:161], v[208:211], v[86:89]
	v_mfma_f32_16x16x32_bf16 v[78:81], v[150:153], v[216:219], v[78:81]
	v_mfma_f32_16x16x32_bf16 v[70:73], v[158:161], v[216:219], v[70:73]
	s_setprio 0
	s_setprio 1
	v_mfma_f32_16x16x32_bf16 v[124:127], v[162:165], v[178:181], v[124:127]
	v_mfma_f32_16x16x32_bf16 v[116:119], v[170:173], v[178:181], v[116:119]
	v_mfma_f32_16x16x32_bf16 v[108:111], v[162:165], v[186:189], v[108:111]
	v_mfma_f32_16x16x32_bf16 v[100:103], v[170:173], v[186:189], v[100:103]
	v_mfma_f32_16x16x32_bf16 v[90:93], v[162:165], v[194:197], v[90:93]
	v_mfma_f32_16x16x32_bf16 v[82:85], v[170:173], v[194:197], v[82:85]
	v_mfma_f32_16x16x32_bf16 v[74:77], v[162:165], v[212:215], v[74:77]
	v_mfma_f32_16x16x32_bf16 v[66:69], v[170:173], v[212:215], v[66:69]
	v_mfma_f32_16x16x32_bf16 v[124:127], v[166:169], v[182:185], v[124:127]
	v_mfma_f32_16x16x32_bf16 v[116:119], v[174:177], v[182:185], v[116:119]
	v_mfma_f32_16x16x32_bf16 v[108:111], v[166:169], v[190:193], v[108:111]
	v_mfma_f32_16x16x32_bf16 v[100:103], v[174:177], v[190:193], v[100:103]
	v_mfma_f32_16x16x32_bf16 v[90:93], v[166:169], v[208:211], v[90:93]
	v_mfma_f32_16x16x32_bf16 v[82:85], v[174:177], v[208:211], v[82:85]
	v_mfma_f32_16x16x32_bf16 v[74:77], v[166:169], v[216:219], v[74:77]
	v_mfma_f32_16x16x32_bf16 v[66:69], v[174:177], v[216:219], v[66:69]
	s_setprio 0
	s_barrier
; #define PG8_STAGE_A(bufoff, h, ptr, nsel) do { if constexpr (Sched::GATHER) { if (nsel) PG8_STAGE_X(bufoff, ptr, vAn[h], PG8_A_AUX); else PG8_STAGE_X(bufoff, ptr, vAc[h], PG8_A_AUX); } \
;         else PG8_STAGE_X(bufoff, (ptr) + (h) * hstep, voffA, PG8_A_AUX); } while (0)
; #define PG8_STAGE(bufoff, gbase, voff) PG8_STAGE_X(bufoff, gbase, voff, PG8_B_AUX)
; #define PG8_LDA(dst, b, h) do { _Pragma("unroll") for (int m = 0; m < 4; ++m) _Pragma("unroll") for (int k = 0; k < 2; ++k) dst[m][k] = *(const PG8_LAS bf16x8*)(lds + PG8_SA(b, h) + aoff + m * 2048 + k * 1024); } while (0)
; #define PG8_MMA(ai, bj, At, Bt) do { __builtin_amdgcn_s_setprio(1); _Pragma("unroll") for (int m = 0; m < 4; ++m) _Pragma("unroll") for (int n = 0; n < 2; ++n) _Pragma("unroll") for (int k = 0; k < 2; ++k) \
;         acc[ai][bj][m][n] = __builtin_amdgcn_mfma_f32_16x16x32_bf16(Bt[n][k], At[m][k], acc[ai][bj][m][n], 0, 0, 0); __builtin_amdgcn_s_setprio(0); } while (0)
; #define PG8_WAIT_V(n) asm volatile("s_waitcnt vmcnt(" #n ")" ::: "memory")
; #define PG8_WAIT_L(n) asm volatile("s_waitcnt lgkmcnt(" #n ")" ::: "memory")
; #define PG8_BAR __builtin_amdgcn_s_barrier()
; #define PG8_SCHED __builtin_amdgcn_sched_barrier(0)
; template <class Epi, class Sched, bool ALIGN_EPI = false, bool SP2 = false>
; __device__ __forceinline__ void gemm_phase(PG8_LAS unsigned char* lds, const Gemm g, const Sched& S, const Epi& E) {
;     ...
;             PG8_LDA(At, 1, 1); PG8_STAGE(PG8_SB(1, 0), b3, voffB); PG8_STAGE(PG8_SB(1, 1), b3 + hstep, voffB); PG8_STAGE_A(PG8_SA(1, 0), 0, a3, last);
;             PG8_WAIT_V(8); PG8_WAIT_L(0); PG8_BAR; PG8_MMA(1, 0, At, B0); PG8_MMA(1, 1, At, B1); PG8_BAR; PG8_SCHED;
	s_mov_b32 m0, s64
	v_lshl_add_u64 v[198:199], v[198:199], 0, s[54:55]
	s_add_u32 s34, s34, 0x40080
	ds_read_b128 v[178:181], v145 offset:49152
	ds_read_b128 v[182:185], v145 offset:50176
	ds_read_b128 v[186:189], v145 offset:51200
	ds_read_b128 v[190:193], v145 offset:52224
	ds_read_b128 v[194:197], v145 offset:53248
	ds_read_b128 v[208:211], v145 offset:54272
	ds_read_b128 v[212:215], v145 offset:55296
	ds_read_b128 v[216:219], v145 offset:56320
	global_load_lds_dwordx4 v[198:199], off
	v_lshl_add_u64 v[198:199], v[220:221], 0, s[54:55]
	s_mov_b32 m0, s68
	s_addc_u32 s35, s35, 0
	global_load_lds_dwordx4 v[198:199], off
	v_lshl_add_u64 v[198:199], s[34:35], 0, v[136:137]
	s_mov_b32 m0, s73
	s_nop 0
	global_load_lds_dwordx4 v[198:199], off
	v_lshl_add_u64 v[198:199], s[34:35], 0, v[132:133]
	s_mov_b32 m0, s86
	s_nop 0
	global_load_lds_dwordx4 v[198:199], off
	v_lshl_add_u64 v[198:199], v[222:223], 0, s[54:55]
	s_mov_b32 m0, s69
	s_nop 0
	global_load_lds_dwordx4 v[198:199], off
	v_lshl_add_u64 v[198:199], v[224:225], 0, s[54:55]
	s_mov_b32 m0, s72
	s_nop 0
	global_load_lds_dwordx4 v[198:199], off
	s_waitcnt vmcnt(8)
	s_waitcnt lgkmcnt(0)
	s_barrier
	s_setprio 1
	s_waitcnt lgkmcnt(0)
	v_mfma_f32_16x16x32_bf16 v[62:65], v[146:149], v[178:181], v[62:65]
	v_mfma_f32_16x16x32_bf16 v[54:57], v[154:157], v[178:181], v[54:57]
	v_mfma_f32_16x16x32_bf16 v[46:49], v[146:149], v[186:189], v[46:49]
	v_mfma_f32_16x16x32_bf16 v[38:41], v[154:157], v[186:189], v[38:41]
	v_mfma_f32_16x16x32_bf16 v[30:33], v[146:149], v[194:197], v[30:33]
	v_mfma_f32_16x16x32_bf16 v[22:25], v[154:157], v[194:197], v[22:25]
	v_mfma_f32_16x16x32_bf16 v[14:17], v[146:149], v[212:215], v[14:17]
	v_mfma_f32_16x16x32_bf16 v[6:9], v[154:157], v[212:215], v[6:9]
	v_mfma_f32_16x16x32_bf16 v[62:65], v[150:153], v[182:185], v[62:65]
	v_mfma_f32_16x16x32_bf16 v[54:57], v[158:161], v[182:185], v[54:57]
	v_mfma_f32_16x16x32_bf16 v[46:49], v[150:153], v[190:193], v[46:49]
	v_mfma_f32_16x16x32_bf16 v[38:41], v[158:161], v[190:193], v[38:41]
	v_mfma_f32_16x16x32_bf16 v[30:33], v[150:153], v[208:211], v[30:33]
	v_mfma_f32_16x16x32_bf16 v[22:25], v[158:161], v[208:211], v[22:25]
	v_mfma_f32_16x16x32_bf16 v[14:17], v[150:153], v[216:219], v[14:17]
	v_mfma_f32_16x16x32_bf16 v[6:9], v[158:161], v[216:219], v[6:9]
	s_setprio 0
	s_setprio 1
	v_mfma_f32_16x16x32_bf16 v[58:61], v[162:165], v[178:181], v[58:61]
	v_mfma_f32_16x16x32_bf16 v[50:53], v[170:173], v[178:181], v[50:53]
	v_mfma_f32_16x16x32_bf16 v[42:45], v[162:165], v[186:189], v[42:45]
	v_mfma_f32_16x16x32_bf16 v[34:37], v[170:173], v[186:189], v[34:37]
	v_mfma_f32_16x16x32_bf16 v[26:29], v[162:165], v[194:197], v[26:29]
	v_mfma_f32_16x16x32_bf16 v[18:21], v[170:173], v[194:197], v[18:21]
	v_mfma_f32_16x16x32_bf16 v[10:13], v[162:165], v[212:215], v[10:13]
	v_mfma_f32_16x16x32_bf16 v[2:5], v[170:173], v[212:215], v[2:5]
	v_mfma_f32_16x16x32_bf16 v[58:61], v[166:169], v[182:185], v[58:61]
	v_mfma_f32_16x16x32_bf16 v[50:53], v[174:177], v[182:185], v[50:53]
	v_mfma_f32_16x16x32_bf16 v[42:45], v[166:169], v[190:193], v[42:45]
	v_mfma_f32_16x16x32_bf16 v[34:37], v[174:177], v[190:193], v[34:37]
	v_mfma_f32_16x16x32_bf16 v[26:29], v[166:169], v[208:211], v[26:29]
	v_mfma_f32_16x16x32_bf16 v[18:21], v[174:177], v[208:211], v[18:21]
	v_mfma_f32_16x16x32_bf16 v[10:13], v[166:169], v[216:219], v[10:13]
	v_mfma_f32_16x16x32_bf16 v[2:5], v[174:177], v[216:219], v[2:5]
	s_setprio 0
	s_barrier
	s_add_i32 s94, s94, 2
	s_add_u32 s30, s30, 0x100
	s_addc_u32 s31, s31, 0
	s_add_u32 s89, s89, 0x100
	s_addc_u32 s90, s90, 0
	s_cmp_gt_u32 s94, 13
	s_cbranch_scc0 .LBB13_1412
	s_and_b64 vcc, exec, s[12:13]
	s_mov_b32 s90, 0x1c000
	s_mov_b32 s88, 0x16000
	s_cbranch_vccz .LBB13_1415
	s_barrier

; #define PG8_LAS __attribute__((address_space(3)))
; #define PG8_STAGE_A(bufoff, h, ptr, nsel) do { if constexpr (Sched::GATHER) { if (nsel) PG8_STAGE_X(bufoff, ptr, vAn[h], PG8_A_AUX); else PG8_STAGE_X(bufoff, ptr, vAc[h], PG8_A_AUX); } \
;         else PG8_STAGE_X(bufoff, (ptr) + (h) * hstep, voffA, PG8_A_AUX); } while (0)
; #define PG8_STAGE(bufoff, gbase, voff) PG8_STAGE_X(bufoff, gbase, voff, PG8_B_AUX)
; #define PG8_LDA(dst, b, h) do { _Pragma("unroll") for (int m = 0; m < 4; ++m) _Pragma("unroll") for (int k = 0; k < 2; ++k) dst[m][k] = *(const PG8_LAS bf16x8*)(lds + PG8_SA(b, h) + aoff + m * 2048 + k * 1024); } while (0)
; #define PG8_LDB(dst, b, h) do { _Pragma("unroll") for (int n = 0; n < 2; ++n) _Pragma("unroll") for (int k = 0; k < 2; ++k) dst[n][k] = *(const PG8_LAS bf16x8*)(lds + PG8_SB(b, h) + boff + n * 2048 + k * 1024); } while (0)
; #define PG8_WAIT_V(n) asm volatile("s_waitcnt vmcnt(" #n ")" ::: "memory")
; #define PG8_WAIT_L(n) asm volatile("s_waitcnt lgkmcnt(" #n ")" ::: "memory")
; template <class Epi, class Sched, bool ALIGN_EPI = false, bool SP2 = false>
; __device__ __forceinline__ void gemm_phase(PG8_LAS unsigned char* lds, const Gemm g, const Sched& S, const Epi& E) {
;     ...
;         for (int t = 0; t < nt; t += 2) {
;             const bool last = (t == nt - 2);
;             const char* a1 = cA + (size_t)(t + 1) * kstep;
;             const char* a2 = last ? nA : cA + (size_t)(t + 2) * kstep; const char* b2 = last ? nB : cB + (size_t)(t + 2) * kstep;
;             const char* a3 = a2 + kstep; const char* b3 = b2 + kstep;
;             if (last && has_next) S.a_ready(nxt);
;             if constexpr (Sched::GATHER) { if (last) { const u32x4 pv_ = *(const PG8_LAS u32x4*)(lds + STAGE_BYTES + tid * 16); vAn[0][0] = pv_.x; vAn[0][1] = pv_.y; vAn[1][0] = pv_.z; vAn[1][1] = pv_.w; } }
;             if constexpr (SP2) {
;             PG8_LDB(B0, 0, 0); PG8_LDB(B1, 0, 1); PG8_SCHED; PG8_LDA(At, 0, 0); PG8_STAGE_A(PG8_SA(1, 1), 1, a1, false);
;             PG8_WAIT_V(8); PG8_WAIT_L(0); PG8_BAR; PG8_MMA(0, 0, At, B0); PG8_MMA(0, 1, At, B1); PG8_BAR; PG8_SCHED;
;             PG8_LDA(At, 0, 1); PG8_STAGE(PG8_SB(0, 0), b2, voffB); PG8_STAGE(PG8_SB(0, 1), b2 + hstep, voffB); PG8_STAGE_A(PG8_SA(0, 0), 0, a2, last);
;             PG8_WAIT_V(8); PG8_WAIT_L(0); PG8_BAR; PG8_MMA(1, 0, At, B0); PG8_MMA(1, 1, At, B1); PG8_BAR; PG8_SCHED;
.LBB13_1448:
	v_add_u32_e32 v136, s47, v245
	v_add_u32_e32 v148, s50, v245
	ds_read_b128 v[152:155], v136
	ds_read_b128 v[156:159], v136 offset:1024
	ds_read_b128 v[160:163], v136 offset:2048
	ds_read_b128 v[164:167], v136 offset:3072
	ds_read_b128 v[136:139], v148
	ds_read_b128 v[140:143], v148 offset:1024
	ds_read_b128 v[144:147], v148 offset:2048
	ds_read_b128 v[148:151], v148 offset:3072
	s_add_u32 s29, s2, s34
	s_addc_u32 s42, s25, s35
	s_and_b64 s[40:41], s[38:39], exec
	s_cselect_b32 s41, s9, s42
	s_cselect_b32 s40, s8, s29
	v_lshl_add_u64 v[228:229], v[222:223], 0, s[34:35]
	v_lshl_add_u64 v[224:225], v[228:229], 0, s[82:83]
	s_add_i32 m0, s69, 0xc000
	v_lshl_add_u64 v[230:231], v[220:221], 0, s[34:35]
	ds_read_b128 v[168:171], v247
	ds_read_b128 v[172:175], v247 offset:1024
	ds_read_b128 v[176:179], v247 offset:2048
	ds_read_b128 v[180:183], v247 offset:3072
	ds_read_b128 v[184:187], v247 offset:4096
	ds_read_b128 v[188:191], v247 offset:5120
	ds_read_b128 v[192:195], v247 offset:6144
	ds_read_b128 v[196:199], v247 offset:7168
	global_load_lds_dwordx4 v[224:225], off
	v_lshl_add_u64 v[224:225], v[230:231], 0, s[82:83]
	s_add_i32 m0, s69, 0xe000
	s_nop 0
	global_load_lds_dwordx4 v[224:225], off
	s_nop 0
	s_waitcnt vmcnt(8)
	s_waitcnt lgkmcnt(0)
	s_barrier
	s_setprio 1
	s_waitcnt lgkmcnt(0)
	v_mfma_f32_16x16x32_bf16 v[132:135], v[152:155], v[168:171], v[132:135]
	v_mfma_f32_16x16x32_bf16 v[124:127], v[160:163], v[168:171], v[124:127]
	v_mfma_f32_16x16x32_bf16 v[116:119], v[152:155], v[176:179], v[116:119]
	v_mfma_f32_16x16x32_bf16 v[108:111], v[160:163], v[176:179], v[108:111]
	v_mfma_f32_16x16x32_bf16 v[94:97], v[152:155], v[184:187], v[94:97]
	v_mfma_f32_16x16x32_bf16 v[86:89], v[160:163], v[184:187], v[86:89]
	v_mfma_f32_16x16x32_bf16 v[78:81], v[152:155], v[192:195], v[78:81]
	v_mfma_f32_16x16x32_bf16 v[70:73], v[160:163], v[192:195], v[70:73]
	v_mfma_f32_16x16x32_bf16 v[132:135], v[156:159], v[172:175], v[132:135]
	v_mfma_f32_16x16x32_bf16 v[124:127], v[164:167], v[172:175], v[124:127]
	v_mfma_f32_16x16x32_bf16 v[116:119], v[156:159], v[180:183], v[116:119]
	v_mfma_f32_16x16x32_bf16 v[108:111], v[164:167], v[180:183], v[108:111]
	v_mfma_f32_16x16x32_bf16 v[94:97], v[156:159], v[188:191], v[94:97]
	v_mfma_f32_16x16x32_bf16 v[86:89], v[164:167], v[188:191], v[86:89]
	v_mfma_f32_16x16x32_bf16 v[78:81], v[156:159], v[196:199], v[78:81]
	v_mfma_f32_16x16x32_bf16 v[70:73], v[164:167], v[196:199], v[70:73]
	s_setprio 0
	s_setprio 1
	v_mfma_f32_16x16x32_bf16 v[128:131], v[136:139], v[168:171], v[128:131]
	v_mfma_f32_16x16x32_bf16 v[120:123], v[144:147], v[168:171], v[120:123]
	v_mfma_f32_16x16x32_bf16 v[112:115], v[136:139], v[176:179], v[112:115]
	v_mfma_f32_16x16x32_bf16 v[104:107], v[144:147], v[176:179], v[104:107]
	v_mfma_f32_16x16x32_bf16 v[90:93], v[136:139], v[184:187], v[90:93]
	v_mfma_f32_16x16x32_bf16 v[82:85], v[144:147], v[184:187], v[82:85]
	v_mfma_f32_16x16x32_bf16 v[74:77], v[136:139], v[192:195], v[74:77]
	v_mfma_f32_16x16x32_bf16 v[66:69], v[144:147], v[192:195], v[66:69]
	v_mfma_f32_16x16x32_bf16 v[128:131], v[140:143], v[172:175], v[128:131]
	v_mfma_f32_16x16x32_bf16 v[120:123], v[148:151], v[172:175], v[120:123]
	v_mfma_f32_16x16x32_bf16 v[112:115], v[140:143], v[180:183], v[112:115]
	v_mfma_f32_16x16x32_bf16 v[104:107], v[148:151], v[180:183], v[104:107]
	v_mfma_f32_16x16x32_bf16 v[90:93], v[140:143], v[188:191], v[90:93]
	v_mfma_f32_16x16x32_bf16 v[82:85], v[148:151], v[188:191], v[82:85]
	v_mfma_f32_16x16x32_bf16 v[74:77], v[140:143], v[196:199], v[74:77]
	v_mfma_f32_16x16x32_bf16 v[66:69], v[148:151], v[196:199], v[66:69]
	s_setprio 0
	s_barrier
	s_mov_b32 m0, s31
	v_lshl_add_u64 v[224:225], s[40:41], 0, v[208:209]
	s_add_u32 s42, s40, 0x40000
	ds_read_b128 v[192:195], v247 offset:16384
	ds_read_b128 v[196:199], v247 offset:17408
	ds_read_b128 v[184:187], v247 offset:18432
	ds_read_b128 v[188:191], v247 offset:19456
	ds_read_b128 v[176:179], v247 offset:20480
	ds_read_b128 v[180:183], v247 offset:21504
	ds_read_b128 v[168:171], v247 offset:22528
	ds_read_b128 v[172:175], v247 offset:23552
	global_load_lds_dwordx4 v[224:225], off
	v_lshl_add_u64 v[226:227], s[40:41], 0, v[210:211]
	s_mov_b32 m0, s59
	s_addc_u32 s43, s41, 0
	global_load_lds_dwordx4 v[226:227], off
	v_lshl_add_u64 v[232:233], s[42:43], 0, v[208:209]
	s_mov_b32 m0, s61
	s_and_b64 vcc, exec, s[36:37]
	global_load_lds_dwordx4 v[232:233], off
	v_lshl_add_u64 v[232:233], s[42:43], 0, v[210:211]
	s_mov_b32 m0, s68
	s_mov_b64 s[42:43], -1
	global_load_lds_dwordx4 v[232:233], off
	s_cbranch_vccz .LBB13_1450
	s_mov_b32 m0, s69
	v_lshl_add_u64 v[232:233], v[218:219], 0, s[34:35]
	global_load_lds_dwordx4 v[232:233], off
	v_lshl_add_u64 v[232:233], v[216:217], 0, s[34:35]
	s_mov_b64 s[42:43], 0

; #define PG8_LAS __attribute__((address_space(3)))
; #define PG8_STAGE_A(bufoff, h, ptr, nsel) do { if constexpr (Sched::GATHER) { if (nsel) PG8_STAGE_X(bufoff, ptr, vAn[h], PG8_A_AUX); else PG8_STAGE_X(bufoff, ptr, vAc[h], PG8_A_AUX); } \
;         else PG8_STAGE_X(bufoff, (ptr) + (h) * hstep, voffA, PG8_A_AUX); } while (0)
; #define PG8_STAGE(bufoff, gbase, voff) PG8_STAGE_X(bufoff, gbase, voff, PG8_B_AUX)
; #define PG8_LDA(dst, b, h) do { _Pragma("unroll") for (int m = 0; m < 4; ++m) _Pragma("unroll") for (int k = 0; k < 2; ++k) dst[m][k] = *(const PG8_LAS bf16x8*)(lds + PG8_SA(b, h) + aoff + m * 2048 + k * 1024); } while (0)
; #define PG8_LDB(dst, b, h) do { _Pragma("unroll") for (int n = 0; n < 2; ++n) _Pragma("unroll") for (int k = 0; k < 2; ++k) dst[n][k] = *(const PG8_LAS bf16x8*)(lds + PG8_SB(b, h) + boff + n * 2048 + k * 1024); } while (0)
; #define PG8_WAIT_V(n) asm volatile("s_waitcnt vmcnt(" #n ")" ::: "memory")
; #define PG8_WAIT_L(n) asm volatile("s_waitcnt lgkmcnt(" #n ")" ::: "memory")
; template <class Epi, class Sched, bool ALIGN_EPI = false, bool SP2 = false>
; __device__ __forceinline__ void gemm_phase(PG8_LAS unsigned char* lds, const Gemm g, const Sched& S, const Epi& E) {
;     ...
;         for (int t = 0; t < nt; t += 2) {
;             const bool last = (t == nt - 2);
;             const char* a1 = cA + (size_t)(t + 1) * kstep;
;             const char* a2 = last ? nA : cA + (size_t)(t + 2) * kstep; const char* b2 = last ? nB : cB + (size_t)(t + 2) * kstep;
;             const char* a3 = a2 + kstep; const char* b3 = b2 + kstep;
;             if (last && has_next) S.a_ready(nxt);
;             if constexpr (Sched::GATHER) { if (last) { const u32x4 pv_ = *(const PG8_LAS u32x4*)(lds + STAGE_BYTES + tid * 16); vAn[0][0] = pv_.x; vAn[0][1] = pv_.y; vAn[1][0] = pv_.z; vAn[1][1] = pv_.w; } }
;             if constexpr (SP2) {
;             PG8_LDB(B0, 0, 0); PG8_LDB(B1, 0, 1); PG8_SCHED; PG8_LDA(At, 0, 0); PG8_STAGE_A(PG8_SA(1, 1), 1, a1, false);
;             PG8_WAIT_V(8); PG8_WAIT_L(0); PG8_BAR; PG8_MMA(0, 0, At, B0); PG8_MMA(0, 1, At, B1); PG8_BAR; PG8_SCHED;
;             PG8_LDA(At, 0, 1); PG8_STAGE(PG8_SB(0, 0), b2, voffB); PG8_STAGE(PG8_SB(0, 1), b2 + hstep, voffB); PG8_STAGE_A(PG8_SA(0, 0), 0, a2, last);
;             PG8_WAIT_V(8); PG8_WAIT_L(0); PG8_BAR; PG8_MMA(1, 0, At, B0); PG8_MMA(1, 1, At, B1); PG8_BAR; PG8_SCHED;
.LBB13_1538:
	v_add_u32_e32 v62, s36, v167
	v_add_u32_e32 v164, s39, v167
	ds_read_b128 v[42:45], v62
	ds_read_b128 v[50:53], v62 offset:1024
	ds_read_b128 v[58:61], v62 offset:2048
	ds_read_b128 v[62:65], v62 offset:3072
	ds_read_b128 v[160:163], v164
	ds_read_b128 v[170:173], v164 offset:1024
	ds_read_b128 v[174:177], v164 offset:2048
	ds_read_b128 v[178:181], v164 offset:3072
	s_add_u32 s18, s16, 0x100
	s_addc_u32 s19, s17, 0
	s_cmp_eq_u32 s73, 40
	s_cselect_b32 s23, s7, s19
	s_cselect_b32 s22, s6, s18
	s_cselect_b32 s21, s15, s72
	s_cselect_b32 s20, s14, s64
	v_lshl_add_u64 v[164:165], s[16:17], 0, v[156:157]
	s_add_i32 m0, s42, 0xc000
	ds_read_b128 v[182:185], v169
	ds_read_b128 v[186:189], v169 offset:1024
	ds_read_b128 v[190:193], v169 offset:2048
	ds_read_b128 v[194:197], v169 offset:3072
	ds_read_b128 v[208:211], v169 offset:4096
	ds_read_b128 v[212:215], v169 offset:5120
	ds_read_b128 v[216:219], v169 offset:6144
	ds_read_b128 v[220:223], v169 offset:7168
	global_load_lds_dwordx4 v[164:165], off
	v_lshl_add_u64 v[164:165], s[16:17], 0, v[158:159]
	s_add_i32 m0, s42, 0xe000
	s_nop 0
	global_load_lds_dwordx4 v[164:165], off
	s_waitcnt vmcnt(8)
	s_waitcnt lgkmcnt(0)
	s_barrier
	s_setprio 1
	s_waitcnt lgkmcnt(0)
	v_mfma_f32_16x16x32_bf16 v[144:147], v[42:45], v[182:185], v[144:147]
	v_mfma_f32_16x16x32_bf16 v[140:143], v[58:61], v[182:185], v[140:143]
	v_mfma_f32_16x16x32_bf16 v[128:131], v[42:45], v[190:193], v[128:131]
	v_mfma_f32_16x16x32_bf16 v[124:127], v[58:61], v[190:193], v[124:127]
	v_mfma_f32_16x16x32_bf16 v[112:115], v[42:45], v[208:211], v[112:115]
	v_mfma_f32_16x16x32_bf16 v[108:111], v[58:61], v[208:211], v[108:111]
	v_mfma_f32_16x16x32_bf16 v[94:97], v[42:45], v[216:219], v[94:97]
	v_mfma_f32_16x16x32_bf16 v[90:93], v[58:61], v[216:219], v[90:93]
	v_mfma_f32_16x16x32_bf16 v[144:147], v[50:53], v[186:189], v[144:147]
	v_mfma_f32_16x16x32_bf16 v[140:143], v[62:65], v[186:189], v[140:143]
	v_mfma_f32_16x16x32_bf16 v[128:131], v[50:53], v[194:197], v[128:131]
	v_mfma_f32_16x16x32_bf16 v[124:127], v[62:65], v[194:197], v[124:127]
	v_mfma_f32_16x16x32_bf16 v[112:115], v[50:53], v[212:215], v[112:115]
	v_mfma_f32_16x16x32_bf16 v[108:111], v[62:65], v[212:215], v[108:111]
	v_mfma_f32_16x16x32_bf16 v[94:97], v[50:53], v[220:223], v[94:97]
	v_mfma_f32_16x16x32_bf16 v[90:93], v[62:65], v[220:223], v[90:93]
	s_setprio 0
	s_setprio 1
	v_mfma_f32_16x16x32_bf16 v[136:139], v[160:163], v[182:185], v[136:139]
	v_mfma_f32_16x16x32_bf16 v[132:135], v[174:177], v[182:185], v[132:135]
	v_mfma_f32_16x16x32_bf16 v[120:123], v[160:163], v[190:193], v[120:123]
	v_mfma_f32_16x16x32_bf16 v[116:119], v[174:177], v[190:193], v[116:119]
	v_mfma_f32_16x16x32_bf16 v[104:107], v[160:163], v[208:211], v[104:107]
	v_mfma_f32_16x16x32_bf16 v[100:103], v[174:177], v[208:211], v[100:103]
	v_mfma_f32_16x16x32_bf16 v[86:89], v[160:163], v[216:219], v[86:89]
	v_mfma_f32_16x16x32_bf16 v[82:85], v[174:177], v[216:219], v[82:85]
	v_mfma_f32_16x16x32_bf16 v[136:139], v[170:173], v[186:189], v[136:139]
	v_mfma_f32_16x16x32_bf16 v[132:135], v[178:181], v[186:189], v[132:135]
	v_mfma_f32_16x16x32_bf16 v[120:123], v[170:173], v[194:197], v[120:123]
	v_mfma_f32_16x16x32_bf16 v[116:119], v[178:181], v[194:197], v[116:119]
	v_mfma_f32_16x16x32_bf16 v[104:107], v[170:173], v[212:215], v[104:107]
	v_mfma_f32_16x16x32_bf16 v[100:103], v[178:181], v[212:215], v[100:103]
	v_mfma_f32_16x16x32_bf16 v[86:89], v[170:173], v[220:223], v[86:89]
	v_mfma_f32_16x16x32_bf16 v[82:85], v[178:181], v[220:223], v[82:85]
	s_setprio 0
	s_barrier
	s_mov_b32 m0, s37
	v_lshl_add_u64 v[164:165], s[20:21], 0, v[150:151]
	s_add_u32 s16, s20, 0xb0000
	ds_read_b128 v[182:185], v169 offset:16384
	ds_read_b128 v[186:189], v169 offset:17408
	ds_read_b128 v[190:193], v169 offset:18432
	ds_read_b128 v[194:197], v169 offset:19456
	ds_read_b128 v[208:211], v169 offset:20480
	ds_read_b128 v[212:215], v169 offset:21504
	ds_read_b128 v[216:219], v169 offset:22528
	ds_read_b128 v[220:223], v169 offset:23552
	global_load_lds_dwordx4 v[164:165], off
	v_lshl_add_u64 v[198:199], s[20:21], 0, v[154:155]
	s_mov_b32 m0, s38
	s_addc_u32 s17, s21, 0
	global_load_lds_dwordx4 v[198:199], off
	v_lshl_add_u64 v[224:225], s[16:17], 0, v[150:151]
	s_mov_b32 m0, s40
	v_lshl_add_u64 v[226:227], s[22:23], 0, v[152:153]
	global_load_lds_dwordx4 v[224:225], off
	v_lshl_add_u64 v[224:225], s[16:17], 0, v[154:155]
	s_mov_b32 m0, s41
	s_nop 0
	global_load_lds_dwordx4 v[224:225], off
	v_lshl_add_u64 v[224:225], s[22:23], 0, v[148:149]
	s_mov_b32 m0, s42
	s_nop 0
	global_load_lds_dwordx4 v[224:225], off
	s_mov_b32 m0, s43
	s_nop 0
	global_load_lds_dwordx4 v[226:227], off
	s_nop 0
	s_waitcnt vmcnt(8)
	s_waitcnt lgkmcnt(0)
	s_barrier
; #define PG8_STAGE_A(bufoff, h, ptr, nsel) do { if constexpr (Sched::GATHER) { if (nsel) PG8_STAGE_X(bufoff, ptr, vAn[h], PG8_A_AUX); else PG8_STAGE_X(bufoff, ptr, vAc[h], PG8_A_AUX); } \
;         else PG8_STAGE_X(bufoff, (ptr) + (h) * hstep, voffA, PG8_A_AUX); } while (0)
; #define PG8_STAGE(bufoff, gbase, voff) PG8_STAGE_X(bufoff, gbase, voff, PG8_B_AUX)
; #define PG8_LDA(dst, b, h) do { _Pragma("unroll") for (int m = 0; m < 4; ++m) _Pragma("unroll") for (int k = 0; k < 2; ++k) dst[m][k] = *(const PG8_LAS bf16x8*)(lds + PG8_SA(b, h) + aoff + m * 2048 + k * 1024); } while (0)
; #define PG8_LDB(dst, b, h) do { _Pragma("unroll") for (int n = 0; n < 2; ++n) _Pragma("unroll") for (int k = 0; k < 2; ++k) dst[n][k] = *(const PG8_LAS bf16x8*)(lds + PG8_SB(b, h) + boff + n * 2048 + k * 1024); } while (0)
; #define PG8_MMA(ai, bj, At, Bt) do { __builtin_amdgcn_s_setprio(1); _Pragma("unroll") for (int m = 0; m < 4; ++m) _Pragma("unroll") for (int n = 0; n < 2; ++n) _Pragma("unroll") for (int k = 0; k < 2; ++k) \
;         acc[ai][bj][m][n] = __builtin_amdgcn_mfma_f32_16x16x32_bf16(Bt[n][k], At[m][k], acc[ai][bj][m][n], 0, 0, 0); __builtin_amdgcn_s_setprio(0); } while (0)
; #define PG8_WAIT_V(n) asm volatile("s_waitcnt vmcnt(" #n ")" ::: "memory")
; #define PG8_WAIT_L(n) asm volatile("s_waitcnt lgkmcnt(" #n ")" ::: "memory")
; #define PG8_BAR __builtin_amdgcn_s_barrier()
; #define PG8_SCHED __builtin_amdgcn_sched_barrier(0)
; template <class Epi, class Sched, bool ALIGN_EPI = false, bool SP2 = false>
; __device__ __forceinline__ void gemm_phase(PG8_LAS unsigned char* lds, const Gemm g, const Sched& S, const Epi& E) {
;     ...
;             PG8_WAIT_V(8); PG8_WAIT_L(0); PG8_BAR; PG8_MMA(1, 0, At, B0); PG8_MMA(1, 1, At, B1); PG8_BAR; PG8_SCHED;
;             PG8_LDB(B0, 1, 0); PG8_LDB(B1, 1, 1); PG8_SCHED; PG8_LDA(At, 1, 0); PG8_STAGE_A(PG8_SA(0, 1), 1, a2, last);
;             PG8_WAIT_V(8); PG8_WAIT_L(0); PG8_BAR; PG8_MMA(0, 0, At, B0); PG8_MMA(0, 1, At, B1); PG8_BAR; PG8_SCHED;
;             PG8_LDA(At, 1, 1); PG8_STAGE(PG8_SB(1, 0), b3, voffB); PG8_STAGE(PG8_SB(1, 1), b3 + hstep, voffB); PG8_STAGE_A(PG8_SA(1, 0), 0, a3, last);
	s_setprio 1
	s_waitcnt lgkmcnt(0)
	v_mfma_f32_16x16x32_bf16 v[78:81], v[42:45], v[182:185], v[78:81]
	v_mfma_f32_16x16x32_bf16 v[74:77], v[58:61], v[182:185], v[74:77]
	v_mfma_f32_16x16x32_bf16 v[54:57], v[42:45], v[190:193], v[54:57]
	v_mfma_f32_16x16x32_bf16 v[46:49], v[58:61], v[190:193], v[46:49]
	v_mfma_f32_16x16x32_bf16 v[30:33], v[42:45], v[208:211], v[30:33]
	v_mfma_f32_16x16x32_bf16 v[26:29], v[58:61], v[208:211], v[26:29]
	v_mfma_f32_16x16x32_bf16 v[14:17], v[42:45], v[216:219], v[14:17]
	v_mfma_f32_16x16x32_bf16 v[10:13], v[58:61], v[216:219], v[10:13]
	v_mfma_f32_16x16x32_bf16 v[78:81], v[50:53], v[186:189], v[78:81]
	v_mfma_f32_16x16x32_bf16 v[74:77], v[62:65], v[186:189], v[74:77]
	v_mfma_f32_16x16x32_bf16 v[54:57], v[50:53], v[194:197], v[54:57]
	v_mfma_f32_16x16x32_bf16 v[46:49], v[62:65], v[194:197], v[46:49]
	v_mfma_f32_16x16x32_bf16 v[30:33], v[50:53], v[212:215], v[30:33]
	v_mfma_f32_16x16x32_bf16 v[26:29], v[62:65], v[212:215], v[26:29]
	v_mfma_f32_16x16x32_bf16 v[14:17], v[50:53], v[220:223], v[14:17]
	v_mfma_f32_16x16x32_bf16 v[10:13], v[62:65], v[220:223], v[10:13]
	s_setprio 0
	s_setprio 1
	v_mfma_f32_16x16x32_bf16 v[38:41], v[160:163], v[190:193], v[38:41]
	v_mfma_f32_16x16x32_bf16 v[34:37], v[174:177], v[190:193], v[34:37]
	v_mfma_f32_16x16x32_bf16 v[22:25], v[160:163], v[208:211], v[22:25]
	v_mfma_f32_16x16x32_bf16 v[18:21], v[174:177], v[208:211], v[18:21]
	v_mfma_f32_16x16x32_bf16 v[6:9], v[160:163], v[216:219], v[6:9]
	v_mfma_f32_16x16x32_bf16 v[2:5], v[174:177], v[216:219], v[2:5]
	v_mfma_f32_16x16x32_bf16 v[42:45], v[160:163], v[182:185], v[70:73]
	v_mfma_f32_16x16x32_bf16 v[50:53], v[174:177], v[182:185], v[66:69]
	v_mfma_f32_16x16x32_bf16 v[38:41], v[170:173], v[194:197], v[38:41]
	v_mfma_f32_16x16x32_bf16 v[34:37], v[178:181], v[194:197], v[34:37]
	v_mfma_f32_16x16x32_bf16 v[22:25], v[170:173], v[212:215], v[22:25]
	v_mfma_f32_16x16x32_bf16 v[18:21], v[178:181], v[212:215], v[18:21]
	v_mfma_f32_16x16x32_bf16 v[6:9], v[170:173], v[220:223], v[6:9]
	v_mfma_f32_16x16x32_bf16 v[2:5], v[178:181], v[220:223], v[2:5]
	v_mfma_f32_16x16x32_bf16 v[42:45], v[170:173], v[186:189], v[42:45]
	v_mfma_f32_16x16x32_bf16 v[50:53], v[178:181], v[186:189], v[50:53]
	s_setprio 0
	s_barrier
	v_add_u32_e32 v70, s48, v167
	v_add_u32_e32 v178, s56, v167
	ds_read_b128 v[58:61], v70
	ds_read_b128 v[62:65], v70 offset:1024
	ds_read_b128 v[66:69], v70 offset:2048
	ds_read_b128 v[70:73], v70 offset:3072
	ds_read_b128 v[160:163], v178
	ds_read_b128 v[170:173], v178 offset:1024
	ds_read_b128 v[174:177], v178 offset:2048
	ds_read_b128 v[178:181], v178 offset:3072
	s_add_u32 s16, s22, 0xb0000
	s_addc_u32 s17, s23, 0
	s_mov_b32 m0, s44
	v_lshl_add_u64 v[228:229], s[16:17], 0, v[148:149]
	ds_read_b128 v[182:185], v169 offset:32768
	ds_read_b128 v[186:189], v169 offset:33792
	ds_read_b128 v[190:193], v169 offset:34816
	ds_read_b128 v[194:197], v169 offset:35840
	ds_read_b128 v[208:211], v169 offset:36864
	ds_read_b128 v[212:215], v169 offset:37888
	ds_read_b128 v[216:219], v169 offset:38912
	ds_read_b128 v[220:223], v169 offset:39936
	global_load_lds_dwordx4 v[228:229], off
	v_lshl_add_u64 v[228:229], s[16:17], 0, v[152:153]
	s_mov_b32 m0, s45
	s_nop 0
	global_load_lds_dwordx4 v[228:229], off
	s_nop 0
	s_waitcnt vmcnt(8)
	s_waitcnt lgkmcnt(0)
	s_barrier
	s_setprio 1
	s_waitcnt lgkmcnt(0)
	v_mfma_f32_16x16x32_bf16 v[144:147], v[58:61], v[182:185], v[144:147]
	v_mfma_f32_16x16x32_bf16 v[140:143], v[66:69], v[182:185], v[140:143]
	v_mfma_f32_16x16x32_bf16 v[128:131], v[58:61], v[190:193], v[128:131]
	v_mfma_f32_16x16x32_bf16 v[124:127], v[66:69], v[190:193], v[124:127]
	v_mfma_f32_16x16x32_bf16 v[112:115], v[58:61], v[208:211], v[112:115]
	v_mfma_f32_16x16x32_bf16 v[108:111], v[66:69], v[208:211], v[108:111]
	v_mfma_f32_16x16x32_bf16 v[94:97], v[58:61], v[216:219], v[94:97]
	v_mfma_f32_16x16x32_bf16 v[90:93], v[66:69], v[216:219], v[90:93]
	v_mfma_f32_16x16x32_bf16 v[144:147], v[62:65], v[186:189], v[144:147]
	v_mfma_f32_16x16x32_bf16 v[140:143], v[70:73], v[186:189], v[140:143]
	v_mfma_f32_16x16x32_bf16 v[128:131], v[62:65], v[194:197], v[128:131]
	v_mfma_f32_16x16x32_bf16 v[124:127], v[70:73], v[194:197], v[124:127]
	v_mfma_f32_16x16x32_bf16 v[112:115], v[62:65], v[212:215], v[112:115]
	v_mfma_f32_16x16x32_bf16 v[108:111], v[70:73], v[212:215], v[108:111]
	v_mfma_f32_16x16x32_bf16 v[94:97], v[62:65], v[220:223], v[94:97]
	v_mfma_f32_16x16x32_bf16 v[90:93], v[70:73], v[220:223], v[90:93]
	s_setprio 0
	s_setprio 1
	v_mfma_f32_16x16x32_bf16 v[136:139], v[160:163], v[182:185], v[136:139]
	v_mfma_f32_16x16x32_bf16 v[132:135], v[174:177], v[182:185], v[132:135]
	v_mfma_f32_16x16x32_bf16 v[120:123], v[160:163], v[190:193], v[120:123]
	v_mfma_f32_16x16x32_bf16 v[116:119], v[174:177], v[190:193], v[116:119]
	v_mfma_f32_16x16x32_bf16 v[104:107], v[160:163], v[208:211], v[104:107]
	v_mfma_f32_16x16x32_bf16 v[100:103], v[174:177], v[208:211], v[100:103]
	v_mfma_f32_16x16x32_bf16 v[86:89], v[160:163], v[216:219], v[86:89]
	v_mfma_f32_16x16x32_bf16 v[82:85], v[174:177], v[216:219], v[82:85]
	v_mfma_f32_16x16x32_bf16 v[136:139], v[170:173], v[186:189], v[136:139]
	v_mfma_f32_16x16x32_bf16 v[132:135], v[178:181], v[186:189], v[132:135]
	v_mfma_f32_16x16x32_bf16 v[120:123], v[170:173], v[194:197], v[120:123]
	v_mfma_f32_16x16x32_bf16 v[116:119], v[178:181], v[194:197], v[116:119]
	v_mfma_f32_16x16x32_bf16 v[104:107], v[170:173], v[212:215], v[104:107]
	v_mfma_f32_16x16x32_bf16 v[100:103], v[178:181], v[212:215], v[100:103]
	v_mfma_f32_16x16x32_bf16 v[86:89], v[170:173], v[220:223], v[86:89]
	v_mfma_f32_16x16x32_bf16 v[82:85], v[178:181], v[220:223], v[82:85]
	s_setprio 0
	s_barrier
; #define PG8_STAGE_A(bufoff, h, ptr, nsel) do { if constexpr (Sched::GATHER) { if (nsel) PG8_STAGE_X(bufoff, ptr, vAn[h], PG8_A_AUX); else PG8_STAGE_X(bufoff, ptr, vAc[h], PG8_A_AUX); } \
;         else PG8_STAGE_X(bufoff, (ptr) + (h) * hstep, voffA, PG8_A_AUX); } while (0)
; #define PG8_STAGE(bufoff, gbase, voff) PG8_STAGE_X(bufoff, gbase, voff, PG8_B_AUX)
; #define PG8_LDA(dst, b, h) do { _Pragma("unroll") for (int m = 0; m < 4; ++m) _Pragma("unroll") for (int k = 0; k < 2; ++k) dst[m][k] = *(const PG8_LAS bf16x8*)(lds + PG8_SA(b, h) + aoff + m * 2048 + k * 1024); } while (0)
; #define PG8_MMA(ai, bj, At, Bt) do { __builtin_amdgcn_s_setprio(1); _Pragma("unroll") for (int m = 0; m < 4; ++m) _Pragma("unroll") for (int n = 0; n < 2; ++n) _Pragma("unroll") for (int k = 0; k < 2; ++k) \
;         acc[ai][bj][m][n] = __builtin_amdgcn_mfma_f32_16x16x32_bf16(Bt[n][k], At[m][k], acc[ai][bj][m][n], 0, 0, 0); __builtin_amdgcn_s_setprio(0); } while (0)
; #define PG8_WAIT_V(n) asm volatile("s_waitcnt vmcnt(" #n ")" ::: "memory")
; #define PG8_WAIT_L(n) asm volatile("s_waitcnt lgkmcnt(" #n ")" ::: "memory")
; #define PG8_BAR __builtin_amdgcn_s_barrier()
; #define PG8_SCHED __builtin_amdgcn_sched_barrier(0)
; template <class Epi, class Sched, bool ALIGN_EPI = false, bool SP2 = false>
; __device__ __forceinline__ void gemm_phase(PG8_LAS unsigned char* lds, const Gemm g, const Sched& S, const Epi& E) {
;     ...
;             PG8_LDA(At, 1, 1); PG8_STAGE(PG8_SB(1, 0), b3, voffB); PG8_STAGE(PG8_SB(1, 1), b3 + hstep, voffB); PG8_STAGE_A(PG8_SA(1, 0), 0, a3, last);
;             PG8_WAIT_V(8); PG8_WAIT_L(0); PG8_BAR; PG8_MMA(1, 0, At, B0); PG8_MMA(1, 1, At, B1); PG8_BAR; PG8_SCHED;
	s_mov_b32 m0, s49
	v_lshl_add_u64 v[164:165], v[164:165], 0, s[54:55]
	s_add_u32 s16, s20, 0xb0080
	ds_read_b128 v[182:185], v169 offset:49152
	ds_read_b128 v[186:189], v169 offset:50176
	ds_read_b128 v[190:193], v169 offset:51200
	ds_read_b128 v[194:197], v169 offset:52224
	ds_read_b128 v[208:211], v169 offset:53248
	ds_read_b128 v[212:215], v169 offset:54272
	ds_read_b128 v[216:219], v169 offset:55296
	ds_read_b128 v[220:223], v169 offset:56320
	global_load_lds_dwordx4 v[164:165], off
	v_lshl_add_u64 v[164:165], v[198:199], 0, s[54:55]
	s_mov_b32 m0, s50
	s_addc_u32 s17, s21, 0
	global_load_lds_dwordx4 v[164:165], off
	v_lshl_add_u64 v[164:165], s[16:17], 0, v[150:151]
	s_mov_b32 m0, s57
	s_nop 0
	global_load_lds_dwordx4 v[164:165], off
	v_lshl_add_u64 v[164:165], s[16:17], 0, v[154:155]
	s_mov_b32 m0, s58
	s_nop 0
	global_load_lds_dwordx4 v[164:165], off
	v_lshl_add_u64 v[164:165], v[224:225], 0, s[54:55]
	s_mov_b32 m0, s51
	s_nop 0
	global_load_lds_dwordx4 v[164:165], off
	v_lshl_add_u64 v[164:165], v[226:227], 0, s[54:55]
	s_mov_b32 m0, s53
	s_nop 0
	global_load_lds_dwordx4 v[164:165], off
	s_waitcnt vmcnt(8)
	s_waitcnt lgkmcnt(0)
	s_barrier
	s_setprio 1
	s_waitcnt lgkmcnt(0)
	v_mfma_f32_16x16x32_bf16 v[78:81], v[58:61], v[182:185], v[78:81]
	v_mfma_f32_16x16x32_bf16 v[74:77], v[66:69], v[182:185], v[74:77]
	v_mfma_f32_16x16x32_bf16 v[54:57], v[58:61], v[190:193], v[54:57]
	v_mfma_f32_16x16x32_bf16 v[46:49], v[66:69], v[190:193], v[46:49]
	v_mfma_f32_16x16x32_bf16 v[30:33], v[58:61], v[208:211], v[30:33]
	v_mfma_f32_16x16x32_bf16 v[26:29], v[66:69], v[208:211], v[26:29]
	v_mfma_f32_16x16x32_bf16 v[14:17], v[58:61], v[216:219], v[14:17]
	v_mfma_f32_16x16x32_bf16 v[10:13], v[66:69], v[216:219], v[10:13]
	v_mfma_f32_16x16x32_bf16 v[78:81], v[62:65], v[186:189], v[78:81]
	v_mfma_f32_16x16x32_bf16 v[74:77], v[70:73], v[186:189], v[74:77]
	v_mfma_f32_16x16x32_bf16 v[54:57], v[62:65], v[194:197], v[54:57]
	v_mfma_f32_16x16x32_bf16 v[46:49], v[70:73], v[194:197], v[46:49]
	v_mfma_f32_16x16x32_bf16 v[30:33], v[62:65], v[212:215], v[30:33]
	v_mfma_f32_16x16x32_bf16 v[26:29], v[70:73], v[212:215], v[26:29]
	v_mfma_f32_16x16x32_bf16 v[14:17], v[62:65], v[220:223], v[14:17]
	v_mfma_f32_16x16x32_bf16 v[10:13], v[70:73], v[220:223], v[10:13]
	s_setprio 0
	s_setprio 1
	v_mfma_f32_16x16x32_bf16 v[42:45], v[160:163], v[182:185], v[42:45]
	v_mfma_f32_16x16x32_bf16 v[70:73], v[170:173], v[186:189], v[42:45]
	v_mfma_f32_16x16x32_bf16 v[42:45], v[174:177], v[182:185], v[50:53]
	v_mfma_f32_16x16x32_bf16 v[38:41], v[160:163], v[190:193], v[38:41]
	v_mfma_f32_16x16x32_bf16 v[34:37], v[174:177], v[190:193], v[34:37]
	v_mfma_f32_16x16x32_bf16 v[22:25], v[160:163], v[208:211], v[22:25]
	v_mfma_f32_16x16x32_bf16 v[18:21], v[174:177], v[208:211], v[18:21]
	v_mfma_f32_16x16x32_bf16 v[6:9], v[160:163], v[216:219], v[6:9]
	v_mfma_f32_16x16x32_bf16 v[2:5], v[174:177], v[216:219], v[2:5]
	v_mfma_f32_16x16x32_bf16 v[66:69], v[178:181], v[186:189], v[42:45]
	v_mfma_f32_16x16x32_bf16 v[38:41], v[170:173], v[194:197], v[38:41]
	v_mfma_f32_16x16x32_bf16 v[34:37], v[178:181], v[194:197], v[34:37]
	v_mfma_f32_16x16x32_bf16 v[22:25], v[170:173], v[212:215], v[22:25]
	v_mfma_f32_16x16x32_bf16 v[18:21], v[178:181], v[212:215], v[18:21]
	v_mfma_f32_16x16x32_bf16 v[6:9], v[170:173], v[220:223], v[6:9]
	v_mfma_f32_16x16x32_bf16 v[2:5], v[178:181], v[220:223], v[2:5]
	s_setprio 0
	s_barrier
	s_add_i32 s73, s73, 2
	s_add_u32 s64, s64, 0x100
	s_addc_u32 s72, s72, 0
	s_cmp_gt_u32 s73, 41
	s_mov_b64 s[16:17], s[18:19]
	s_cbranch_scc0 .LBB13_1538
	s_and_b64 vcc, exec, s[12:13]
	s_cbranch_vccz .LBB13_1541
	s_barrier

; #define PG8_LAS __attribute__((address_space(3)))
; #define PG8_STAGE_A(bufoff, h, ptr, nsel) do { if constexpr (Sched::GATHER) { if (nsel) PG8_STAGE_X(bufoff, ptr, vAn[h], PG8_A_AUX); else PG8_STAGE_X(bufoff, ptr, vAc[h], PG8_A_AUX); } \
;         else PG8_STAGE_X(bufoff, (ptr) + (h) * hstep, voffA, PG8_A_AUX); } while (0)
; #define PG8_STAGE(bufoff, gbase, voff) PG8_STAGE_X(bufoff, gbase, voff, PG8_B_AUX)
; #define PG8_LDA(dst, b, h) do { _Pragma("unroll") for (int m = 0; m < 4; ++m) _Pragma("unroll") for (int k = 0; k < 2; ++k) dst[m][k] = *(const PG8_LAS bf16x8*)(lds + PG8_SA(b, h) + aoff + m * 2048 + k * 1024); } while (0)
; #define PG8_LDB(dst, b, h) do { _Pragma("unroll") for (int n = 0; n < 2; ++n) _Pragma("unroll") for (int k = 0; k < 2; ++k) dst[n][k] = *(const PG8_LAS bf16x8*)(lds + PG8_SB(b, h) + boff + n * 2048 + k * 1024); } while (0)
; #define PG8_WAIT_V(n) asm volatile("s_waitcnt vmcnt(" #n ")" ::: "memory")
; #define PG8_WAIT_L(n) asm volatile("s_waitcnt lgkmcnt(" #n ")" ::: "memory")
; template <class Epi, class Sched, bool ALIGN_EPI = false, bool SP2 = false>
; __device__ __forceinline__ void gemm_phase(PG8_LAS unsigned char* lds, const Gemm g, const Sched& S, const Epi& E) {
;     ...
;         for (int t = 0; t < nt; t += 2) {
;             const bool last = (t == nt - 2);
;             const char* a1 = cA + (size_t)(t + 1) * kstep;
;             const char* a2 = last ? nA : cA + (size_t)(t + 2) * kstep; const char* b2 = last ? nB : cB + (size_t)(t + 2) * kstep;
;             const char* a3 = a2 + kstep; const char* b3 = b2 + kstep;
;             if (last && has_next) S.a_ready(nxt);
;             if constexpr (Sched::GATHER) { if (last) { const u32x4 pv_ = *(const PG8_LAS u32x4*)(lds + STAGE_BYTES + tid * 16); vAn[0][0] = pv_.x; vAn[0][1] = pv_.y; vAn[1][0] = pv_.z; vAn[1][1] = pv_.w; } }
;             if constexpr (SP2) {
;             PG8_LDB(B0, 0, 0); PG8_LDB(B1, 0, 1); PG8_SCHED; PG8_LDA(At, 0, 0); PG8_STAGE_A(PG8_SA(1, 1), 1, a1, false);
;             PG8_WAIT_V(8); PG8_WAIT_L(0); PG8_BAR; PG8_MMA(0, 0, At, B0); PG8_MMA(0, 1, At, B1); PG8_BAR; PG8_SCHED;
;             PG8_LDA(At, 0, 1); PG8_STAGE(PG8_SB(0, 0), b2, voffB); PG8_STAGE(PG8_SB(0, 1), b2 + hstep, voffB); PG8_STAGE_A(PG8_SA(0, 0), 0, a2, last);
;             PG8_WAIT_V(8); PG8_WAIT_L(0); PG8_BAR; PG8_MMA(1, 0, At, B0); PG8_MMA(1, 1, At, B1); PG8_BAR; PG8_SCHED;
.LBB13_1573:
	v_add_u32_e32 v160, s13, v145
	v_add_u32_e32 v176, s49, v145
	ds_read_b128 v[148:151], v160
	ds_read_b128 v[152:155], v160 offset:1024
	ds_read_b128 v[156:159], v160 offset:2048
	ds_read_b128 v[160:163], v160 offset:3072
	ds_read_b128 v[164:167], v176
	ds_read_b128 v[168:171], v176 offset:1024
	ds_read_b128 v[172:175], v176 offset:2048
	ds_read_b128 v[176:179], v176 offset:3072
	s_add_u32 s22, s20, 0x100
	s_addc_u32 s23, s21, 0
	s_cmp_eq_u32 s88, 52
	s_cselect_b32 s27, s7, s23
	s_cselect_b32 s26, s6, s22
	s_cselect_b32 s25, s19, s87
	s_cselect_b32 s24, s18, s17
	v_lshl_add_u64 v[220:221], s[20:21], 0, v[140:141]
	s_add_i32 m0, s52, 0xc000
	ds_read_b128 v[180:183], v147
	ds_read_b128 v[184:187], v147 offset:1024
	ds_read_b128 v[188:191], v147 offset:2048
	ds_read_b128 v[192:195], v147 offset:3072
	ds_read_b128 v[196:199], v147 offset:4096
	ds_read_b128 v[208:211], v147 offset:5120
	ds_read_b128 v[212:215], v147 offset:6144
	ds_read_b128 v[216:219], v147 offset:7168
	global_load_lds_dwordx4 v[220:221], off
	v_lshl_add_u64 v[220:221], s[20:21], 0, v[142:143]
	s_add_i32 m0, s52, 0xe000
	s_nop 0
	global_load_lds_dwordx4 v[220:221], off
	s_waitcnt vmcnt(8)
	s_waitcnt lgkmcnt(0)
	s_barrier
	s_setprio 1
	s_waitcnt lgkmcnt(0)
	v_mfma_f32_16x16x32_bf16 v[128:131], v[148:151], v[180:183], v[128:131]
	v_mfma_f32_16x16x32_bf16 v[124:127], v[156:159], v[180:183], v[124:127]
	v_mfma_f32_16x16x32_bf16 v[120:123], v[148:151], v[188:191], v[120:123]
	v_mfma_f32_16x16x32_bf16 v[116:119], v[156:159], v[188:191], v[116:119]
	v_mfma_f32_16x16x32_bf16 v[104:107], v[148:151], v[196:199], v[104:107]
	v_mfma_f32_16x16x32_bf16 v[100:103], v[156:159], v[196:199], v[100:103]
	v_mfma_f32_16x16x32_bf16 v[86:89], v[148:151], v[212:215], v[86:89]
	v_mfma_f32_16x16x32_bf16 v[82:85], v[156:159], v[212:215], v[82:85]
	v_mfma_f32_16x16x32_bf16 v[128:131], v[152:155], v[184:187], v[128:131]
	v_mfma_f32_16x16x32_bf16 v[124:127], v[160:163], v[184:187], v[124:127]
	v_mfma_f32_16x16x32_bf16 v[120:123], v[152:155], v[192:195], v[120:123]
	v_mfma_f32_16x16x32_bf16 v[116:119], v[160:163], v[192:195], v[116:119]
	v_mfma_f32_16x16x32_bf16 v[104:107], v[152:155], v[208:211], v[104:107]
	v_mfma_f32_16x16x32_bf16 v[100:103], v[160:163], v[208:211], v[100:103]
	v_mfma_f32_16x16x32_bf16 v[86:89], v[152:155], v[216:219], v[86:89]
	v_mfma_f32_16x16x32_bf16 v[82:85], v[160:163], v[216:219], v[82:85]
	s_setprio 0
	s_setprio 1
	v_mfma_f32_16x16x32_bf16 v[112:115], v[164:167], v[180:183], v[112:115]
	v_mfma_f32_16x16x32_bf16 v[108:111], v[172:175], v[180:183], v[108:111]
	v_mfma_f32_16x16x32_bf16 v[94:97], v[164:167], v[188:191], v[94:97]
	v_mfma_f32_16x16x32_bf16 v[90:93], v[172:175], v[188:191], v[90:93]
	v_mfma_f32_16x16x32_bf16 v[78:81], v[164:167], v[196:199], v[78:81]
	v_mfma_f32_16x16x32_bf16 v[74:77], v[172:175], v[196:199], v[74:77]
	v_mfma_f32_16x16x32_bf16 v[70:73], v[164:167], v[212:215], v[70:73]
	v_mfma_f32_16x16x32_bf16 v[66:69], v[172:175], v[212:215], v[66:69]
	v_mfma_f32_16x16x32_bf16 v[112:115], v[168:171], v[184:187], v[112:115]
	v_mfma_f32_16x16x32_bf16 v[108:111], v[176:179], v[184:187], v[108:111]
	v_mfma_f32_16x16x32_bf16 v[94:97], v[168:171], v[192:195], v[94:97]
	v_mfma_f32_16x16x32_bf16 v[90:93], v[176:179], v[192:195], v[90:93]
	v_mfma_f32_16x16x32_bf16 v[78:81], v[168:171], v[208:211], v[78:81]
	v_mfma_f32_16x16x32_bf16 v[74:77], v[176:179], v[208:211], v[74:77]
	v_mfma_f32_16x16x32_bf16 v[70:73], v[168:171], v[216:219], v[70:73]
	v_mfma_f32_16x16x32_bf16 v[66:69], v[176:179], v[216:219], v[66:69]
	s_setprio 0
	s_barrier
	s_mov_b32 m0, s47
	v_lshl_add_u64 v[220:221], s[24:25], 0, v[134:135]
	s_add_u32 s20, s24, 0xe0000
	ds_read_b128 v[180:183], v147 offset:16384
	ds_read_b128 v[184:187], v147 offset:17408
	ds_read_b128 v[188:191], v147 offset:18432
	ds_read_b128 v[192:195], v147 offset:19456
	ds_read_b128 v[196:199], v147 offset:20480
	ds_read_b128 v[208:211], v147 offset:21504
	ds_read_b128 v[212:215], v147 offset:22528
	ds_read_b128 v[216:219], v147 offset:23552
	global_load_lds_dwordx4 v[220:221], off
	v_lshl_add_u64 v[222:223], s[24:25], 0, v[138:139]
	s_mov_b32 m0, s48
	s_addc_u32 s21, s25, 0
	global_load_lds_dwordx4 v[222:223], off
	v_lshl_add_u64 v[224:225], s[20:21], 0, v[134:135]
	s_mov_b32 m0, s50
	v_lshl_add_u64 v[226:227], s[26:27], 0, v[136:137]
	global_load_lds_dwordx4 v[224:225], off
	v_lshl_add_u64 v[224:225], s[20:21], 0, v[138:139]
	s_mov_b32 m0, s51
	s_nop 0
	global_load_lds_dwordx4 v[224:225], off
	v_lshl_add_u64 v[224:225], s[26:27], 0, v[132:133]
	s_mov_b32 m0, s52
	s_nop 0
	global_load_lds_dwordx4 v[224:225], off
	s_mov_b32 m0, s53
	s_nop 0
	global_load_lds_dwordx4 v[226:227], off
	s_nop 0
	s_waitcnt vmcnt(8)
	s_waitcnt lgkmcnt(0)
	s_barrier
; #define PG8_STAGE_A(bufoff, h, ptr, nsel) do { if constexpr (Sched::GATHER) { if (nsel) PG8_STAGE_X(bufoff, ptr, vAn[h], PG8_A_AUX); else PG8_STAGE_X(bufoff, ptr, vAc[h], PG8_A_AUX); } \
;         else PG8_STAGE_X(bufoff, (ptr) + (h) * hstep, voffA, PG8_A_AUX); } while (0)
; #define PG8_STAGE(bufoff, gbase, voff) PG8_STAGE_X(bufoff, gbase, voff, PG8_B_AUX)
; #define PG8_LDA(dst, b, h) do { _Pragma("unroll") for (int m = 0; m < 4; ++m) _Pragma("unroll") for (int k = 0; k < 2; ++k) dst[m][k] = *(const PG8_LAS bf16x8*)(lds + PG8_SA(b, h) + aoff + m * 2048 + k * 1024); } while (0)
; #define PG8_LDB(dst, b, h) do { _Pragma("unroll") for (int n = 0; n < 2; ++n) _Pragma("unroll") for (int k = 0; k < 2; ++k) dst[n][k] = *(const PG8_LAS bf16x8*)(lds + PG8_SB(b, h) + boff + n * 2048 + k * 1024); } while (0)
; #define PG8_MMA(ai, bj, At, Bt) do { __builtin_amdgcn_s_setprio(1); _Pragma("unroll") for (int m = 0; m < 4; ++m) _Pragma("unroll") for (int n = 0; n < 2; ++n) _Pragma("unroll") for (int k = 0; k < 2; ++k) \
;         acc[ai][bj][m][n] = __builtin_amdgcn_mfma_f32_16x16x32_bf16(Bt[n][k], At[m][k], acc[ai][bj][m][n], 0, 0, 0); __builtin_amdgcn_s_setprio(0); } while (0)
; #define PG8_WAIT_V(n) asm volatile("s_waitcnt vmcnt(" #n ")" ::: "memory")
; #define PG8_WAIT_L(n) asm volatile("s_waitcnt lgkmcnt(" #n ")" ::: "memory")
; #define PG8_BAR __builtin_amdgcn_s_barrier()
; #define PG8_SCHED __builtin_amdgcn_sched_barrier(0)
; template <class Epi, class Sched, bool ALIGN_EPI = false, bool SP2 = false>
; __device__ __forceinline__ void gemm_phase(PG8_LAS unsigned char* lds, const Gemm g, const Sched& S, const Epi& E) {
;     ...
;             PG8_WAIT_V(8); PG8_WAIT_L(0); PG8_BAR; PG8_MMA(1, 0, At, B0); PG8_MMA(1, 1, At, B1); PG8_BAR; PG8_SCHED;
;             PG8_LDB(B0, 1, 0); PG8_LDB(B1, 1, 1); PG8_SCHED; PG8_LDA(At, 1, 0); PG8_STAGE_A(PG8_SA(0, 1), 1, a2, last);
;             PG8_WAIT_V(8); PG8_WAIT_L(0); PG8_BAR; PG8_MMA(0, 0, At, B0); PG8_MMA(0, 1, At, B1); PG8_BAR; PG8_SCHED;
;             PG8_LDA(At, 1, 1); PG8_STAGE(PG8_SB(1, 0), b3, voffB); PG8_STAGE(PG8_SB(1, 1), b3 + hstep, voffB); PG8_STAGE_A(PG8_SA(1, 0), 0, a3, last);
	s_setprio 1
	s_waitcnt lgkmcnt(0)
	v_mfma_f32_16x16x32_bf16 v[62:65], v[148:151], v[180:183], v[62:65]
	v_mfma_f32_16x16x32_bf16 v[58:61], v[156:159], v[180:183], v[58:61]
	v_mfma_f32_16x16x32_bf16 v[54:57], v[148:151], v[188:191], v[54:57]
	v_mfma_f32_16x16x32_bf16 v[50:53], v[156:159], v[188:191], v[50:53]
	v_mfma_f32_16x16x32_bf16 v[38:41], v[148:151], v[196:199], v[38:41]
	v_mfma_f32_16x16x32_bf16 v[34:37], v[156:159], v[196:199], v[34:37]
	v_mfma_f32_16x16x32_bf16 v[22:25], v[148:151], v[212:215], v[22:25]
	v_mfma_f32_16x16x32_bf16 v[18:21], v[156:159], v[212:215], v[18:21]
	v_mfma_f32_16x16x32_bf16 v[62:65], v[152:155], v[184:187], v[62:65]
	v_mfma_f32_16x16x32_bf16 v[58:61], v[160:163], v[184:187], v[58:61]
	v_mfma_f32_16x16x32_bf16 v[54:57], v[152:155], v[192:195], v[54:57]
	v_mfma_f32_16x16x32_bf16 v[50:53], v[160:163], v[192:195], v[50:53]
	v_mfma_f32_16x16x32_bf16 v[38:41], v[152:155], v[208:211], v[38:41]
	v_mfma_f32_16x16x32_bf16 v[34:37], v[160:163], v[208:211], v[34:37]
	v_mfma_f32_16x16x32_bf16 v[22:25], v[152:155], v[216:219], v[22:25]
	v_mfma_f32_16x16x32_bf16 v[18:21], v[160:163], v[216:219], v[18:21]
	s_setprio 0
	s_setprio 1
	v_mfma_f32_16x16x32_bf16 v[46:49], v[164:167], v[180:183], v[46:49]
	v_mfma_f32_16x16x32_bf16 v[42:45], v[172:175], v[180:183], v[42:45]
	v_mfma_f32_16x16x32_bf16 v[30:33], v[164:167], v[188:191], v[30:33]
	v_mfma_f32_16x16x32_bf16 v[26:29], v[172:175], v[188:191], v[26:29]
	v_mfma_f32_16x16x32_bf16 v[14:17], v[164:167], v[196:199], v[14:17]
	v_mfma_f32_16x16x32_bf16 v[10:13], v[172:175], v[196:199], v[10:13]
	v_mfma_f32_16x16x32_bf16 v[6:9], v[164:167], v[212:215], v[6:9]
	v_mfma_f32_16x16x32_bf16 v[2:5], v[172:175], v[212:215], v[2:5]
	v_mfma_f32_16x16x32_bf16 v[46:49], v[168:171], v[184:187], v[46:49]
	v_mfma_f32_16x16x32_bf16 v[42:45], v[176:179], v[184:187], v[42:45]
	v_mfma_f32_16x16x32_bf16 v[30:33], v[168:171], v[192:195], v[30:33]
	v_mfma_f32_16x16x32_bf16 v[26:29], v[176:179], v[192:195], v[26:29]
	v_mfma_f32_16x16x32_bf16 v[14:17], v[168:171], v[208:211], v[14:17]
	v_mfma_f32_16x16x32_bf16 v[10:13], v[176:179], v[208:211], v[10:13]
	v_mfma_f32_16x16x32_bf16 v[6:9], v[168:171], v[216:219], v[6:9]
	v_mfma_f32_16x16x32_bf16 v[2:5], v[176:179], v[216:219], v[2:5]
	s_setprio 0
	s_barrier
	v_add_u32_e32 v160, s58, v145
	v_add_u32_e32 v176, s69, v145
	ds_read_b128 v[148:151], v160
	ds_read_b128 v[152:155], v160 offset:1024
	ds_read_b128 v[156:159], v160 offset:2048
	ds_read_b128 v[160:163], v160 offset:3072
	ds_read_b128 v[164:167], v176
	ds_read_b128 v[168:171], v176 offset:1024
	ds_read_b128 v[172:175], v176 offset:2048
	ds_read_b128 v[176:179], v176 offset:3072
	s_add_u32 s20, s26, 0xe0000
	s_addc_u32 s21, s27, 0
	s_mov_b32 m0, s56
	v_lshl_add_u64 v[228:229], s[20:21], 0, v[132:133]
	ds_read_b128 v[180:183], v147 offset:32768
	ds_read_b128 v[184:187], v147 offset:33792
	ds_read_b128 v[188:191], v147 offset:34816
	ds_read_b128 v[192:195], v147 offset:35840
	ds_read_b128 v[196:199], v147 offset:36864
	ds_read_b128 v[208:211], v147 offset:37888
	ds_read_b128 v[212:215], v147 offset:38912
	ds_read_b128 v[216:219], v147 offset:39936
	global_load_lds_dwordx4 v[228:229], off
	v_lshl_add_u64 v[228:229], s[20:21], 0, v[136:137]
	s_mov_b32 m0, s57
	s_nop 0
	global_load_lds_dwordx4 v[228:229], off
	s_nop 0
	s_waitcnt vmcnt(8)
	s_waitcnt lgkmcnt(0)
	s_barrier
	s_setprio 1
	s_waitcnt lgkmcnt(0)
	v_mfma_f32_16x16x32_bf16 v[128:131], v[148:151], v[180:183], v[128:131]
	v_mfma_f32_16x16x32_bf16 v[124:127], v[156:159], v[180:183], v[124:127]
	v_mfma_f32_16x16x32_bf16 v[120:123], v[148:151], v[188:191], v[120:123]
	v_mfma_f32_16x16x32_bf16 v[116:119], v[156:159], v[188:191], v[116:119]
	v_mfma_f32_16x16x32_bf16 v[104:107], v[148:151], v[196:199], v[104:107]
	v_mfma_f32_16x16x32_bf16 v[100:103], v[156:159], v[196:199], v[100:103]
	v_mfma_f32_16x16x32_bf16 v[86:89], v[148:151], v[212:215], v[86:89]
	v_mfma_f32_16x16x32_bf16 v[82:85], v[156:159], v[212:215], v[82:85]
	v_mfma_f32_16x16x32_bf16 v[128:131], v[152:155], v[184:187], v[128:131]
	v_mfma_f32_16x16x32_bf16 v[124:127], v[160:163], v[184:187], v[124:127]
	v_mfma_f32_16x16x32_bf16 v[120:123], v[152:155], v[192:195], v[120:123]
	v_mfma_f32_16x16x32_bf16 v[116:119], v[160:163], v[192:195], v[116:119]
	v_mfma_f32_16x16x32_bf16 v[104:107], v[152:155], v[208:211], v[104:107]
	v_mfma_f32_16x16x32_bf16 v[100:103], v[160:163], v[208:211], v[100:103]
	v_mfma_f32_16x16x32_bf16 v[86:89], v[152:155], v[216:219], v[86:89]
	v_mfma_f32_16x16x32_bf16 v[82:85], v[160:163], v[216:219], v[82:85]
	s_setprio 0
	s_setprio 1
	v_mfma_f32_16x16x32_bf16 v[112:115], v[164:167], v[180:183], v[112:115]
	v_mfma_f32_16x16x32_bf16 v[108:111], v[172:175], v[180:183], v[108:111]
	v_mfma_f32_16x16x32_bf16 v[94:97], v[164:167], v[188:191], v[94:97]
	v_mfma_f32_16x16x32_bf16 v[90:93], v[172:175], v[188:191], v[90:93]
	v_mfma_f32_16x16x32_bf16 v[78:81], v[164:167], v[196:199], v[78:81]
	v_mfma_f32_16x16x32_bf16 v[74:77], v[172:175], v[196:199], v[74:77]
	v_mfma_f32_16x16x32_bf16 v[70:73], v[164:167], v[212:215], v[70:73]
	v_mfma_f32_16x16x32_bf16 v[66:69], v[172:175], v[212:215], v[66:69]
	v_mfma_f32_16x16x32_bf16 v[112:115], v[168:171], v[184:187], v[112:115]
	v_mfma_f32_16x16x32_bf16 v[108:111], v[176:179], v[184:187], v[108:111]
	v_mfma_f32_16x16x32_bf16 v[94:97], v[168:171], v[192:195], v[94:97]
	v_mfma_f32_16x16x32_bf16 v[90:93], v[176:179], v[192:195], v[90:93]
	v_mfma_f32_16x16x32_bf16 v[78:81], v[168:171], v[208:211], v[78:81]
	v_mfma_f32_16x16x32_bf16 v[74:77], v[176:179], v[208:211], v[74:77]
	v_mfma_f32_16x16x32_bf16 v[70:73], v[168:171], v[216:219], v[70:73]
	v_mfma_f32_16x16x32_bf16 v[66:69], v[176:179], v[216:219], v[66:69]
	s_setprio 0
	s_barrier
; #define PG8_STAGE_A(bufoff, h, ptr, nsel) do { if constexpr (Sched::GATHER) { if (nsel) PG8_STAGE_X(bufoff, ptr, vAn[h], PG8_A_AUX); else PG8_STAGE_X(bufoff, ptr, vAc[h], PG8_A_AUX); } \
;         else PG8_STAGE_X(bufoff, (ptr) + (h) * hstep, voffA, PG8_A_AUX); } while (0)
; #define PG8_STAGE(bufoff, gbase, voff) PG8_STAGE_X(bufoff, gbase, voff, PG8_B_AUX)
; #define PG8_LDA(dst, b, h) do { _Pragma("unroll") for (int m = 0; m < 4; ++m) _Pragma("unroll") for (int k = 0; k < 2; ++k) dst[m][k] = *(const PG8_LAS bf16x8*)(lds + PG8_SA(b, h) + aoff + m * 2048 + k * 1024); } while (0)
; #define PG8_MMA(ai, bj, At, Bt) do { __builtin_amdgcn_s_setprio(1); _Pragma("unroll") for (int m = 0; m < 4; ++m) _Pragma("unroll") for (int n = 0; n < 2; ++n) _Pragma("unroll") for (int k = 0; k < 2; ++k) \
;         acc[ai][bj][m][n] = __builtin_amdgcn_mfma_f32_16x16x32_bf16(Bt[n][k], At[m][k], acc[ai][bj][m][n], 0, 0, 0); __builtin_amdgcn_s_setprio(0); } while (0)
; #define PG8_WAIT_V(n) asm volatile("s_waitcnt vmcnt(" #n ")" ::: "memory")
; #define PG8_WAIT_L(n) asm volatile("s_waitcnt lgkmcnt(" #n ")" ::: "memory")
; #define PG8_BAR __builtin_amdgcn_s_barrier()
; #define PG8_SCHED __builtin_amdgcn_sched_barrier(0)
; template <class Epi, class Sched, bool ALIGN_EPI = false, bool SP2 = false>
; __device__ __forceinline__ void gemm_phase(PG8_LAS unsigned char* lds, const Gemm g, const Sched& S, const Epi& E) {
;     ...
;             PG8_LDA(At, 1, 1); PG8_STAGE(PG8_SB(1, 0), b3, voffB); PG8_STAGE(PG8_SB(1, 1), b3 + hstep, voffB); PG8_STAGE_A(PG8_SA(1, 0), 0, a3, last);
;             PG8_WAIT_V(8); PG8_WAIT_L(0); PG8_BAR; PG8_MMA(1, 0, At, B0); PG8_MMA(1, 1, At, B1); PG8_BAR; PG8_SCHED;
	s_mov_b32 m0, s59
	v_lshl_add_u64 v[220:221], v[220:221], 0, s[54:55]
	s_add_u32 s20, s24, 0xe0080
	ds_read_b128 v[180:183], v147 offset:49152
	ds_read_b128 v[184:187], v147 offset:50176
	ds_read_b128 v[188:191], v147 offset:51200
	ds_read_b128 v[192:195], v147 offset:52224
	ds_read_b128 v[196:199], v147 offset:53248
	ds_read_b128 v[208:211], v147 offset:54272
	ds_read_b128 v[212:215], v147 offset:55296
	ds_read_b128 v[216:219], v147 offset:56320
	global_load_lds_dwordx4 v[220:221], off
	v_lshl_add_u64 v[220:221], v[222:223], 0, s[54:55]
	s_mov_b32 m0, s61
	s_addc_u32 s21, s25, 0
	global_load_lds_dwordx4 v[220:221], off
	v_lshl_add_u64 v[220:221], s[20:21], 0, v[134:135]
	s_mov_b32 m0, s72
	s_nop 0
	global_load_lds_dwordx4 v[220:221], off
	v_lshl_add_u64 v[220:221], s[20:21], 0, v[138:139]
	s_mov_b32 m0, s73
	s_nop 0
	global_load_lds_dwordx4 v[220:221], off
	v_lshl_add_u64 v[220:221], v[224:225], 0, s[54:55]
	s_mov_b32 m0, s64
	s_nop 0
	global_load_lds_dwordx4 v[220:221], off
	v_lshl_add_u64 v[220:221], v[226:227], 0, s[54:55]
	s_mov_b32 m0, s68
	s_nop 0
	global_load_lds_dwordx4 v[220:221], off
	s_waitcnt vmcnt(8)
	s_waitcnt lgkmcnt(0)
	s_barrier
	s_setprio 1
	s_waitcnt lgkmcnt(0)
	v_mfma_f32_16x16x32_bf16 v[62:65], v[148:151], v[180:183], v[62:65]
	v_mfma_f32_16x16x32_bf16 v[58:61], v[156:159], v[180:183], v[58:61]
	v_mfma_f32_16x16x32_bf16 v[54:57], v[148:151], v[188:191], v[54:57]
	v_mfma_f32_16x16x32_bf16 v[50:53], v[156:159], v[188:191], v[50:53]
	v_mfma_f32_16x16x32_bf16 v[38:41], v[148:151], v[196:199], v[38:41]
	v_mfma_f32_16x16x32_bf16 v[34:37], v[156:159], v[196:199], v[34:37]
	v_mfma_f32_16x16x32_bf16 v[22:25], v[148:151], v[212:215], v[22:25]
	v_mfma_f32_16x16x32_bf16 v[18:21], v[156:159], v[212:215], v[18:21]
	v_mfma_f32_16x16x32_bf16 v[62:65], v[152:155], v[184:187], v[62:65]
	v_mfma_f32_16x16x32_bf16 v[58:61], v[160:163], v[184:187], v[58:61]
	v_mfma_f32_16x16x32_bf16 v[54:57], v[152:155], v[192:195], v[54:57]
	v_mfma_f32_16x16x32_bf16 v[50:53], v[160:163], v[192:195], v[50:53]
	v_mfma_f32_16x16x32_bf16 v[38:41], v[152:155], v[208:211], v[38:41]
	v_mfma_f32_16x16x32_bf16 v[34:37], v[160:163], v[208:211], v[34:37]
	v_mfma_f32_16x16x32_bf16 v[22:25], v[152:155], v[216:219], v[22:25]
	v_mfma_f32_16x16x32_bf16 v[18:21], v[160:163], v[216:219], v[18:21]
	s_setprio 0
	s_setprio 1
	v_mfma_f32_16x16x32_bf16 v[46:49], v[164:167], v[180:183], v[46:49]
	v_mfma_f32_16x16x32_bf16 v[42:45], v[172:175], v[180:183], v[42:45]
	v_mfma_f32_16x16x32_bf16 v[30:33], v[164:167], v[188:191], v[30:33]
	v_mfma_f32_16x16x32_bf16 v[26:29], v[172:175], v[188:191], v[26:29]
	v_mfma_f32_16x16x32_bf16 v[14:17], v[164:167], v[196:199], v[14:17]
	v_mfma_f32_16x16x32_bf16 v[10:13], v[172:175], v[196:199], v[10:13]
	v_mfma_f32_16x16x32_bf16 v[6:9], v[164:167], v[212:215], v[6:9]
	v_mfma_f32_16x16x32_bf16 v[2:5], v[172:175], v[212:215], v[2:5]
	v_mfma_f32_16x16x32_bf16 v[46:49], v[168:171], v[184:187], v[46:49]
	v_mfma_f32_16x16x32_bf16 v[42:45], v[176:179], v[184:187], v[42:45]
	v_mfma_f32_16x16x32_bf16 v[30:33], v[168:171], v[192:195], v[30:33]
	v_mfma_f32_16x16x32_bf16 v[26:29], v[176:179], v[192:195], v[26:29]
	v_mfma_f32_16x16x32_bf16 v[14:17], v[168:171], v[208:211], v[14:17]
	v_mfma_f32_16x16x32_bf16 v[10:13], v[176:179], v[208:211], v[10:13]
	v_mfma_f32_16x16x32_bf16 v[6:9], v[168:171], v[216:219], v[6:9]
	v_mfma_f32_16x16x32_bf16 v[2:5], v[176:179], v[216:219], v[2:5]
	s_setprio 0
	s_barrier
	s_add_i32 s88, s88, 2
	s_add_u32 s17, s17, 0x100
	s_addc_u32 s87, s87, 0
	s_cmp_gt_u32 s88, 53
	s_mov_b64 s[20:21], s[22:23]
	s_cbranch_scc0 .LBB13_1573
	s_and_b64 vcc, exec, s[14:15]
	s_cbranch_vccz .LBB13_1576
	s_barrier
